# hybrid: scan WGs' producer waves compute packs of chunks [0,160) into the LDS ring, the 192 conversion WGs compute packs of chunks [160,256) to d_ws before converting, same waves then stream them via
# speedup vs baseline: 1.0379x; 1.0206x over previous
; #define LAS __attribute__((address_space(3)))
; __global__ void __launch_bounds__(NTHR, 2) mk_fwd(Args args) {
;     ...
;         const int tr = lane & 15, q = lane >> 4;
;         for (int arep_ = 0; arep_ < P5A_REPS; ++arep_) {
;                 const int j = lane;
;                 LAS bf16* IMG = (LAS bf16*)(lds + wave * 13312);
;                 LAS bf16* QGT = (LAS bf16*)(lds + wave * 13312 + 10240);
;                 for (int i = lane; i < 768; i += 64) ((LAS unsigned*)QGT)[i] = 0u;
;                 const int pos = (j & 32) | ((j & 12) << 1) | ((j & 16) >> 2) | (j & 3);
;                 bf16 nr_[17], nk_[17], nv_[17], nwl_[16], nal_[16]; float ncst_[7];
;     ...
;                 if (gw < 64 * NCHUNK) P4_FETCH(gw);
.LBB0_472:
	s_cmp_lt_i32 s88, 5
	s_cselect_b64 s[0:1], -1, 0
	s_and_b64 s[2:3], s[0:1], s[2:3]
	s_andn2_b64 vcc, exec, s[2:3]
	s_cbranch_vccnz .LBB0_481
	s_cmp_lt_i32 s18, 64
	s_cbranch_scc1 .LBB0_481
	v_writelane_b32 v252, s28, 54
	v_writelane_b32 v252, s30, 55
	v_readlane_b32 s0, v252, 38
	s_nop 3
	s_mul_i32 s0, s0, 24
	v_readlane_b32 s1, v252, 39
	s_nop 3
	s_add_i32 s0, s0, s1
	s_lshl_b32 s0, s0, 3
	v_readlane_b32 s1, v252, 43
	s_nop 3
	s_add_i32 s0, s1, s0
	s_sub_i32 s1, s0, 64
	s_and_b32 s0, s1, 63
	s_lshr_b32 s1, s1, 6
	s_add_i32 s1, s1, 160
	s_lshl_b32 s1, s1, 4
	s_lshr_b32 s30, s0, 4
	s_lshl_b32 s30, s30, 12
	s_add_i32 s101, s30, 0x1000
	s_and_b32 s0, s0, 15
	s_or_b32 s30, s30, s0
	s_or_b32 s30, s30, s1
	s_movk_i32 s28, 0x180
	v_readlane_b32 s0, v252, 43
	s_mulk_i32 s0, 0x3400
	s_add_i32 s4, s0, 0
	s_mov_b32 s77, 0
	s_cmpk_gt_i32 s30, 0x3fff
	v_lshl_add_u32 v125, v194, 2, s4
	v_mov_b32_e32 v7, 0
	ds_write2st64_b32 v125, v7, v7 offset0:40 offset1:41
	ds_write2st64_b32 v125, v7, v7 offset0:42 offset1:43
	ds_write2st64_b32 v125, v7, v7 offset0:44 offset1:45
	ds_write2st64_b32 v125, v7, v7 offset0:46 offset1:47
	ds_write2st64_b32 v125, v7, v7 offset0:48 offset1:49
	ds_write2st64_b32 v125, v7, v7 offset0:50 offset1:51
	s_cbranch_scc1 .LBB0_481
	v_writelane_b32 v252, s2, 52
	s_ashr_i32 s0, s30, 12
	s_lshl_b32 s5, s30, 6
	v_writelane_b32 v252, s3, 53
	s_bfe_u32 s2, s30, 0x80004
	s_ashr_i32 s1, s0, 31
	s_lshl_b32 s3, s2, 4
	s_and_b32 s5, s5, 0x3c0
	s_add_u32 s29, s26, 0x21c08000
	s_addc_u32 s31, s27, 0
	s_lshl_b32 s8, s5, 1
	s_add_u32 s6, s66, s8
	s_addc_u32 s7, s67, 0
	s_add_u32 s8, s10, s8
	s_addc_u32 s9, s11, 0
	s_lshl_b64 s[12:13], s[0:1], 12
	v_lshlrev_b32_e32 v1, 1, v0
	v_lshrrev_b32_e32 v2, 2, v0
	s_or_b32 s0, s12, s3
	v_and_b32_e32 v92, 15, v0
	v_and_b32_e32 v1, 24, v1
	v_and_b32_e32 v2, 4, v2
	v_and_b32_e32 v4, 3, v0
	v_and_b32_e32 v3, 35, v0
	s_add_u32 s1, s0, -1
	v_lshlrev_b32_e32 v5, 3, v0
	v_or3_b32 v101, v3, v2, v1
	s_addc_u32 s14, s13, -1
	v_and_b32_e32 v97, 56, v5
	v_mul_u32_u24_e32 v5, 0x48, v92
	v_lshlrev_b32_e32 v1, 1, v1
	v_lshlrev_b32_e32 v4, 1, v4
	s_cmp_eq_u32 s2, 0
	v_lshlrev_b32_e32 v5, 1, v5
	v_add3_u32 v1, s4, v1, v4
	v_lshlrev_b32_e32 v18, 1, v194
	v_mov_b32_e32 v19, v7
	v_and_b32_e32 v4, 48, v194
	v_lshl_add_u64 v[14:15], s[10:11], 0, v[18:19]
	v_lshl_add_u64 v[16:17], s[66:67], 0, v[18:19]
	v_add3_u32 v98, s4, v5, v4
	v_lshl_add_u64 v[4:5], s[6:7], 0, v[18:19]
	v_lshl_add_u64 v[18:19], s[8:9], 0, v[18:19]
	s_cselect_b32 s1, s12, s1
	s_cselect_b32 s6, s13, s14
	v_mov_b32_e32 v99, 0x2400
	s_mul_i32 s8, s6, 0x2400
	v_mad_u64_u32 v[22:23], s[6:7], s1, v99, v[18:19]
	v_add_u32_e32 v23, s8, v23
	s_movk_i32 s36, 0x1000
	global_load_ushort v24, v[22:23], off
	global_load_ushort v21, v[22:23], off offset:2048
	v_add_co_u32_e32 v22, vcc, s36, v22
	v_mad_i64_i32 v[18:19], s[6:7], s0, v99, v[18:19]
	s_nop 0
	v_addc_co_u32_e32 v23, vcc, 0, v23, vcc
	v_add_co_u32_e32 v26, vcc, s36, v18
	s_movk_i32 s37, 0x2000
	s_nop 0
	v_addc_co_u32_e32 v27, vcc, 0, v19, vcc
	global_load_ushort v20, v[22:23], off
	global_load_ushort v25, v[18:19], off
	s_nop 0
	global_load_ushort v22, v[18:19], off offset:2048
	global_load_ushort v23, v[26:27], off
	s_mov_b64 s[6:7], 0x2400
	v_add_co_u32_e32 v26, vcc, s37, v18
	v_lshl_add_u64 v[28:29], v[18:19], 0, s[6:7]
	s_nop 0
	v_addc_co_u32_e32 v27, vcc, 0, v19, vcc
	s_movk_i32 s38, 0x3000
	global_load_ushort v27, v[26:27], off offset:1024
	s_nop 0
	global_load_ushort v26, v[28:29], off offset:2048
	v_add_co_u32_e32 v28, vcc, s38, v18
	s_movk_i32 s8, 0x4000
	s_nop 0
	v_addc_co_u32_e32 v29, vcc, 0, v19, vcc
	global_load_ushort v96, v[28:29], off offset:1024
	v_add_co_u32_e32 v28, vcc, s8, v18
	s_movk_i32 s1, 0x5000
	s_nop 0
	v_addc_co_u32_e32 v29, vcc, 0, v19, vcc
	s_mov_b64 s[6:7], 0x4800
	v_add_co_u32_e32 v32, vcc, s1, v18
	v_lshl_add_u64 v[30:31], v[18:19], 0, s[6:7]
	s_nop 0
	v_addc_co_u32_e32 v33, vcc, 0, v19, vcc
	s_movk_i32 s9, 0x6000
	global_load_ushort v29, v[28:29], off offset:2048
	s_nop 0
	global_load_ushort v30, v[30:31], off offset:2048
	s_mov_b64 s[10:11], 0x6c00
	global_load_ushort v121, v[32:33], off offset:2048
	v_add_co_u32_e32 v32, vcc, s9, v18
	v_lshl_add_u64 v[34:35], v[18:19], 0, s[10:11]
	s_nop 0
	v_addc_co_u32_e32 v33, vcc, 0, v19, vcc
	s_movk_i32 s42, 0x7000
	global_load_ushort v32, v[32:33], off offset:3072
	s_nop 0
	global_load_ushort v31, v[34:35], off offset:2048
	v_add_co_u32_e32 v34, vcc, s42, v18
	s_mov_b32 s44, 0xa000
	s_nop 0
	v_addc_co_u32_e32 v35, vcc, 0, v19, vcc
	s_mov_b64 s[10:11], 0x9000
	v_add_co_u32_e32 v36, vcc, s44, v18
	global_load_ushort v122, v[34:35], off offset:3072
	v_lshl_add_u64 v[34:35], v[18:19], 0, s[10:11]
	v_addc_co_u32_e32 v37, vcc, 0, v19, vcc
	s_mov_b32 s1, 0xb000
	global_load_ushort v33, v[36:37], off offset:-4096
	s_nop 0
	global_load_ushort v34, v[34:35], off offset:2048
	s_nop 0
	global_load_ushort v123, v[36:37], off
	s_mov_b64 s[14:15], 0xb400
	v_add_co_u32_e32 v36, vcc, s1, v18
	v_lshl_add_u64 v[38:39], v[18:19], 0, s[14:15]
	s_nop 0
	v_addc_co_u32_e32 v37, vcc, 0, v19, vcc
	s_mov_b32 s39, 0xc000
	global_load_ushort v36, v[36:37], off offset:1024
	s_nop 0
	global_load_ushort v35, v[38:39], off offset:2048
	v_add_co_u32_e32 v38, vcc, s39, v18
	s_mov_b32 s41, 0xd000
	s_nop 0
	v_addc_co_u32_e32 v39, vcc, 0, v19, vcc
	global_load_ushort v124, v[38:39], off offset:1024
	s_mov_b64 s[14:15], 0xd800
	v_add_co_u32_e32 v38, vcc, s41, v18
	v_lshl_add_u64 v[40:41], v[18:19], 0, s[14:15]
	s_nop 0
	v_addc_co_u32_e32 v39, vcc, 0, v19, vcc
	s_mov_b32 s1, 0xe000
	global_load_ushort v38, v[38:39], off offset:2048
	s_nop 0
	global_load_ushort v37, v[40:41], off offset:2048
	v_add_co_u32_e32 v40, vcc, s1, v18
	s_mov_b32 s49, 0xf000
	s_nop 0
	v_addc_co_u32_e32 v41, vcc, 0, v19, vcc
	s_mov_b64 s[16:17], 0xfc00
	v_add_co_u32_e32 v42, vcc, s49, v18
	global_load_ushort v127, v[40:41], off offset:2048
	v_lshl_add_u64 v[40:41], v[18:19], 0, s[16:17]
	v_addc_co_u32_e32 v43, vcc, 0, v19, vcc
	s_mov_b32 s50, 0x10000
	global_load_ushort v43, v[42:43], off offset:3072
	s_nop 0
	global_load_ushort v39, v[40:41], off offset:2048
	v_add_co_u32_e32 v40, vcc, s50, v18
	s_mov_b32 s73, 0x13000
	s_nop 0
	v_addc_co_u32_e32 v41, vcc, 0, v19, vcc
	s_mov_b64 s[46:47], 0x12000
	v_add_co_u32_e32 v46, vcc, s73, v18
	global_load_ushort v128, v[40:41], off offset:3072
	v_lshl_add_u64 v[40:41], v[18:19], 0, s[46:47]
	v_addc_co_u32_e32 v47, vcc, 0, v19, vcc
	s_mov_b32 s1, 0x14000
	global_load_ushort v45, v[46:47], off offset:-4096
	global_load_ushort v44, v[40:41], off offset:2048
	s_nop 0
	global_load_ushort v41, v[46:47], off
	s_mov_b64 s[16:17], 0x14400
	v_add_co_u32_e32 v46, vcc, s1, v18
	v_lshl_add_u64 v[48:49], v[18:19], 0, s[16:17]
	s_nop 0
	v_addc_co_u32_e32 v47, vcc, 0, v19, vcc
	s_mov_b32 s78, 0x15000
	global_load_ushort v47, v[46:47], off offset:1024
	s_nop 0
	global_load_ushort v46, v[48:49], off offset:2048
	v_add_co_u32_e32 v48, vcc, s78, v18
	s_mov_b32 s72, 0x16000
	s_nop 0
	v_addc_co_u32_e32 v49, vcc, 0, v19, vcc
	global_load_ushort v129, v[48:49], off offset:1024
	s_mov_b64 s[16:17], 0x16800
	v_add_co_u32_e32 v48, vcc, s72, v18
	v_lshl_add_u64 v[50:51], v[18:19], 0, s[16:17]
	s_nop 0
	v_addc_co_u32_e32 v49, vcc, 0, v19, vcc
	s_mov_b32 s1, 0x17000
	global_load_ushort v49, v[48:49], off offset:2048
	s_nop 0
	global_load_ushort v48, v[50:51], off offset:2048
	v_add_co_u32_e32 v50, vcc, s1, v18
	s_mov_b32 s1, 0x18000
	s_nop 0
	v_addc_co_u32_e32 v51, vcc, 0, v19, vcc
	global_load_ushort v130, v[50:51], off offset:2048
	s_mov_b64 s[34:35], 0x18c00
	v_add_co_u32_e32 v50, vcc, s1, v18
	v_lshl_add_u64 v[52:53], v[18:19], 0, s[34:35]
	s_nop 0
	v_addc_co_u32_e32 v51, vcc, 0, v19, vcc
	s_mov_b32 s1, 0x19000
	global_load_ushort v51, v[50:51], off offset:3072
	s_nop 0
	global_load_ushort v50, v[52:53], off offset:2048
	v_add_co_u32_e32 v52, vcc, s1, v18
	s_mov_b32 s1, 0x1c000
	s_nop 0
	v_addc_co_u32_e32 v53, vcc, 0, v19, vcc
	s_mov_b64 s[34:35], 0x1b000
	v_add_co_u32_e32 v56, vcc, s1, v18
	v_lshl_add_u64 v[54:55], v[18:19], 0, s[34:35]
	s_nop 0
	v_addc_co_u32_e32 v57, vcc, 0, v19, vcc
	s_mov_b32 s1, 0x1d000
	global_load_ushort v133, v[52:53], off offset:3072
	s_nop 0
	global_load_ushort v53, v[56:57], off offset:-4096
	global_load_ushort v52, v[54:55], off offset:2048
	global_load_ushort v134, v[56:57], off
	s_mov_b64 s[34:35], 0x1d400
	v_add_co_u32_e32 v54, vcc, s1, v18
	v_lshl_add_u64 v[56:57], v[18:19], 0, s[34:35]
	s_nop 0
	v_addc_co_u32_e32 v55, vcc, 0, v19, vcc
	s_mov_b32 s1, 0x1e000
	global_load_ushort v55, v[54:55], off offset:1024
	s_nop 0
	global_load_ushort v54, v[56:57], off offset:2048
	v_add_co_u32_e32 v56, vcc, s1, v18
	s_mov_b32 s1, 0x1f000
	s_nop 0
	v_addc_co_u32_e32 v57, vcc, 0, v19, vcc
	v_add_co_u32_e32 v58, vcc, s1, v18
	s_mov_b32 s1, 0x20000
	s_nop 0
	v_addc_co_u32_e32 v59, vcc, 0, v19, vcc
	v_add_co_u32_e32 v60, vcc, s1, v18
	s_mov_b32 s1, 0x21000
	s_nop 0
	v_addc_co_u32_e32 v61, vcc, 0, v19, vcc
	s_mov_b64 s[34:35], 0x1f800
	v_add_co_u32_e32 v62, vcc, s1, v18
	global_load_ushort v135, v[56:57], off offset:1024
	v_lshl_add_u64 v[56:57], v[18:19], 0, s[34:35]
	s_mov_b64 s[34:35], 0x21c00
	v_addc_co_u32_e32 v63, vcc, 0, v19, vcc
	s_mov_b32 s1, 0x22000
	global_load_ushort v59, v[58:59], off offset:2048
	s_nop 0
	global_load_ushort v56, v[56:57], off offset:2048
	v_mov_b32_e32 v100, 0x1800
	global_load_ushort v136, v[60:61], off offset:2048
	v_lshl_add_u64 v[60:61], v[18:19], 0, s[34:35]
	v_add_co_u32_e32 v18, vcc, s1, v18
	v_mad_i64_i32 v[4:5], s[0:1], s0, v100, v[4:5]
	s_nop 0
	v_addc_co_u32_e32 v19, vcc, 0, v19, vcc
	global_load_ushort v64, v[62:63], off offset:3072
	s_nop 0
	global_load_ushort v61, v[60:61], off offset:2048
	v_add_co_u32_e32 v62, vcc, s36, v4
	s_mov_b64 s[0:1], 0x1800
	s_nop 0
	v_addc_co_u32_e32 v63, vcc, 0, v5, vcc
	v_add_co_u32_e32 v66, vcc, s38, v4
	global_load_ushort v137, v[18:19], off offset:3072
	v_lshl_add_u64 v[18:19], v[4:5], 0, s[0:1]
	s_mov_b64 s[0:1], 0x3000
	v_addc_co_u32_e32 v67, vcc, 0, v5, vcc
	global_load_ushort v58, v[4:5], off
	global_load_ushort v57, v[4:5], off offset:2048
	s_nop 0
	global_load_ushort v62, v[62:63], off offset:2048
	s_nop 0
	global_load_ushort v60, v[18:19], off offset:2048
	v_lshl_add_u64 v[18:19], v[4:5], 0, s[0:1]
	global_load_ushort v65, v[66:67], off
	global_load_ushort v63, v[18:19], off offset:2048
	v_add_co_u32_e32 v66, vcc, s8, v4
	s_mov_b32 s12, 0x9000
	s_nop 0
	v_addc_co_u32_e32 v67, vcc, 0, v5, vcc
	v_add_co_u32_e32 v68, vcc, s9, v4
	v_lshl_add_u64 v[18:19], v[4:5], 0, s[6:7]
	s_nop 0
	v_addc_co_u32_e32 v69, vcc, 0, v5, vcc
	v_add_co_u32_e32 v70, vcc, s42, v4
	s_mov_b64 s[0:1], 0x6000
	s_nop 0
	v_addc_co_u32_e32 v71, vcc, 0, v5, vcc
	v_add_co_u32_e32 v72, vcc, s12, v4
	global_load_ushort v67, v[66:67], off offset:2048
	s_nop 0
	global_load_ushort v66, v[18:19], off offset:2048
	v_addc_co_u32_e32 v73, vcc, 0, v5, vcc
	v_add_co_u32_e32 v74, vcc, s44, v4
	v_lshl_add_u64 v[18:19], v[4:5], 0, s[0:1]
	s_nop 0
	v_addc_co_u32_e32 v75, vcc, 0, v5, vcc
	v_add_co_u32_e32 v76, vcc, s39, v4
	s_mov_b64 s[0:1], 0x7800
	s_nop 0
	v_addc_co_u32_e32 v77, vcc, 0, v5, vcc
	v_add_co_u32_e32 v78, vcc, s41, v4
	global_load_ushort v69, v[68:69], off
	s_nop 0
	global_load_ushort v68, v[18:19], off offset:2048
	v_addc_co_u32_e32 v79, vcc, 0, v5, vcc
; __device__ __forceinline__ unsigned f2bf(float f) { return cvt_pk_bf16_nat(f, 0.f) & 0xffffu; }
; __global__ void __launch_bounds__(NTHR, 2) mk_fwd(Args args) {
;     ...
;                 const int pos = (j & 32) | ((j & 12) << 1) | ((j & 16) >> 2) | (j & 3);
;                 bf16 nr_[17], nk_[17], nv_[17], nwl_[16], nal_[16]; float ncst_[7];
;     ...
;                     const int s_ = tr, rec = (s_ >> 2) * 8 + (s_ & 3);
; #pragma unroll
;                     for (int e = 0; e < 4; ++e) { const int t = 4 * q + e;
;                         const float qv = s_ < t ? QT[e] : 0.f, gb = s_ <= t ? GB[e] : 0.f, gk = s_ <= t ? GK[e] : 0.f;
;                         QGT[t * 32 + rec] = (bf16)f2bf(qv);
;                         QGT[512 + t * 32 + rec] = (bf16)f2bf(gb); QGT[512 + t * 32 + rec + 4] = (bf16)f2bf(gk); }
;                     float Tr[16]; const pg8::v4i_t PTi = __builtin_bit_cast(pg8::v4i_t, PT);
; #pragma unroll
;                     for (int t = 0; t < 16; ++t) { float acc = (t == s_) ? 1.f : 0.f;
	v_lshl_add_u64 v[18:19], v[4:5], 0, s[0:1]
	v_add_co_u32_e32 v80, vcc, s49, v4
	global_load_ushort v71, v[70:71], off offset:2048
	s_nop 0
	global_load_ushort v70, v[18:19], off offset:2048
	v_lshl_add_u64 v[18:19], v[4:5], 0, s[10:11]
	s_mov_b64 s[0:1], 0xa800
	v_addc_co_u32_e32 v81, vcc, 0, v5, vcc
	global_load_ushort v73, v[72:73], off
	s_nop 0
	global_load_ushort v72, v[18:19], off offset:2048
	v_lshl_add_u64 v[18:19], v[4:5], 0, s[0:1]
	s_mov_b64 s[0:1], 0xc000
	v_add_co_u32_e32 v82, vcc, s50, v4
	s_mov_b32 s13, 0x12000
	global_load_ushort v75, v[74:75], off offset:2048
	s_nop 0
	global_load_ushort v74, v[18:19], off offset:2048
	v_lshl_add_u64 v[18:19], v[4:5], 0, s[0:1]
	v_addc_co_u32_e32 v83, vcc, 0, v5, vcc
	global_load_ushort v77, v[76:77], off
	s_nop 0
	global_load_ushort v76, v[18:19], off offset:2048
	v_lshl_add_u64 v[18:19], v[4:5], 0, s[14:15]
	s_mov_b64 s[0:1], 0xf000
	v_add_co_u32_e32 v84, vcc, s13, v4
	global_load_ushort v79, v[78:79], off offset:2048
	s_nop 0
	global_load_ushort v78, v[18:19], off offset:2048
	v_lshl_add_u64 v[18:19], v[4:5], 0, s[0:1]
	s_mov_b64 s[0:1], 0x10800
	v_addc_co_u32_e32 v85, vcc, 0, v5, vcc
	global_load_ushort v81, v[80:81], off
	s_nop 0
	global_load_ushort v80, v[18:19], off offset:2048
	v_lshl_add_u64 v[18:19], v[4:5], 0, s[0:1]
	v_add_co_u32_e32 v86, vcc, s73, v4
	global_load_ushort v83, v[82:83], off offset:2048
	s_nop 0
	global_load_ushort v82, v[18:19], off offset:2048
	v_lshl_add_u64 v[18:19], v[4:5], 0, s[46:47]
	s_mov_b64 s[0:1], 0x13800
	v_addc_co_u32_e32 v87, vcc, 0, v5, vcc
	global_load_ushort v85, v[84:85], off
	s_nop 0
	global_load_ushort v84, v[18:19], off offset:2048
	v_lshl_add_u64 v[18:19], v[4:5], 0, s[0:1]
	s_mov_b64 s[0:1], 0x15000
	v_add_co_u32_e32 v88, vcc, s78, v4
	v_or_b32_e32 v2, s5, v194
	v_readlane_b32 s80, v252, 0
	global_load_ushort v87, v[86:87], off offset:2048
	s_nop 0
	global_load_ushort v86, v[18:19], off offset:2048
	v_lshl_add_u64 v[18:19], v[4:5], 0, s[0:1]
	v_addc_co_u32_e32 v89, vcc, 0, v5, vcc
	v_lshlrev_b32_e32 v6, 2, v2
	v_readlane_b32 s84, v252, 4
	v_readlane_b32 s85, v252, 5
	global_load_ushort v89, v[88:89], off
	s_nop 0
	global_load_ushort v88, v[18:19], off offset:2048
	v_lshl_add_u64 v[18:19], v[4:5], 0, s[16:17]
	v_add_co_u32_e32 v4, vcc, s72, v4
	v_lshl_add_u64 v[2:3], s[84:85], 0, v[6:7]
	s_nop 0
	v_addc_co_u32_e32 v5, vcc, 0, v5, vcc
	v_add_co_u32_e32 v2, vcc, s37, v2
	v_readlane_b32 s86, v252, 6
	s_nop 0
	v_addc_co_u32_e32 v3, vcc, 0, v3, vcc
	v_readlane_b32 s87, v252, 7
	v_readlane_b32 s90, v252, 10
	v_readlane_b32 s91, v252, 11
	global_load_ushort v91, v[4:5], off offset:2048
	global_load_ushort v90, v[18:19], off offset:2048
	global_load_dword v40, v6, s[84:85]
	global_load_dword v42, v[2:3], off offset:-4096
	s_nop 0
	global_load_dword v2, v[2:3], off
	s_nop 0
	global_load_dword v95, v6, s[86:87]
	global_load_dword v94, v6, s[90:91]
	global_load_dword v28, v6, s[52:53]
	global_load_dword v3, v6, s[54:55]
	s_movk_i32 s5, 0x48
	v_lshrrev_b32_e32 v4, 3, v194
	v_mad_u32_u24 v4, v4, s5, v97
	v_lshrrev_b32_e32 v93, 4, v194
	v_lshl_add_u32 v102, v4, 1, s4
	v_or_b32_e32 v4, 64, v194
	v_lshlrev_b32_e32 v104, 2, v93
	v_lshrrev_b32_e32 v5, 3, v4
	v_mad_u32_u24 v5, v5, s5, v97
	v_or_b32_e32 v6, 2, v104
	v_cmp_eq_u32_e32 vcc, 0, v92
	v_lshl_add_u32 v101, v101, 1, s4
	v_lshl_add_u32 v103, v5, 1, s4
	v_cmp_lt_u32_e64 s[4:5], v92, v104
	v_cmp_gt_u32_e64 s[6:7], v92, v104
	v_or_b32_e32 v5, 1, v104
	v_cmp_lt_u32_e64 s[10:11], v92, v6
	v_cmp_gt_u32_e64 s[12:13], v92, v6
	v_lshlrev_b32_e32 v131, 6, v6
	v_or_b32_e32 v6, 3, v104
	v_cndmask_b32_e64 v104, 0, 1.0, vcc
	v_cmp_eq_u32_e32 vcc, 1, v92
	v_cvt_pk_bf16_f32 v120, v104, s0
	v_readlane_b32 s0, v252, 40
	v_cndmask_b32_e64 v105, 0, 1.0, vcc
	v_cmp_eq_u32_e32 vcc, 2, v92
	s_lshl_b32 s0, s0, 3
	v_readlane_b32 s1, v252, 43
	v_cndmask_b32_e64 v106, 0, 1.0, vcc
	v_cmp_eq_u32_e32 vcc, 3, v92
	s_add_i32 s0, s1, s0
	s_mov_b32 s45, 0x5040100
	v_cndmask_b32_e64 v107, 0, 1.0, vcc
	v_cmp_eq_u32_e32 vcc, 4, v92
	s_add_i32 s34, s0, s28
	v_readlane_b32 s0, v252, 37
	v_cndmask_b32_e64 v108, 0, 1.0, vcc
	v_cmp_eq_u32_e32 vcc, 5, v92
	v_mul_u32_u24_e32 v126, 12, v194
	v_lshlrev_b32_e32 v18, 4, v4
	v_cndmask_b32_e64 v109, 0, 1.0, vcc
	v_cmp_eq_u32_e32 vcc, 6, v92
	v_lshlrev_b32_e32 v4, 8, v93
	v_cmp_gt_u32_e64 s[8:9], v92, v5
	v_cndmask_b32_e64 v110, 0, 1.0, vcc
	v_cmp_eq_u32_e32 vcc, 7, v92
	v_lshlrev_b32_e32 v5, 6, v5
	v_cmp_lt_u32_e64 s[14:15], v92, v6
	v_cndmask_b32_e64 v111, 0, 1.0, vcc
	v_cmp_eq_u32_e32 vcc, 8, v92
	v_cmp_gt_u32_e64 s[16:17], v92, v6
	v_lshlrev_b32_e32 v132, 6, v6
	v_cndmask_b32_e64 v112, 0, 1.0, vcc
	v_cmp_eq_u32_e32 vcc, 9, v92
	s_waitcnt vmcnt(0)
; __global__ void __launch_bounds__(NTHR, 2) mk_fwd(Args args) {
;     ...
;                 if (gw < 64 * NCHUNK) P4_FETCH(gw);
; #pragma unroll 1
;                 for (int u = gw; u < 64 * NCHUNK; u += NGW) {
;     ...
; #pragma unroll
;                     for (int t = 0; t < 17; ++t) { xr_[t] = __builtin_bit_cast(float, (unsigned)nr_[t] << 16); xk_[t] = __builtin_bit_cast(float, (unsigned)nk_[t] << 16); xv_[t] = __builtin_bit_cast(float, (unsigned)nv_[t] << 16); }
; #pragma unroll
;                     for (int t = 0; t < 16; ++t) { xwl_[t] = __builtin_bit_cast(float, (unsigned)nwl_[t] << 16); xal_[t] = __builtin_bit_cast(float, (unsigned)nal_[t] << 16); }
	v_perm_b32 v212, v127, v124, s45
	v_perm_b32 v213, v128, v127, s45
	v_cndmask_b32_e64 v113, 0, 1.0, vcc
	v_cmp_eq_u32_e32 vcc, 10, v92
	v_perm_b32 v214, v123, v122, s45
	v_perm_b32 v215, v121, v96, s45
	v_cndmask_b32_e64 v114, 0, 1.0, vcc
	v_cmp_eq_u32_e32 vcc, 11, v92
	v_perm_b32 v93, v137, v136, s45
	v_perm_b32 v96, v134, v133, s45
	v_cndmask_b32_e64 v115, 0, 1.0, vcc
	v_cmp_eq_u32_e32 vcc, 12, v92
	v_perm_b32 v97, v130, v129, s45
	s_add_i32 s34, s30, s28
	v_cndmask_b32_e64 v116, 0, 1.0, vcc
	v_cmp_eq_u32_e32 vcc, 13, v92
	v_lshlrev_b32_e32 v8, 6, v194
	v_lshlrev_b32_e32 v10, 5, v194
	v_cndmask_b32_e64 v117, 0, 1.0, vcc
	v_cmp_eq_u32_e32 vcc, 14, v92
	v_mov_b32_e32 v11, v7
	v_cmp_gt_u32_e64 s[2:3], 16, v194
	v_cndmask_b32_e64 v118, 0, 1.0, vcc
	v_cmp_eq_u32_e32 vcc, 15, v92
	v_perm_b32 v92, v136, v135, s45
	v_lshlrev_b32_e32 v12, 4, v194
	v_mov_b32_e32 v9, v7
	v_mov_b32_e32 v13, v7
	v_mov_b32_e32 v19, v7
	v_cndmask_b32_e64 v119, 0, 1.0, vcc
	s_lshl_b32 s48, s34, 6
	s_lshl_b32 s51, s28, 6
	s_mov_b32 s79, 0xbfb8aa3b
	v_lshlrev_b32_e32 v6, 2, v194
	v_add_u32_e32 v121, v1, v4
	v_add_u32_e32 v122, v1, v5
	v_add_u32_e32 v123, v1, v131
	v_add_u32_e32 v124, v1, v132
	v_add_u32_e32 v125, v125, v126
	s_mov_b32 s34, s30
	v_mov_b32_e32 v160, v57
	v_mov_b32_e32 v163, v60
	v_mov_b32_e32 v166, v63
	v_mov_b32_e32 v169, v66
	v_mov_b32_e32 v171, v68
	v_mov_b32_e32 v173, v70
	v_mov_b32_e32 v175, v72
	v_mov_b32_e32 v177, v74
	v_mov_b32_e32 v179, v76
	v_mov_b32_e32 v181, v78
	v_mov_b32_e32 v183, v80
	v_mov_b32_e32 v185, v82
	v_mov_b32_e32 v187, v84
	v_mov_b32_e32 v189, v86
	v_mov_b32_e32 v191, v88
	v_mov_b32_e32 v193, v90
	v_mov_b32_e32 v162, v58
	v_mov_b32_e32 v165, v62
	v_mov_b32_e32 v168, v65
	v_mov_b32_e32 v170, v67
	v_mov_b32_e32 v172, v69
	v_mov_b32_e32 v174, v71
	v_mov_b32_e32 v176, v73
	v_mov_b32_e32 v178, v75
	v_mov_b32_e32 v180, v77
	v_mov_b32_e32 v182, v79
	v_mov_b32_e32 v184, v81
	v_mov_b32_e32 v186, v83
	v_mov_b32_e32 v188, v85
	v_mov_b32_e32 v190, v87
	v_mov_b32_e32 v192, v89
	v_mov_b32_e32 v196, v91
	v_mov_b32_e32 v127, v20
	v_mov_b32_e32 v130, v23
	v_mov_b32_e32 v146, v41
	v_mov_b32_e32 v126, v21
	v_mov_b32_e32 v129, v22
	v_mov_b32_e32 v132, v26
	v_mov_b32_e32 v134, v30
	v_mov_b32_e32 v136, v31
	v_mov_b32_e32 v138, v34
	v_mov_b32_e32 v140, v35
	v_mov_b32_e32 v142, v37
	v_mov_b32_e32 v144, v39
	v_mov_b32_e32 v147, v44
	v_mov_b32_e32 v149, v46
	v_mov_b32_e32 v151, v48
	v_mov_b32_e32 v153, v50
	v_mov_b32_e32 v155, v52
	v_mov_b32_e32 v157, v54
	v_mov_b32_e32 v159, v56
	v_mov_b32_e32 v164, v61
	v_mov_b32_e32 v128, v24
	v_mov_b32_e32 v131, v25
	v_mov_b32_e32 v133, v27
	v_mov_b32_e32 v135, v29
	v_mov_b32_e32 v137, v32
	v_mov_b32_e32 v139, v33
	v_mov_b32_e32 v141, v36
	v_mov_b32_e32 v143, v38
	v_mov_b32_e32 v145, v43
	v_mov_b32_e32 v148, v45
	v_mov_b32_e32 v150, v47
	v_mov_b32_e32 v152, v49
	v_mov_b32_e32 v154, v51
	v_mov_b32_e32 v156, v53
	v_mov_b32_e32 v158, v55
	v_mov_b32_e32 v161, v59
	v_mov_b32_e32 v167, v64
	v_mov_b32_e32 v197, v40
	v_mov_b32_e32 v198, v42
	v_mov_b32_e32 v200, v95
	v_mov_b32_e32 v201, v94
	v_mov_b32_e32 v202, v28
	v_mov_b32_e32 v203, v3
	v_mov_b32_e32 v204, v212
	v_mov_b32_e32 v205, v213
	v_mov_b32_e32 v206, v214
	v_mov_b32_e32 v207, v215
	v_mov_b32_e32 v208, v92
	v_mov_b32_e32 v209, v93
	v_mov_b32_e32 v210, v96
	v_mov_b32_e32 v211, v97
	v_readlane_b32 s81, v252, 1
	v_readlane_b32 s82, v252, 2
	v_readlane_b32 s83, v252, 3
	v_readlane_b32 s88, v252, 8
	v_readlane_b32 s89, v252, 9
	v_readlane_b32 s92, v252, 12
	v_readlane_b32 s93, v252, 13
	v_readlane_b32 s94, v252, 14
	v_readlane_b32 s95, v252, 15
	s_branch .LBB0_476

; __global__ void __launch_bounds__(NTHR, 2) mk_fwd(Args args) {
;     ...
;                 if (gw < 64 * NCHUNK) P4_FETCH(gw);
; #pragma unroll 1
;                 for (int u = gw; u < 64 * NCHUNK; u += NGW) {
;                     const int h = u & 15, c = (u >> 4) & 255, b = u >> 12, hd = b * 16 + h;
;                     const float mu_r = ncst_[0], mu_k = ncst_[1], mu_v = ncst_[2], c_w0 = ncst_[3], c_a0 = ncst_[4], c_kk = ncst_[5], c_ka = ncst_[6];
;                     unsigned char* pk = ws + WS_R + ((size_t)hd * NCHUNK + c) * PK_BYTES;
;                     float At[16], Rt[16], Bt[16], Kt[16], Vt[16];
;                     float xr_[17], xk_[17], xv_[17], xwl_[16], xal_[16];
; #pragma unroll
;                     for (int t = 0; t < 17; ++t) { xr_[t] = __builtin_bit_cast(float, (unsigned)nr_[t] << 16); xk_[t] = __builtin_bit_cast(float, (unsigned)nk_[t] << 16); xv_[t] = __builtin_bit_cast(float, (unsigned)nv_[t] << 16); }
; #pragma unroll
;                     for (int t = 0; t < 16; ++t) { xwl_[t] = __builtin_bit_cast(float, (unsigned)nwl_[t] << 16); xal_[t] = __builtin_bit_cast(float, (unsigned)nal_[t] << 16); }
;                     if (c == 0) { xr_[0] = 0.f; xk_[0] = 0.f; xv_[0] = 0.f; }
;                     asm volatile("" ::: "memory");
;                     if (u + NGW < 64 * NCHUNK) P4_FETCH(u + NGW);
.LBB0_476:
	s_add_i32 s75, s34, s28
	s_cmp_ge_i32 s75, s101
	s_cselect_b64 s[68:69], -1, 0
	s_and_b64 vcc, exec, s[68:69]
	v_mov_b32_e32 v199, v2
	s_cbranch_vccnz .LBB0_478
	s_ashr_i32 s0, s75, 12
	s_bfe_u32 s40, s75, 0x80004
	s_ashr_i32 s1, s0, 31
	s_lshl_b64 s[0:1], s[0:1], 12
	s_lshl_b32 s35, s40, 4
	s_or_b32 s88, s0, s35
	s_add_u32 s43, s88, -1
	s_addc_u32 s64, s1, -1
	s_and_b32 s35, s48, 0x3c0
	s_lshl_b32 s76, s35, 1
	s_cmp_eq_u32 s40, 0
	v_lshl_add_u64 v[4:5], v[14:15], 0, s[76:77]
	s_cselect_b32 s0, s0, s43
	s_cselect_b32 s1, s1, s64
	s_mul_i32 s40, s1, 0x2400
	v_mad_u64_u32 v[130:131], s[0:1], s0, v99, v[4:5]
	v_add_u32_e32 v131, s40, v131
	global_load_ushort v128, v[130:131], off
	global_load_ushort v126, v[130:131], off offset:2048
	v_add_co_u32_e32 v130, vcc, s36, v130
	v_mad_i64_i32 v[4:5], s[0:1], s88, v99, v[4:5]
	s_nop 0
	v_addc_co_u32_e32 v131, vcc, 0, v131, vcc
	v_add_co_u32_e32 v132, vcc, s36, v4
	global_load_ushort v127, v[130:131], off
	s_nop 0
	v_addc_co_u32_e32 v133, vcc, 0, v5, vcc
	global_load_ushort v131, v[4:5], off
	global_load_ushort v129, v[4:5], off offset:2048
	global_load_ushort v130, v[132:133], off
	s_mov_b64 s[0:1], 0x2400
	v_add_co_u32_e32 v132, vcc, s37, v4
	v_lshl_add_u64 v[134:135], v[4:5], 0, s[0:1]
	s_nop 0
	v_addc_co_u32_e32 v133, vcc, 0, v5, vcc
	global_load_ushort v133, v[132:133], off offset:1024
	s_nop 0
	global_load_ushort v132, v[134:135], off offset:2048
	v_add_co_u32_e32 v134, vcc, s38, v4
	s_movk_i32 s40, 0x4000
	s_nop 0
	v_addc_co_u32_e32 v135, vcc, 0, v5, vcc
	global_load_ushort v207, v[134:135], off offset:1024
	s_mov_b64 s[64:65], 0x4800
	v_add_co_u32_e32 v134, vcc, s40, v4
	v_lshl_add_u64 v[136:137], v[4:5], 0, s[64:65]
	s_nop 0
	v_addc_co_u32_e32 v135, vcc, 0, v5, vcc
	s_movk_i32 s0, 0x5000
	global_load_ushort v135, v[134:135], off offset:2048
	s_nop 0
	global_load_ushort v134, v[136:137], off offset:2048
	v_add_co_u32_e32 v136, vcc, s0, v4
	s_movk_i32 s43, 0x6000
	s_nop 0
	v_addc_co_u32_e32 v137, vcc, 0, v5, vcc
	global_load_ushort v208, v[136:137], off offset:2048
	s_mov_b64 s[0:1], 0x6c00
	v_add_co_u32_e32 v136, vcc, s43, v4
	v_lshl_add_u64 v[138:139], v[4:5], 0, s[0:1]
	s_nop 0
	v_addc_co_u32_e32 v137, vcc, 0, v5, vcc
	global_load_ushort v137, v[136:137], off offset:3072
	s_nop 0
	global_load_ushort v136, v[138:139], off offset:2048
	v_add_co_u32_e32 v138, vcc, s42, v4
	s_mov_b64 s[70:71], 0x9000
	s_nop 0
	v_addc_co_u32_e32 v139, vcc, 0, v5, vcc
	v_add_co_u32_e32 v142, vcc, s44, v4
	s_mov_b64 s[0:1], 0xb400
	s_nop 0
	v_addc_co_u32_e32 v143, vcc, 0, v5, vcc
	global_load_ushort v206, v[138:139], off offset:3072
	v_lshl_add_u64 v[140:141], v[4:5], 0, s[70:71]
	global_load_ushort v139, v[142:143], off offset:-4096
	global_load_ushort v138, v[140:141], off offset:2048
	global_load_ushort v209, v[142:143], off
	v_lshl_add_u64 v[142:143], v[4:5], 0, s[0:1]
	s_mov_b32 s0, 0xb000
	v_add_co_u32_e32 v140, vcc, s0, v4
	s_mov_b64 s[80:81], 0xd800
	s_nop 0
	v_addc_co_u32_e32 v141, vcc, 0, v5, vcc
	global_load_ushort v141, v[140:141], off offset:1024
	s_nop 0
	global_load_ushort v140, v[142:143], off offset:2048
	v_add_co_u32_e32 v142, vcc, s39, v4
	v_lshl_add_u64 v[144:145], v[4:5], 0, s[80:81]
	s_nop 0
	v_addc_co_u32_e32 v143, vcc, 0, v5, vcc
	global_load_ushort v204, v[142:143], off offset:1024
	v_add_co_u32_e32 v142, vcc, s41, v4
	s_mov_b32 s0, 0xe000
	s_nop 0
	v_addc_co_u32_e32 v143, vcc, 0, v5, vcc
	global_load_ushort v143, v[142:143], off offset:2048
	s_nop 0
	global_load_ushort v142, v[144:145], off offset:2048
	v_add_co_u32_e32 v144, vcc, s0, v4
	s_mov_b64 s[0:1], 0xfc00
	s_nop 0
	v_addc_co_u32_e32 v145, vcc, 0, v5, vcc
	global_load_ushort v205, v[144:145], off offset:2048
	v_add_co_u32_e32 v144, vcc, s49, v4
	v_lshl_add_u64 v[146:147], v[4:5], 0, s[0:1]
	s_nop 0
	v_addc_co_u32_e32 v145, vcc, 0, v5, vcc
	global_load_ushort v145, v[144:145], off offset:3072
	s_nop 0
	global_load_ushort v144, v[146:147], off offset:2048
	v_add_co_u32_e32 v146, vcc, s50, v4
	s_mov_b64 s[0:1], 0x14400
	s_nop 0
	v_addc_co_u32_e32 v147, vcc, 0, v5, vcc
	v_add_co_u32_e32 v150, vcc, s73, v4
	global_load_ushort v210, v[146:147], off offset:3072
	v_lshl_add_u64 v[146:147], v[4:5], 0, s[46:47]
	v_addc_co_u32_e32 v151, vcc, 0, v5, vcc
	v_lshl_add_u64 v[152:153], v[4:5], 0, s[0:1]
	s_mov_b32 s0, 0x14000
	global_load_ushort v148, v[150:151], off offset:-4096
	s_nop 0
	global_load_ushort v147, v[146:147], off offset:2048
	s_nop 0
	global_load_ushort v146, v[150:151], off
	v_add_co_u32_e32 v150, vcc, s0, v4
	s_mov_b64 s[82:83], 0x16800
	s_nop 0
	v_addc_co_u32_e32 v151, vcc, 0, v5, vcc
	global_load_ushort v150, v[150:151], off offset:1024
	s_nop 0
	global_load_ushort v149, v[152:153], off offset:2048
	v_add_co_u32_e32 v152, vcc, s78, v4
	v_lshl_add_u64 v[154:155], v[4:5], 0, s[82:83]
	s_nop 0
	v_addc_co_u32_e32 v153, vcc, 0, v5, vcc
	global_load_ushort v211, v[152:153], off offset:1024
	v_add_co_u32_e32 v152, vcc, s72, v4
	s_mov_b32 s0, 0x17000
	s_nop 0
	v_addc_co_u32_e32 v153, vcc, 0, v5, vcc
	global_load_ushort v152, v[152:153], off offset:2048
	s_nop 0
	global_load_ushort v151, v[154:155], off offset:2048
	v_add_co_u32_e32 v154, vcc, s0, v4
	s_mov_b64 s[0:1], 0x18c00
	s_nop 0
	v_addc_co_u32_e32 v155, vcc, 0, v5, vcc
	v_lshl_add_u64 v[156:157], v[4:5], 0, s[0:1]
	s_mov_b32 s0, 0x18000
	global_load_ushort v250, v[154:155], off offset:2048
	v_add_co_u32_e32 v154, vcc, s0, v4
	s_mov_b32 s0, 0x19000
	s_nop 0
	v_addc_co_u32_e32 v155, vcc, 0, v5, vcc
	global_load_ushort v154, v[154:155], off offset:3072
	s_nop 0
	global_load_ushort v153, v[156:157], off offset:2048
	v_add_co_u32_e32 v156, vcc, s0, v4
	s_mov_b64 s[0:1], 0x1b000
	s_nop 0
	v_addc_co_u32_e32 v157, vcc, 0, v5, vcc
	v_lshl_add_u64 v[158:159], v[4:5], 0, s[0:1]
	s_mov_b32 s0, 0x1c000
	v_add_co_u32_e32 v160, vcc, s0, v4
	s_mov_b64 s[0:1], 0x1d400
	s_nop 0
	v_addc_co_u32_e32 v161, vcc, 0, v5, vcc
	global_load_ushort v251, v[156:157], off offset:3072
	s_nop 0
	global_load_ushort v156, v[160:161], off offset:-4096
	global_load_ushort v155, v[158:159], off offset:2048
	global_load_ushort v253, v[160:161], off
	v_lshl_add_u64 v[160:161], v[4:5], 0, s[0:1]
	s_mov_b32 s0, 0x1d000
	v_add_co_u32_e32 v158, vcc, s0, v4
	s_mov_b32 s0, 0x1e000
	s_nop 0
	v_addc_co_u32_e32 v159, vcc, 0, v5, vcc
	global_load_ushort v158, v[158:159], off offset:1024
	s_nop 0
	global_load_ushort v157, v[160:161], off offset:2048
	v_add_co_u32_e32 v160, vcc, s0, v4
	s_mov_b64 s[0:1], 0x1f800
	s_nop 0
	v_addc_co_u32_e32 v161, vcc, 0, v5, vcc
	v_lshl_add_u64 v[162:163], v[4:5], 0, s[0:1]
	s_mov_b32 s0, 0x1f000
	global_load_ushort v254, v[160:161], off offset:1024
	v_add_co_u32_e32 v160, vcc, s0, v4
	s_mov_b32 s0, 0x20000
	s_nop 0
	v_addc_co_u32_e32 v161, vcc, 0, v5, vcc
	global_load_ushort v161, v[160:161], off offset:2048
	s_nop 0
	global_load_ushort v159, v[162:163], off offset:2048
	v_add_co_u32_e32 v162, vcc, s0, v4
	s_mov_b64 s[0:1], 0x21c00
	s_nop 0
	v_addc_co_u32_e32 v163, vcc, 0, v5, vcc
	global_load_ushort v255, v[162:163], off offset:2048
	v_lshl_add_u64 v[162:163], v[4:5], 0, s[0:1]
	s_mov_b32 s0, 0x21000
	v_add_co_u32_e32 v164, vcc, s0, v4
	s_mov_b32 s0, 0x22000
	s_nop 0
	v_addc_co_u32_e32 v165, vcc, 0, v5, vcc
	v_add_co_u32_e32 v4, vcc, s0, v4
	global_load_ushort v167, v[164:165], off offset:3072
	s_nop 0
	global_load_ushort v164, v[162:163], off offset:2048
	v_addc_co_u32_e32 v5, vcc, 0, v5, vcc
	global_load_ushort v195, v[4:5], off offset:3072
	v_lshl_add_u64 v[4:5], v[16:17], 0, s[76:77]
	v_mad_i64_i32 v[4:5], s[0:1], s88, v100, v[4:5]
	s_mov_b64 s[0:1], 0x1800
	v_add_co_u32_e32 v170, vcc, s36, v4
	v_lshl_add_u64 v[168:169], v[4:5], 0, s[0:1]
	s_nop 0
	v_addc_co_u32_e32 v171, vcc, 0, v5, vcc
	global_load_ushort v162, v[4:5], off
	global_load_ushort v160, v[4:5], off offset:2048
	global_load_ushort v165, v[170:171], off offset:2048
	global_load_ushort v163, v[168:169], off offset:2048
	s_mov_b64 s[0:1], 0x3000
	v_add_co_u32_e32 v168, vcc, s38, v4
	v_lshl_add_u64 v[170:171], v[4:5], 0, s[0:1]
	s_nop 0
	v_addc_co_u32_e32 v169, vcc, 0, v5, vcc
	global_load_ushort v168, v[168:169], off
	s_nop 0
	global_load_ushort v166, v[170:171], off offset:2048
	v_add_co_u32_e32 v170, vcc, s40, v4
	v_lshl_add_u64 v[172:173], v[4:5], 0, s[64:65]
	s_nop 0
	v_addc_co_u32_e32 v171, vcc, 0, v5, vcc
	global_load_ushort v170, v[170:171], off offset:2048
	s_nop 0
	global_load_ushort v169, v[172:173], off offset:2048
	s_mov_b64 s[0:1], 0x6000
	v_add_co_u32_e32 v172, vcc, s43, v4
	v_lshl_add_u64 v[174:175], v[4:5], 0, s[0:1]
	s_nop 0
	v_addc_co_u32_e32 v173, vcc, 0, v5, vcc
	global_load_ushort v172, v[172:173], off
	s_nop 0
	global_load_ushort v171, v[174:175], off offset:2048
	s_mov_b64 s[0:1], 0x7800
	v_add_co_u32_e32 v174, vcc, s42, v4
	v_lshl_add_u64 v[176:177], v[4:5], 0, s[0:1]
	s_nop 0
	v_addc_co_u32_e32 v175, vcc, 0, v5, vcc
	s_mov_b32 s0, 0x9000
	global_load_ushort v174, v[174:175], off offset:2048
	s_nop 0
	global_load_ushort v173, v[176:177], off offset:2048
	v_add_co_u32_e32 v176, vcc, s0, v4
	v_lshl_add_u64 v[178:179], v[4:5], 0, s[70:71]
	s_nop 0
	v_addc_co_u32_e32 v177, vcc, 0, v5, vcc
	global_load_ushort v176, v[176:177], off
	s_nop 0
	global_load_ushort v175, v[178:179], off offset:2048
	s_mov_b64 s[0:1], 0xa800
	v_add_co_u32_e32 v178, vcc, s44, v4
	v_lshl_add_u64 v[180:181], v[4:5], 0, s[0:1]
	s_nop 0
	v_addc_co_u32_e32 v179, vcc, 0, v5, vcc
	global_load_ushort v178, v[178:179], off offset:2048
	s_nop 0
	global_load_ushort v177, v[180:181], off offset:2048
	s_mov_b64 s[0:1], 0xc000
	v_add_co_u32_e32 v180, vcc, s39, v4
	v_lshl_add_u64 v[182:183], v[4:5], 0, s[0:1]
	s_nop 0
	v_addc_co_u32_e32 v181, vcc, 0, v5, vcc
	global_load_ushort v180, v[180:181], off
	s_nop 0
	global_load_ushort v179, v[182:183], off offset:2048
	v_add_co_u32_e32 v182, vcc, s41, v4
	v_lshl_add_u64 v[184:185], v[4:5], 0, s[80:81]
	s_nop 0
	v_addc_co_u32_e32 v183, vcc, 0, v5, vcc
	global_load_ushort v182, v[182:183], off offset:2048
	s_nop 0
	global_load_ushort v181, v[184:185], off offset:2048
	s_mov_b64 s[0:1], 0xf000
	v_add_co_u32_e32 v184, vcc, s49, v4
	v_lshl_add_u64 v[186:187], v[4:5], 0, s[0:1]
	s_nop 0
	v_addc_co_u32_e32 v185, vcc, 0, v5, vcc
	global_load_ushort v184, v[184:185], off
	s_nop 0
	global_load_ushort v183, v[186:187], off offset:2048
	s_mov_b64 s[0:1], 0x10800
	v_add_co_u32_e32 v186, vcc, s50, v4
	v_lshl_add_u64 v[188:189], v[4:5], 0, s[0:1]
	s_nop 0
	v_addc_co_u32_e32 v187, vcc, 0, v5, vcc
	s_mov_b32 s0, 0x12000
	global_load_ushort v186, v[186:187], off offset:2048
	s_nop 0
	global_load_ushort v185, v[188:189], off offset:2048
	v_add_co_u32_e32 v188, vcc, s0, v4
	v_lshl_add_u64 v[190:191], v[4:5], 0, s[46:47]
	s_nop 0
	v_addc_co_u32_e32 v189, vcc, 0, v5, vcc
	global_load_ushort v188, v[188:189], off
	s_nop 0
	global_load_ushort v187, v[190:191], off offset:2048
	s_mov_b64 s[0:1], 0x13800
	v_add_co_u32_e32 v190, vcc, s73, v4
	v_lshl_add_u64 v[192:193], v[4:5], 0, s[0:1]
	s_nop 0
	v_addc_co_u32_e32 v191, vcc, 0, v5, vcc
	global_load_ushort v190, v[190:191], off offset:2048
	s_nop 0
	global_load_ushort v189, v[192:193], off offset:2048
	v_add_co_u32_e32 v192, vcc, s78, v4
	s_mov_b64 s[0:1], 0x15000
	s_nop 0
	v_addc_co_u32_e32 v193, vcc, 0, v5, vcc
	v_lshl_add_u64 v[196:197], v[4:5], 0, s[0:1]
	v_lshl_add_u64 v[198:199], v[4:5], 0, s[82:83]
	v_add_co_u32_e32 v4, vcc, s72, v4
	global_load_ushort v192, v[192:193], off
	s_nop 0
	global_load_ushort v191, v[196:197], off offset:2048
	v_addc_co_u32_e32 v5, vcc, 0, v5, vcc
	global_load_ushort v196, v[4:5], off offset:2048
	global_load_ushort v193, v[198:199], off offset:2048
	v_or_b32_e32 v4, s35, v194
	v_readlane_b32 s80, v252, 0
	v_lshlrev_b32_e32 v4, 2, v4
	v_mov_b32_e32 v5, v7
	v_readlane_b32 s84, v252, 4
	v_readlane_b32 s85, v252, 5
	v_readlane_b32 s86, v252, 6
	v_readlane_b32 s87, v252, 7
	v_lshl_add_u64 v[200:201], s[84:85], 0, v[4:5]
	v_add_co_u32_e32 v198, vcc, s36, v200
	v_readlane_b32 s90, v252, 10
	s_nop 0
	v_addc_co_u32_e32 v199, vcc, 0, v201, vcc
	v_add_co_u32_e32 v200, vcc, 0x2000, v200
	v_readlane_b32 s91, v252, 11
	s_nop 0
	v_addc_co_u32_e32 v201, vcc, 0, v201, vcc
	global_load_dword v197, v4, s[84:85]
	global_load_dword v198, v[198:199], off
	s_nop 0
	global_load_dword v199, v[200:201], off
	s_nop 0
	global_load_dword v200, v4, s[86:87]
	global_load_dword v201, v4, s[90:91]
	global_load_dword v202, v4, s[52:53]
	global_load_dword v203, v4, s[54:55]
	v_readlane_b32 s81, v252, 1
	v_readlane_b32 s82, v252, 2
	v_readlane_b32 s83, v252, 3
	v_readlane_b32 s88, v252, 8
	v_readlane_b32 s89, v252, 9
	v_readlane_b32 s92, v252, 12
	v_readlane_b32 s93, v252, 13
	v_readlane_b32 s94, v252, 14
	v_readlane_b32 s95, v252, 15

; __device__ __forceinline__ unsigned xb_ld(unsigned* p)              { return __hip_atomic_load(p, __ATOMIC_RELAXED, __HIP_MEMORY_SCOPE_AGENT); }
; __device__ __forceinline__ unsigned xb_add(unsigned* p, unsigned v) { return __hip_atomic_fetch_add(p, v, __ATOMIC_RELAXED, __HIP_MEMORY_SCOPE_AGENT); }
; #define XB_SPIN(cond, bar) do { unsigned _sp = 0; while (cond) { __builtin_amdgcn_s_sleep(1); \
;     if ((++_sp & 255u) == 0u) { if (xb_ld(&(bar)[XB_TMO])) break; if (_sp > XB_SPIN_CAP) { atomicAdd(&(bar)[XB_TMO], 1u); break; } } } } while (0)
; #define SEAM(k) do { if (IN(k) && IN((k) + 1)) xcd_barrier(bar); } while (0)
; __device__ __forceinline__ void xcd_barrier(const XcdBarrier& b) {
;     asm volatile("s_waitcnt vmcnt(0)" ::: "memory");
;     __syncthreads();
;     if (threadIdx.x == 0) {
;         unsigned* bar = b.bar;
;         __builtin_amdgcn_s_waitcnt(0);
;         unsigned nloc = b.st[0], nx = b.st[1];
;         if (nloc == 0u) { xcd_barrier_complete(bar, b.x, nloc, nx); b.st[0] = nloc; b.st[1] = nx; }
;         const unsigned old = xb_add(&bar[XB_XSUB(b.x)], 1u);
;         const unsigned gen = old / nloc;
;         if (old + 1u == (gen + 1u) * nloc) {
;             __builtin_amdgcn_fence(__ATOMIC_RELEASE, "agent");
;             asm volatile("s_waitcnt vmcnt(0)" ::: "memory");
;             const unsigned og = xb_add(&bar[XB_TOP], 1u);
;             const unsigned tg = og / nx;
;             if (og + 1u == (tg + 1u) * nx) xb_add(&bar[XB_TOPGEN], 1u);
;             else XB_SPIN(xb_ld(&bar[XB_TOPGEN]) == tg, bar);
;             __builtin_amdgcn_fence(__ATOMIC_ACQUIRE, "agent");
;             xb_add(&bar[XB_XGEN(b.x)], 1u);
;             asm volatile("s_waitcnt vmcnt(0)" ::: "memory");
;         } else {
;             XB_SPIN(xb_ld(&bar[XB_XGEN(b.x)]) == gen, bar);
;             __builtin_amdgcn_fence(__ATOMIC_ACQUIRE, "agent");
;             asm volatile("s_waitcnt vmcnt(0)" ::: "memory");
;         }
;     }
;     __syncthreads();
; }
; __global__ void __launch_bounds__(NTHR, 2) mk_fwd(Args args) {
;     ...
;     SEAM(4);
.LBB0_480:
	v_lshlrev_b32_e32 v195, 2, v0
	v_readlane_b32 s88, v252, 44
	v_readlane_b32 s78, v252, 50
	v_readlane_b32 s2, v252, 52
	v_readlane_b32 s89, v252, 45
	v_readlane_b32 s79, v252, 51
	v_readlane_b32 s3, v252, 53
	s_mov_b64 exec, -1
	s_waitcnt vmcnt(0) lgkmcnt(0)
	s_barrier
	v_readlane_b32 s28, v252, 54
	v_readlane_b32 s30, v252, 55
	v_readlane_b32 s0, v252, 43
	s_nop 3
	s_cmp_lg_u32 s0, 0
	s_cbranch_scc1 .Lrel_skip
	buffer_wbl2 sc1
	s_waitcnt vmcnt(0) lgkmcnt(0)
	v_cmp_eq_u32_e32 vcc, 0, v194
	s_and_saveexec_b64 s[0:1], vcc
	v_mov_b32_e32 v1, 0
	v_mov_b32_e32 v2, 1
	global_atomic_add v1, v2, s[26:27] offset:256
	s_or_b64 exec, exec, s[0:1]
	s_waitcnt vmcnt(0) lgkmcnt(0)
.Lrel_skip:
.LBB0_481:
	s_cmp_gt_i32 s89, 5
	s_cselect_b64 s[0:1], -1, 0
	s_and_b64 s[2:3], s[2:3], s[0:1]
	s_andn2_b64 vcc, exec, s[2:3]
	s_branch .LBB0_535
	s_waitcnt vmcnt(0)
	s_waitcnt vmcnt(0) lgkmcnt(0)
	s_barrier
	s_mov_b64 s[2:3], exec
	v_readlane_b32 s4, v252, 35
	v_readlane_b32 s5, v252, 36
	s_and_b64 s[4:5], s[2:3], s[4:5]
	s_mov_b64 exec, s[4:5]
	s_cbranch_execz .LBB0_534
	s_add_i32 s4, 0, 0x27020
	v_mov_b32_e32 v1, s4
	s_waitcnt vmcnt(0) expcnt(0) lgkmcnt(0)
	ds_read_b32 v3, v1
	s_add_i32 s4, 0, 0x27024
	v_mov_b32_e32 v1, s4
	ds_read_b32 v1, v1
	s_waitcnt lgkmcnt(1)
	v_cmp_ne_u32_e32 vcc, 0, v3
	s_cbranch_vccnz .LBB0_498
	v_readlane_b32 s4, v252, 32
	v_readlane_b32 s5, v252, 33
	s_load_dwordx2 s[8:9], s[4:5], 0x4
	s_add_u32 s4, s26, 0x4200
	s_addc_u32 s5, s27, 0
	s_add_u32 s6, s26, 0x4400
	s_addc_u32 s7, s27, 0
	s_waitcnt lgkmcnt(0)
	s_mul_i32 s29, s8, s33
	s_add_u32 s8, s26, 0x4500
	s_mul_i32 s29, s29, s9
	s_addc_u32 s9, s27, 0
	s_add_u32 s10, s26, 0x4600
	s_addc_u32 s11, s27, 0
	s_add_u32 s12, s26, 0x4700
	s_addc_u32 s13, s27, 0
	s_add_u32 s14, s26, 0x4800
	s_addc_u32 s15, s27, 0
	s_add_u32 s16, s26, 0x4900
	s_addc_u32 s17, s27, 0
	s_add_u32 s34, s26, 0x4a00
	s_addc_u32 s35, s27, 0
	s_add_u32 s36, s26, 0x4b00
	s_addc_u32 s37, s27, 0
	s_add_u32 s38, s26, 0x4c00
	s_addc_u32 s39, s27, 0
	s_add_u32 s40, s26, 0x4d00
	s_addc_u32 s41, s27, 0
	s_add_u32 s42, s26, 0x4e00
	s_addc_u32 s43, s27, 0
	s_add_u32 s44, s26, 0x4f00
	s_addc_u32 s45, s27, 0
	s_add_u32 s46, s26, 0x5000
	s_addc_u32 s47, s27, 0
	s_add_u32 s48, s26, 0x5100
	s_addc_u32 s49, s27, 0
	s_add_u32 s50, s26, 0x5200
	s_addc_u32 s51, s27, 0
	s_add_u32 s52, s26, 0x5300
	s_addc_u32 s53, s27, 0
	s_mov_b32 s31, 1
	v_mov_b32_e32 v17, 0
	s_branch .LBB0_486

; #define LAS __attribute__((address_space(3)))
; __global__ void __launch_bounds__(NTHR, 2) mk_fwd(Args args) {
;     ...
;             } else {
;                 const int lw = wave - 4;
; #pragma unroll 1
;                 for (int c = 0; c < NCHUNK + LAG; ++c) {
;                     if (c < NCHUNK) {
;                         if (c >= NSLOT) { const unsigned want = (unsigned)(c - NSLOT + 1); unsigned sp_ = 0;
;                             for (;;) { const v4u dd_ = *(volatile LAS v4u*)ring_done; if (min(min(dd_.x, dd_.y), min(dd_.z, dd_.w)) >= want) break; __builtin_amdgcn_s_sleep(0); if (++sp_ > (1u << 26)) break; } }
;                         asm volatile("" ::: "memory");
;                         const unsigned char* src = PACK + (size_t)c * PK_BYTES + lw * 1024 + lane * 16;
;                         LAS unsigned char* dst = lds + (c & (NSLOT - 1)) * PK_BYTES + lw * 1024;
; #pragma unroll
;                         for (int p = 0; p < 3; ++p) __builtin_amdgcn_global_load_lds((const unsigned*)(src + p * 4096), (LAS unsigned*)(dst + p * 4096), 16, 0, 0);
;                         if (lw < 2) __builtin_amdgcn_global_load_lds((const unsigned*)(src + 3 * 4096), (LAS unsigned*)(dst + 3 * 4096), 16, 0, 0);
;                     }
;                     if (c >= LAG) {
;                         if (c < NCHUNK) { if (lw < 2) asm volatile("s_waitcnt vmcnt(12)" ::: "memory"); else asm volatile("s_waitcnt vmcnt(9)" ::: "memory"); } else asm volatile("s_waitcnt vmcnt(0)" ::: "memory");
;                         if (lane == 0) __hip_atomic_fetch_add(ring_ready + lw, 1u, __ATOMIC_RELAXED, __HIP_MEMORY_SCOPE_WORKGROUP);
;                     }
;                 }
;             }
.LBB0_586:
	s_andn2_b64 vcc, exec, s[2:3]
	s_cbranch_vccnz .LBB0_670
	v_readlane_b32 s2, v252, 38
	s_lshl_b32 s2, s2, 3
	v_readlane_b32 s3, v252, 39
	s_add_i32 s6, s2, s3
	v_readlane_b32 s10, v252, 42
	s_cmpk_gt_u32 s10, 0xff
	s_mov_b64 s[2:3], -1
	s_cbranch_scc0 .LBB0_611
	v_writelane_b32 v252, s0, 54
	v_writelane_b32 v252, s1, 55
	v_writelane_b32 v252, s28, 56
	v_writelane_b32 v252, s29, 57
	v_writelane_b32 v252, s30, 58
	v_writelane_b32 v252, s72, 59
	v_writelane_b32 v252, s86, 60
	v_writelane_b32 v252, s90, 61
	v_writelane_b32 v252, s91, 62
	v_readlane_b32 s4, v252, 43
	s_nop 3
	s_sub_i32 s4, s4, 4
	s_lshr_b32 s5, s6, 4
	s_and_b32 s7, s6, 15
	s_lshl_b32 s5, s5, 12
	s_or_b32 s5, s5, s7
	s_lshl_b32 s7, s4, 4
	s_or_b32 s30, s5, s7
	s_movk_i32 s28, 64
	s_add_u32 s10, s26, 0x6008000
	s_addc_u32 s11, s27, 0
	s_and_b32 s101, s30, 0xfffff000
	s_add_i32 s101, s101, 2560
	s_lshl_b32 s100, s4, 14
	s_lshl_b32 s98, s4, 2
	s_add_i32 s98, s98, 0x27380
	v_mov_b32_e32 v1, s98
	v_mov_b32_e32 v2, s4
	ds_write_b32 v1, v2
	s_waitcnt vmcnt(0) lgkmcnt(0)
	s_branch .Lprod_code
.Lprod_exit:
	s_mov_b64 exec, -1
	v_readlane_b32 s4, v252, 38
	s_nop 3
	s_lshl_b32 s4, s4, 3
	v_readlane_b32 s5, v252, 39
	s_nop 3
	s_add_i32 s6, s4, s5
	s_mov_b32 s7, 0
	s_lshl_b64 s[4:5], s[6:7], 22
	s_add_u32 s4, s26, s4
	s_addc_u32 s5, s27, s5
	s_sub_i32 s7, s98, 0x27380
	s_lshl_b32 s7, s7, 8
	s_add_u32 s4, s4, s7
	s_addc_u32 s5, s5, 0
	s_add_u32 s4, s4, 0x21c08000
	s_addc_u32 s5, s5, 0
	v_lshlrev_b32_e32 v2, 4, v194
	v_mov_b32_e32 v3, 0
	v_lshl_add_u64 v[2:3], s[4:5], 0, v[2:3]
	s_mov_b64 s[12:13], 0x1000
	s_mov_b64 s[14:15], 0x2000
	s_mov_b64 s[16:17], 0x3000
	v_mov_b32_e32 v1, 0
	s_mov_b32 s5, 0
.Lld_gpoll:
	global_load_dword v4, v1, s[26:27] offset:256 sc1
	s_waitcnt vmcnt(0)
	v_readfirstlane_b32 s8, v4
	s_nop 3
	s_cmpk_eq_u32 s8, 192
	s_cbranch_scc1 .Lld_gok
	s_sleep 8
	s_add_i32 s5, s5, 1
	s_cmp_lt_u32 s5, 0x100000
	s_cbranch_scc1 .Lld_gpoll
.Lld_gok:
	buffer_inv sc1
	s_waitcnt vmcnt(0)
	s_movk_i32 s39, 160
	s_mov_b32 s9, 0
.Lld_loop:
	s_sub_i32 s8, s39, 3
	v_mov_b32_e32 v1, 0x27390
	s_mov_b32 s5, 0
.Lld_spoll:
	ds_read_b128 v[4:7], v1
	s_waitcnt lgkmcnt(0)
	v_min_u32_e32 v6, v6, v7
	v_min3_u32 v4, v4, v5, v6
	v_cmp_le_i32_e32 vcc, s8, v4
	s_cbranch_vccnz .Lld_sok
	s_sleep 0
	s_add_i32 s5, s5, 1
	s_cmp_lt_u32 s5, 0x1000000
	s_cbranch_scc1 .Lld_spoll
.Lld_sok:
	s_lshl_b32 s8, s39, 14
	v_lshl_add_u64 v[4:5], v[2:3], 0, s[8:9]
	s_and_b32 s8, s8, 0xc000
	s_add_i32 s8, s8, s7
	s_mov_b32 m0, s8
	v_lshl_add_u64 v[6:7], v[4:5], 0, s[12:13]
	global_load_lds_dwordx4 v[4:5], off
	s_add_i32 m0, s8, 0x1000
	s_nop 0
	global_load_lds_dwordx4 v[6:7], off
	v_lshl_add_u64 v[6:7], v[4:5], 0, s[14:15]
	s_add_i32 m0, s8, 0x2000
	s_nop 0
	global_load_lds_dwordx4 v[6:7], off
	s_cmpk_gt_u32 s7, 0x400
	s_cbranch_scc1 .Lld_three
	v_lshl_add_u64 v[6:7], v[4:5], 0, s[16:17]
	s_add_i32 m0, s8, 0x3000
	s_nop 0
	global_load_lds_dwordx4 v[6:7], off
	s_cmpk_eq_i32 s39, 160
	s_cbranch_scc1 .Lld_next
	s_waitcnt vmcnt(4)
	s_branch .Lld_pub
.Lld_three:
	s_cmpk_eq_i32 s39, 160
	s_cbranch_scc1 .Lld_next
	s_waitcnt vmcnt(3)
.Lld_pub:
	v_mov_b32_e32 v4, s98
	v_mov_b32_e32 v5, s39
	ds_write_b32 v4, v5
.Lld_next:
	s_add_i32 s39, s39, 1
	s_cmpk_lt_i32 s39, 0x100
	s_cbranch_scc1 .Lld_loop
	s_waitcnt vmcnt(0)
	v_mov_b32_e32 v4, s98
	v_mov_b32_e32 v5, 0x100
	ds_write_b32 v4, v5
	s_waitcnt lgkmcnt(0)
	v_readlane_b32 s0, v252, 54
	v_readlane_b32 s1, v252, 55
	v_readlane_b32 s28, v252, 56
	v_readlane_b32 s29, v252, 57
	v_readlane_b32 s30, v252, 58
	v_readlane_b32 s72, v252, 59
	v_readlane_b32 s86, v252, 60
	v_readlane_b32 s90, v252, 61
	v_readlane_b32 s91, v252, 62
	s_nop 3

.LBB0_623:
	s_add_i32 s8, s5, -1
	s_lshl_b32 s12, s8, 14
	s_and_b32 s12, s12, 0xc000
	s_add_i32 s12, s12, 0
	v_lshlrev_b32_e32 v30, 1, v176
	v_add3_u32 v87, s12, v181, v30
	ds_read_u16 v30, v87 offset:11264
	ds_read_u16 v31, v87 offset:11296
	ds_read_u16 v82, v87 offset:11328
	s_lshl_b32 s13, s8, 12
	s_and_b32 s13, s13, 0x3000
	v_add_u32_e32 v78, s13, v190
	v_add_u32_e32 v88, s12, v180
	s_waitcnt lgkmcnt(0)
	v_lshlrev_b32_e32 v86, 16, v82
	s_add_i32 s13, s35, s12
	v_add_u32_e32 v82, s12, v1
	ds_read_b128 v[78:81], v78
	v_add3_u32 v90, s13, v178, v179
	ds_read_b128 v[82:85], v82 offset:13312
	ds_read_u16 v87, v87 offset:11360
	ds_read_b64 v[88:89], v88 offset:2048
	ds_read_u16 v92, v90 offset:7176
	ds_read_u16 v93, v90 offset:7240
	ds_read_u16 v94, v90 offset:7304
	ds_read_u16 v95, v90 offset:7368
	s_waitcnt lgkmcnt(6)
	v_rcp_f32_e32 v82, v82
	v_rcp_f32_e32 v83, v83
	s_waitcnt lgkmcnt(4)
	v_lshlrev_b32_e32 v90, 16, v88
	v_and_b32_e32 v91, 0xffff0000, v88
	s_waitcnt lgkmcnt(2)
	v_lshlrev_b32_e32 v93, 16, v93
	v_lshlrev_b32_e32 v92, 16, v92
	v_pk_mul_f32 v[90:91], v[90:91], v[92:93]
	v_rcp_f32_e32 v84, v84
	s_waitcnt vmcnt(1)
	v_pk_mul_f32 v[90:91], v[10:11], v[90:91]
	v_rcp_f32_e32 v85, v85
	v_pk_mul_f32 v[82:83], v[82:83], v[90:91]
	v_lshlrev_b32_e32 v88, 16, v89
	v_and_b32_e32 v89, 0xffff0000, v89
	s_waitcnt lgkmcnt(0)
	v_lshlrev_b32_e32 v91, 16, v95
	v_lshlrev_b32_e32 v90, 16, v94
	v_pk_mul_f32 v[88:89], v[88:89], v[90:91]
	v_add_f32_e32 v82, v82, v83
	v_pk_mul_f32 v[88:89], v[12:13], v[88:89]
	v_lshlrev_b32_e32 v30, 16, v30
	v_pk_mul_f32 v[84:85], v[84:85], v[88:89]
	v_lshlrev_b32_e32 v31, 16, v31
	v_add_f32_e32 v82, v82, v84
	v_add_f32_e32 v82, v82, v85
	v_lshlrev_b32_e32 v87, 16, v87
	s_lshl_b64 s[12:13], s[8:9], 16
	v_add_f32_dpp v88, v82, v82 quad_perm:[1,0,3,2] row_mask:0xf bank_mask:0xf bound_ctrl:1
	v_add_f32_e32 v82, v78, v79
	v_add_f32_e32 v82, v80, v82
	v_add_f32_e32 v82, v81, v82
	s_nop 1
	v_add_f32_dpp v82, v82, v82 quad_perm:[1,0,3,2] row_mask:0xf bank_mask:0xf bound_ctrl:1
	s_nop 1
	v_add_f32_dpp v82, v82, v82 quad_perm:[2,3,0,1] row_mask:0xf bank_mask:0xf bound_ctrl:1
	s_nop 1
	v_add_f32_dpp v82, v82, v82 row_half_mirror row_mask:0xf bank_mask:0xf bound_ctrl:1
	s_nop 1
	v_add_f32_dpp v82, v82, v82 row_mirror row_mask:0xf bank_mask:0xf bound_ctrl:1
	v_fmamk_f32 v79, v82, 0xbc800000, v79
	v_fmamk_f32 v78, v82, 0xbc800000, v78
	v_fmamk_f32 v81, v82, 0xbc800000, v81
	v_fmac_f32_e32 v80, 0xbc800000, v82
	v_pk_mul_f32 v[84:85], v[78:79], v[78:79]
	v_pk_mul_f32 v[82:83], v[80:81], v[80:81]
	v_add_f32_e32 v84, v84, v85
	v_add_f32_e32 v82, v82, v84
	v_add_f32_e32 v82, v83, v82
	v_add_f32_dpp v83, v88, v88 quad_perm:[2,3,0,1] row_mask:0xf bank_mask:0xf bound_ctrl:1
	s_nop 0
	v_add_f32_dpp v82, v82, v82 quad_perm:[1,0,3,2] row_mask:0xf bank_mask:0xf bound_ctrl:1
	v_add_f32_dpp v83, v83, v83 row_half_mirror row_mask:0xf bank_mask:0xf bound_ctrl:1
	s_nop 0
	v_add_f32_dpp v82, v82, v82 quad_perm:[2,3,0,1] row_mask:0xf bank_mask:0xf bound_ctrl:1
	v_add_f32_dpp v84, v83, v83 row_mirror row_mask:0xf bank_mask:0xf bound_ctrl:1
	s_nop 0
	v_add_f32_dpp v82, v82, v82 row_half_mirror row_mask:0xf bank_mask:0xf bound_ctrl:1
	s_nop 1
	v_add_f32_dpp v82, v82, v82 row_mirror row_mask:0xf bank_mask:0xf bound_ctrl:1
	v_fmamk_f32 v82, v82, 0x3c800000, v193
	v_rsq_f32_e32 v82, v82
	s_nop 0
	v_pk_mul_f32 v[78:79], v[78:79], v[82:83] op_sel_hi:[1,0]
	v_pk_mul_f32 v[80:81], v[80:81], v[82:83] op_sel_hi:[1,0]
	v_pk_fma_f32 v[78:79], v[2:3], v[78:79], v[6:7]
	v_pk_fma_f32 v[80:81], v[4:5], v[80:81], v[8:9]
	v_pk_fma_f32 v[30:31], v[84:85], v[30:31], v[78:79] op_sel_hi:[0,1,1]
	v_pk_fma_f32 v[78:79], v[84:85], v[86:87], v[80:81] op_sel_hi:[0,1,1]
	v_lshlrev_b32_e32 v80, 16, v172
	v_and_b32_e32 v81, 0xffff0000, v172
	v_lshlrev_b32_e32 v82, 16, v173
	v_and_b32_e32 v83, 0xffff0000, v173
	v_pk_mul_f32 v[78:79], v[78:79], v[82:83]
	v_pk_mul_f32 v[30:31], v[30:31], v[80:81]
	s_nop 0
	v_cvt_pk_bf16_f32 v30, v30, v31
	v_cvt_pk_bf16_f32 v31, v78, v79
	v_lshl_add_u64 v[78:79], v[170:171], 0, s[12:13]
	global_store_dwordx2 v[78:79], v[30:31], off
	s_waitcnt lgkmcnt(0)
	s_and_saveexec_b64 s[12:13], s[2:3]
	v_mov_b32_e32 v30, s34
	v_mov_b32_e32 v31, 1
	ds_add_u32 v30, v31
	v_mov_b32_e32 v30, s31
	ds_add_u32 v30, v31

.LBB0_633:
	s_or_b32 s43, s5, 1
	v_lshl_or_b32 v30, s43, 4, v176
	v_or_b32_e32 v78, s6, v30
	v_mov_b64_e32 v[30:31], s[66:67]
	v_mad_u64_u32 v[30:31], s[12:13], v78, s36, v[30:31]
	v_mad_i32_i24 v31, s7, v177, v31
	v_lshl_add_u64 v[30:31], v[30:31], 0, s[10:11]
	v_lshl_add_u64 v[30:31], v[30:31], 0, v[162:163]
	v_add_co_u32_e32 v30, vcc, s37, v30
	v_cvt_pk_bf16_f32 v198, v106, v107
	s_nop 0
	v_addc_co_u32_e32 v31, vcc, 0, v31, vcc
	global_load_dwordx2 v[172:173], v[30:31], off
	v_cvt_pk_bf16_f32 v199, v108, v109
	v_cvt_pk_bf16_f32 v200, v110, v111
	v_cvt_pk_bf16_f32 v201, v112, v113
	s_lshl_b32 s8, s43, 14
	s_and_b32 s8, s8, 0xc000
	v_mfma_f32_16x16x32_bf16 v[70:73], v[70:73], v[198:201], 0
	s_add_i32 s12, s8, 0
	v_cvt_pk_bf16_f32 v158, v114, v115
	v_cvt_pk_bf16_f32 v159, v116, v117
	v_cvt_pk_bf16_f32 v160, v118, v119
	v_cvt_pk_bf16_f32 v161, v120, v121
	v_add_u32_e32 v30, s12, v184
	ds_read_b128 v[154:157], v30
	ds_read_b128 v[146:149], v30 offset:64
	ds_read_b128 v[138:141], v30 offset:2048
	ds_read_b128 v[98:101], v30 offset:2112
	v_mfma_f32_16x16x32_bf16 v[62:65], v[62:65], v[158:161], v[70:73]
	v_add_u32_e32 v30, s12, v185
	ds_read_b128 v[150:153], v30 offset:4096
	ds_read_b128 v[142:145], v30 offset:5120
	ds_read_b128 v[102:105], v30 offset:6144
	ds_read_b128 v[94:97], v30 offset:7168
	v_add_u32_e32 v30, s12, v187
	v_add3_u32 v31, s12, v188, v183
	ds_read_b128 v[90:93], v30 offset:8192
	ds_read_b128 v[86:89], v30 offset:9216
	ds_read_b128 v[78:81], v30 offset:10240
	ds_read_b64 v[84:85], v31 offset:11264
	v_mov_b32_e32 v30, v32
	v_mov_b32_e32 v31, v33
	v_add_u32_e32 v70, s12, v186
	ds_read_b128 v[134:137], v70 offset:13312
	ds_read_b128 v[130:133], v70 offset:13376
	ds_read_b128 v[126:129], v70 offset:13440
	ds_read_b128 v[122:125], v70 offset:13504
	v_mfma_f32_16x16x32_bf16 v[62:65], v[74:77], v[30:33], v[62:65]
	s_mov_b32 s8, 0
	v_mfma_f32_16x16x32_bf16 v[58:61], v[58:61], v[198:201], 0
	s_nop 5
	v_cvt_pk_bf16_f32 v62, v62, v63
	v_cvt_pk_bf16_f32 v63, v64, v65
	v_mov_b32_e32 v64, v163
	v_mov_b32_e32 v65, v163
	s_nop 1
	v_mfma_f32_16x16x32_bf16 v[62:65], v[66:69], v[62:65], 0
	s_cmp_lt_u32 s5, s99
	s_cbranch_scc1 .Lscan_y1_skip
	s_branch .LBB0_635

.LBB0_644:
	s_lshl_b32 s12, s5, 14
	s_and_b32 s12, s12, 0x8000
	s_add_i32 s12, s12, 0
	v_lshlrev_b32_e32 v31, 1, v176
	v_add3_u32 v25, s12, v181, v31
	ds_read_u16 v18, v25 offset:11264
	ds_read_u16 v19, v25 offset:11296
	ds_read_u16 v20, v25 offset:11328
	v_lshlrev_b32_e32 v30, 2, v189
	v_add3_u32 v14, s8, v30, v182
	s_waitcnt lgkmcnt(2)
	v_lshlrev_b32_e32 v22, 16, v18
	v_add_u32_e32 v26, s12, v180
	s_add_i32 s8, s35, s12
	v_add_u32_e32 v18, s12, v1
	ds_read_b128 v[14:17], v14
	s_waitcnt lgkmcnt(2)
	v_lshlrev_b32_e32 v23, 16, v19
	s_waitcnt lgkmcnt(1)
	v_lshlrev_b32_e32 v24, 16, v20
	v_add3_u32 v28, s8, v178, v179
	ds_read_b128 v[18:21], v18 offset:13312
	ds_read_u16 v25, v25 offset:11360
	ds_read_b64 v[26:27], v26 offset:2048
	ds_read_u16 v32, v28 offset:7176
	ds_read_u16 v33, v28 offset:7240
	ds_read_u16 v34, v28 offset:7304
	ds_read_u16 v35, v28 offset:7368
	s_waitcnt lgkmcnt(6)
	v_rcp_f32_e32 v18, v18
	v_rcp_f32_e32 v19, v19
	s_waitcnt lgkmcnt(4)
	v_lshlrev_b32_e32 v28, 16, v26
	v_and_b32_e32 v29, 0xffff0000, v26
	s_waitcnt lgkmcnt(2)
	v_lshlrev_b32_e32 v33, 16, v33
	v_lshlrev_b32_e32 v32, 16, v32
	v_pk_mul_f32 v[28:29], v[28:29], v[32:33]
	v_rcp_f32_e32 v20, v20
	s_waitcnt vmcnt(2)
	v_pk_mul_f32 v[28:29], v[10:11], v[28:29]
	v_rcp_f32_e32 v21, v21
	v_pk_mul_f32 v[18:19], v[18:19], v[28:29]
	v_lshlrev_b32_e32 v26, 16, v27
	v_and_b32_e32 v27, 0xffff0000, v27
	s_waitcnt lgkmcnt(0)
	v_lshlrev_b32_e32 v29, 16, v35
	v_lshlrev_b32_e32 v28, 16, v34
	v_pk_mul_f32 v[26:27], v[26:27], v[28:29]
	v_add_f32_e32 v18, v18, v19
	v_pk_mul_f32 v[26:27], v[12:13], v[26:27]
	v_lshlrev_b32_e32 v25, 16, v25
	v_pk_mul_f32 v[20:21], v[20:21], v[26:27]
	s_nop 0
	v_add_f32_e32 v18, v18, v20
	v_add_f32_e32 v18, v18, v21
	s_nop 1
	v_add_f32_dpp v26, v18, v18 quad_perm:[1,0,3,2] row_mask:0xf bank_mask:0xf bound_ctrl:1
	v_add_f32_e32 v18, v14, v15
	v_add_f32_e32 v18, v16, v18
	v_add_f32_e32 v18, v17, v18
	s_nop 1
	v_add_f32_dpp v18, v18, v18 quad_perm:[1,0,3,2] row_mask:0xf bank_mask:0xf bound_ctrl:1
	s_nop 1
	v_add_f32_dpp v18, v18, v18 quad_perm:[2,3,0,1] row_mask:0xf bank_mask:0xf bound_ctrl:1
	s_nop 1
	v_add_f32_dpp v18, v18, v18 row_half_mirror row_mask:0xf bank_mask:0xf bound_ctrl:1
	s_nop 1
	v_add_f32_dpp v18, v18, v18 row_mirror row_mask:0xf bank_mask:0xf bound_ctrl:1
	v_fmamk_f32 v15, v18, 0xbc800000, v15
	v_fmamk_f32 v14, v18, 0xbc800000, v14
	v_fmamk_f32 v17, v18, 0xbc800000, v17
	v_fmac_f32_e32 v16, 0xbc800000, v18
	v_pk_mul_f32 v[20:21], v[14:15], v[14:15]
	v_pk_mul_f32 v[18:19], v[16:17], v[16:17]
	v_add_f32_e32 v20, v20, v21
	v_add_f32_e32 v18, v18, v20
	v_add_f32_e32 v18, v19, v18
	v_add_f32_dpp v19, v26, v26 quad_perm:[2,3,0,1] row_mask:0xf bank_mask:0xf bound_ctrl:1
	s_nop 0
	v_add_f32_dpp v18, v18, v18 quad_perm:[1,0,3,2] row_mask:0xf bank_mask:0xf bound_ctrl:1
	v_add_f32_dpp v19, v19, v19 row_half_mirror row_mask:0xf bank_mask:0xf bound_ctrl:1
	s_nop 0
	v_add_f32_dpp v18, v18, v18 quad_perm:[2,3,0,1] row_mask:0xf bank_mask:0xf bound_ctrl:1
	v_add_f32_dpp v20, v19, v19 row_mirror row_mask:0xf bank_mask:0xf bound_ctrl:1
	s_nop 0
	v_add_f32_dpp v18, v18, v18 row_half_mirror row_mask:0xf bank_mask:0xf bound_ctrl:1
	s_nop 1
	v_add_f32_dpp v18, v18, v18 row_mirror row_mask:0xf bank_mask:0xf bound_ctrl:1
	v_fmamk_f32 v18, v18, 0x3c800000, v193
	v_rsq_f32_e32 v18, v18
	s_nop 0
	v_pk_mul_f32 v[14:15], v[14:15], v[18:19] op_sel_hi:[1,0]
	v_pk_mul_f32 v[16:17], v[16:17], v[18:19] op_sel_hi:[1,0]
	v_pk_fma_f32 v[14:15], v[2:3], v[14:15], v[6:7]
	v_pk_fma_f32 v[16:17], v[4:5], v[16:17], v[8:9]
	v_pk_fma_f32 v[14:15], v[20:21], v[22:23], v[14:15] op_sel_hi:[0,1,1]
	v_pk_fma_f32 v[16:17], v[20:21], v[24:25], v[16:17] op_sel_hi:[0,1,1]
	s_waitcnt vmcnt(1)
	v_lshlrev_b32_e32 v18, 16, v174
	v_and_b32_e32 v19, 0xffff0000, v174
	v_lshlrev_b32_e32 v20, 16, v175
	v_and_b32_e32 v21, 0xffff0000, v175
	v_pk_mul_f32 v[16:17], v[16:17], v[20:21]
	v_pk_mul_f32 v[14:15], v[14:15], v[18:19]
	s_nop 0
	v_cvt_pk_bf16_f32 v14, v14, v15
	v_cvt_pk_bf16_f32 v15, v16, v17
	v_lshl_or_b32 v16, s5, 4, v176
	v_or_b32_e32 v16, s6, v16
	v_mov_b32_e32 v17, s7
	v_lshlrev_b64 v[16:17], 12, v[16:17]
	v_lshl_add_u64 v[16:17], v[168:169], 0, v[16:17]
	global_store_dwordx2 v[16:17], v[14:15], off
	s_waitcnt lgkmcnt(0)
	s_and_saveexec_b64 s[12:13], s[2:3]
	v_mov_b32_e32 v14, s34
	v_mov_b32_e32 v15, 1
	ds_add_u32 v14, v15
	v_mov_b32_e32 v14, s31
	ds_add_u32 v14, v15

.LBB0_653:
	s_lshl_b32 s8, s16, 4
	v_lshl_add_u64 v[14:15], v[166:167], 0, s[8:9]
	v_mov_b64_e32 v[16:17], s[66:67]
	v_mad_u64_u32 v[16:17], s[14:15], v14, s36, v[16:17]
	v_mov_b32_e32 v14, v17
	v_mad_u64_u32 v[14:15], s[14:15], v15, s36, v[14:15]
	v_mov_b32_e32 v17, v14
	s_mov_b32 s5, s9
	v_lshl_add_u64 v[14:15], v[16:17], 0, s[4:5]
	v_lshl_add_u64 v[14:15], v[14:15], 0, v[162:163]
	v_add_co_u32_e32 v14, vcc, s37, v14
	v_cvt_pk_bf16_f32 v198, v106, v107
	s_nop 0
	v_addc_co_u32_e32 v15, vcc, 0, v15, vcc
	global_load_dwordx2 v[174:175], v[14:15], off
	v_cvt_pk_bf16_f32 v199, v108, v109
	v_cvt_pk_bf16_f32 v200, v110, v111
	v_cvt_pk_bf16_f32 v201, v112, v113
	v_cvt_pk_bf16_f32 v158, v114, v115
	v_cvt_pk_bf16_f32 v159, v116, v117
	v_mfma_f32_16x16x32_bf16 v[42:45], v[154:157], v[198:201], 0
	v_cvt_pk_bf16_f32 v160, v118, v119
	v_cvt_pk_bf16_f32 v161, v120, v121
	v_mov_b32_e32 v82, v84
	v_mov_b32_e32 v83, v85
	v_mfma_f32_16x16x32_bf16 v[42:45], v[146:149], v[158:161], v[42:45]
	s_lshl_b32 s5, s16, 14
	s_and_b32 s5, s5, 0x8000
	s_add_i32 s8, s5, 0
	v_mfma_f32_16x16x32_bf16 v[42:45], v[150:153], v[82:85], v[42:45]
	v_add_u32_e32 v14, s8, v184
	v_add_u32_e32 v18, s8, v185
	v_add_u32_e32 v22, s8, v187
	v_add3_u32 v32, s8, v188, v183
	v_add_u32_e32 v146, s8, v186
	s_nop 2
	v_cvt_pk_bf16_f32 v42, v42, v43
	v_cvt_pk_bf16_f32 v43, v44, v45
	v_mov_b32_e32 v44, v163
	v_mov_b32_e32 v45, v163
	ds_read_b128 v[70:73], v14
	ds_read_b128 v[62:65], v14 offset:64
	ds_read_b128 v[58:61], v14 offset:2048
	ds_read_b128 v[14:17], v14 offset:2112
	ds_read_b128 v[74:77], v18 offset:4096
	ds_read_b128 v[66:69], v18 offset:5120
	ds_read_b128 v[38:41], v18 offset:6144
	ds_read_b128 v[34:37], v18 offset:7168
	ds_read_b128 v[26:29], v22 offset:8192
	ds_read_b128 v[18:21], v22 offset:9216
	ds_read_b128 v[22:25], v22 offset:10240
	ds_read_b64 v[32:33], v32 offset:11264
	v_mfma_f32_16x16x32_bf16 v[142:145], v[142:145], v[42:45], 0
	ds_read_b128 v[54:57], v146 offset:13312
	ds_read_b128 v[46:49], v146 offset:13376
	ds_read_b128 v[50:53], v146 offset:13440
	ds_read_b128 v[42:45], v146 offset:13504
	s_mov_b32 s5, 0
	v_mfma_f32_16x16x32_bf16 v[138:141], v[138:141], v[198:201], 0
	s_cmp_lt_u32 s43, s99
	s_cbranch_scc1 .Lscan_y2_skip
	s_branch .LBB0_655

; __global__ void __launch_bounds__(NTHR, 2) mk_fwd(Args args) {
;     ...
;                 CK_POST(B, NCHUNK - 1);
.LBB0_664:
	s_add_i32 s5, 0, 0x23000
	v_add3_u32 v14, s5, v30, v182
	s_add_i32 s5, 0, 0xec00
	v_add3_u32 v25, s5, v181, v31
	ds_read_u16 v18, v25
	ds_read_u16 v19, v25 offset:32
	ds_read_u16 v20, v25 offset:64
	ds_read_b128 v[14:17], v14
	s_add_i32 s6, s35, 0
	s_waitcnt lgkmcnt(3)
	v_lshlrev_b32_e32 v22, 16, v18
	v_add_u32_e32 v18, 0, v180
	v_add_u32_e32 v1, 0, v1
	v_add_u32_e32 v26, 0xc800, v18
	s_add_i32 s6, s6, 0xdc00
	v_add_u32_e32 v1, 0xf400, v1
	s_waitcnt lgkmcnt(2)
	v_lshlrev_b32_e32 v23, 16, v19
	s_waitcnt lgkmcnt(1)
	v_lshlrev_b32_e32 v24, 16, v20
	v_add3_u32 v28, s6, v178, v179
	ds_read_b128 v[18:21], v1
	ds_read_u16 v1, v25 offset:96
	ds_read_b64 v[26:27], v26
	ds_read_u16 v30, v28 offset:8
	ds_read_u16 v31, v28 offset:72
	ds_read_u16 v32, v28 offset:136
	ds_read_u16 v33, v28 offset:200
	s_waitcnt lgkmcnt(6)
	v_rcp_f32_e32 v18, v18
	v_rcp_f32_e32 v19, v19
	s_waitcnt lgkmcnt(4)
	v_lshlrev_b32_e32 v28, 16, v26
	v_and_b32_e32 v29, 0xffff0000, v26
	s_waitcnt lgkmcnt(2)
	v_lshlrev_b32_e32 v31, 16, v31
	v_lshlrev_b32_e32 v30, 16, v30
	v_pk_mul_f32 v[28:29], v[28:29], v[30:31]
	v_lshlrev_b32_e32 v25, 16, v1
	v_pk_mul_f32 v[10:11], v[10:11], v[28:29]
	s_waitcnt lgkmcnt(1)
	v_lshlrev_b32_e32 v26, 16, v32
	v_pk_mul_f32 v[10:11], v[18:19], v[10:11]
	v_rcp_f32_e32 v18, v20
	v_add_f32_e32 v1, v10, v11
	v_add_f32_e32 v10, v14, v15
	v_rcp_f32_e32 v19, v21
	v_add_f32_e32 v10, v16, v10
	v_lshlrev_b32_e32 v20, 16, v27
	v_and_b32_e32 v21, 0xffff0000, v27
	s_waitcnt lgkmcnt(0)
	v_lshlrev_b32_e32 v27, 16, v33
	v_add_f32_e32 v10, v17, v10
	v_pk_mul_f32 v[20:21], v[20:21], v[26:27]
	v_or_b32_e32 v164, 0xff0000, v164
	v_add_f32_dpp v10, v10, v10 quad_perm:[1,0,3,2] row_mask:0xf bank_mask:0xf bound_ctrl:1
	v_pk_mul_f32 v[12:13], v[12:13], v[20:21]
	s_mov_b32 s5, 0
	v_add_f32_dpp v10, v10, v10 quad_perm:[2,3,0,1] row_mask:0xf bank_mask:0xf bound_ctrl:1
	v_pk_mul_f32 v[12:13], v[18:19], v[12:13]
	v_mov_b32_e32 v163, 0
	v_add_f32_dpp v10, v10, v10 row_half_mirror row_mask:0xf bank_mask:0xf bound_ctrl:1
	v_add_f32_e32 v1, v1, v12
	v_add_f32_e32 v1, v1, v13
	v_add_f32_dpp v12, v10, v10 row_mirror row_mask:0xf bank_mask:0xf bound_ctrl:1
	v_fmamk_f32 v11, v12, 0xbc800000, v15
	v_fmamk_f32 v10, v12, 0xbc800000, v14
	v_fmamk_f32 v17, v12, 0xbc800000, v17
	v_fmac_f32_e32 v16, 0xbc800000, v12
	v_pk_mul_f32 v[14:15], v[10:11], v[10:11]
	v_pk_mul_f32 v[12:13], v[16:17], v[16:17]
	v_add_f32_e32 v14, v14, v15
	v_add_f32_e32 v12, v12, v14
	v_add_f32_e32 v12, v13, v12
	v_mov_b32_e32 v13, 0x3a27c5ac
	v_add_f32_dpp v1, v1, v1 quad_perm:[1,0,3,2] row_mask:0xf bank_mask:0xf bound_ctrl:1
	v_add_f32_dpp v12, v12, v12 quad_perm:[1,0,3,2] row_mask:0xf bank_mask:0xf bound_ctrl:1
	s_nop 0
	v_add_f32_dpp v1, v1, v1 quad_perm:[2,3,0,1] row_mask:0xf bank_mask:0xf bound_ctrl:1
	v_add_f32_dpp v12, v12, v12 quad_perm:[2,3,0,1] row_mask:0xf bank_mask:0xf bound_ctrl:1
	s_nop 0
	v_add_f32_dpp v1, v1, v1 row_half_mirror row_mask:0xf bank_mask:0xf bound_ctrl:1
	v_add_f32_dpp v12, v12, v12 row_half_mirror row_mask:0xf bank_mask:0xf bound_ctrl:1
	s_nop 0
	v_add_f32_dpp v14, v1, v1 row_mirror row_mask:0xf bank_mask:0xf bound_ctrl:1
	v_add_f32_dpp v12, v12, v12 row_mirror row_mask:0xf bank_mask:0xf bound_ctrl:1
	v_fmac_f32_e32 v13, 0x3c800000, v12
	v_rsq_f32_e32 v12, v13
	s_nop 0
	v_pk_mul_f32 v[10:11], v[10:11], v[12:13] op_sel_hi:[1,0]
	v_pk_mul_f32 v[12:13], v[16:17], v[12:13] op_sel_hi:[1,0]
	v_pk_fma_f32 v[2:3], v[2:3], v[10:11], v[6:7]
	v_pk_fma_f32 v[4:5], v[4:5], v[12:13], v[8:9]
	v_pk_fma_f32 v[2:3], v[14:15], v[22:23], v[2:3] op_sel_hi:[0,1,1]
	v_pk_fma_f32 v[4:5], v[14:15], v[24:25], v[4:5] op_sel_hi:[0,1,1]
	s_waitcnt vmcnt(2)
	v_lshlrev_b32_e32 v6, 16, v172
	v_and_b32_e32 v7, 0xffff0000, v172
	v_lshlrev_b32_e32 v8, 16, v173
	v_and_b32_e32 v9, 0xffff0000, v173
	v_pk_mul_f32 v[4:5], v[4:5], v[8:9]
	v_pk_mul_f32 v[2:3], v[2:3], v[6:7]
	s_nop 0
	v_cvt_pk_bf16_f32 v2, v2, v3
	v_cvt_pk_bf16_f32 v3, v4, v5
	v_lshl_add_u64 v[4:5], s[62:63], 0, v[164:165]
	v_lshl_add_u64 v[4:5], v[4:5], 0, s[4:5]
	v_lshl_add_u64 v[4:5], v[4:5], 0, v[162:163]
	global_store_dwordx2 v[4:5], v[2:3], off
	s_waitcnt lgkmcnt(0)
	s_and_saveexec_b64 s[4:5], s[2:3]
	s_cbranch_execz .LBB0_669
	s_mov_b64 s[6:7], exec
	v_mbcnt_lo_u32_b32 v1, s6, 0
	v_mbcnt_hi_u32_b32 v1, s7, v1
	v_cmp_eq_u32_e32 vcc, 0, v1
	s_and_saveexec_b64 s[2:3], vcc
	s_bcnt1_i32_b64 s6, s[6:7]
	v_mov_b32_e32 v1, s34
	v_mov_b32_e32 v2, s6
	ds_add_u32 v1, v2
	s_or_b64 exec, exec, s[2:3]
	s_mov_b64 s[2:3], exec
	v_mbcnt_lo_u32_b32 v1, s2, 0
	v_mbcnt_hi_u32_b32 v1, s3, v1
	v_cmp_eq_u32_e32 vcc, 0, v1
	s_and_b64 s[6:7], exec, vcc
	s_mov_b64 exec, s[6:7]
	s_bcnt1_i32_b64 s2, s[2:3]
	v_mov_b32_e32 v1, s31
	v_mov_b32_e32 v2, s2
	ds_add_u32 v1, v2

; #define LAS __attribute__((address_space(3)))
; __global__ void __launch_bounds__(NTHR, 2) mk_fwd(Args args) {
;     ...
;                 const int j = lane;
;                 LAS bf16* IMG = (LAS bf16*)(lds + wave * 13312);
;                 LAS bf16* QGT = (LAS bf16*)(lds + wave * 13312 + 10240);
;                 for (int i = lane; i < 768; i += 64) ((LAS unsigned*)QGT)[i] = 0u;
;                 const int pos = (j & 32) | ((j & 12) << 1) | ((j & 16) >> 2) | (j & 3);
;                 bf16 nr_[17], nk_[17], nv_[17], nwl_[16], nal_[16]; float ncst_[7];
;     ...
;                 if (gw < 64 * NCHUNK) P4_FETCH(gw);
.Lprod_code:
	v_readlane_b32 s0, v252, 43
	s_nop 3
	s_sub_i32 s0, s0, 4
	s_mulk_i32 s0, 0x3400
	s_add_i32 s4, s0, 0x10000
	s_mov_b32 s77, 0
	s_cmpk_gt_i32 s30, 0x3fff
	v_lshl_add_u32 v125, v194, 2, s4
	v_mov_b32_e32 v7, 0
	ds_write2st64_b32 v125, v7, v7 offset0:40 offset1:41
	ds_write2st64_b32 v125, v7, v7 offset0:42 offset1:43
	ds_write2st64_b32 v125, v7, v7 offset0:44 offset1:45
	ds_write2st64_b32 v125, v7, v7 offset0:46 offset1:47
	ds_write2st64_b32 v125, v7, v7 offset0:48 offset1:49
	ds_write2st64_b32 v125, v7, v7 offset0:50 offset1:51
	s_cbranch_scc1 .Lprod_exit
	v_writelane_b32 v252, s2, 52
	s_ashr_i32 s0, s30, 12
	s_lshl_b32 s5, s30, 6
	v_writelane_b32 v252, s3, 53
	s_bfe_u32 s2, s30, 0x80004
	s_ashr_i32 s1, s0, 31
	s_lshl_b32 s3, s2, 4
	s_and_b32 s5, s5, 0x3c0
	s_add_u32 s29, s26, 0x21c08000
	s_addc_u32 s31, s27, 0
	s_lshl_b32 s8, s5, 1
	s_add_u32 s6, s66, s8
	s_addc_u32 s7, s67, 0
	s_add_u32 s8, s10, s8
	s_addc_u32 s9, s11, 0
	s_lshl_b64 s[12:13], s[0:1], 12
	v_lshlrev_b32_e32 v1, 1, v0
	v_lshrrev_b32_e32 v2, 2, v0
	s_or_b32 s0, s12, s3
	v_and_b32_e32 v92, 15, v0
	v_and_b32_e32 v1, 24, v1
	v_and_b32_e32 v2, 4, v2
	v_and_b32_e32 v4, 3, v0
	v_and_b32_e32 v3, 35, v0
	s_add_u32 s1, s0, -1
	v_lshlrev_b32_e32 v5, 3, v0
	v_or3_b32 v101, v3, v2, v1
	s_addc_u32 s14, s13, -1
	v_and_b32_e32 v97, 56, v5
	v_mul_u32_u24_e32 v5, 0x48, v92
	v_lshlrev_b32_e32 v1, 1, v1
	v_lshlrev_b32_e32 v4, 1, v4
	s_cmp_eq_u32 s2, 0
	v_lshlrev_b32_e32 v5, 1, v5
	v_add3_u32 v1, s4, v1, v4
	v_lshlrev_b32_e32 v18, 1, v194
	v_mov_b32_e32 v19, v7
	v_and_b32_e32 v4, 48, v194
	v_lshl_add_u64 v[14:15], s[10:11], 0, v[18:19]
	v_lshl_add_u64 v[16:17], s[66:67], 0, v[18:19]
	v_add3_u32 v98, s4, v5, v4
	v_lshl_add_u64 v[4:5], s[6:7], 0, v[18:19]
	v_lshl_add_u64 v[18:19], s[8:9], 0, v[18:19]
	s_cselect_b32 s1, s12, s1
	s_cselect_b32 s6, s13, s14
	v_mov_b32_e32 v99, 0x2400
	s_mul_i32 s8, s6, 0x2400
	v_mad_u64_u32 v[22:23], s[6:7], s1, v99, v[18:19]
	v_add_u32_e32 v23, s8, v23
	s_movk_i32 s36, 0x1000
	global_load_ushort v24, v[22:23], off
	global_load_ushort v21, v[22:23], off offset:2048
	v_add_co_u32_e32 v22, vcc, s36, v22
	v_mad_i64_i32 v[18:19], s[6:7], s0, v99, v[18:19]
	s_nop 0
	v_addc_co_u32_e32 v23, vcc, 0, v23, vcc
	v_add_co_u32_e32 v26, vcc, s36, v18
	s_movk_i32 s37, 0x2000
	s_nop 0
	v_addc_co_u32_e32 v27, vcc, 0, v19, vcc
	global_load_ushort v20, v[22:23], off
	global_load_ushort v25, v[18:19], off
	s_nop 0
	global_load_ushort v22, v[18:19], off offset:2048
	global_load_ushort v23, v[26:27], off
	s_mov_b64 s[6:7], 0x2400
	v_add_co_u32_e32 v26, vcc, s37, v18
	v_lshl_add_u64 v[28:29], v[18:19], 0, s[6:7]
	s_nop 0
	v_addc_co_u32_e32 v27, vcc, 0, v19, vcc
	s_movk_i32 s38, 0x3000
	global_load_ushort v27, v[26:27], off offset:1024
	s_nop 0
	global_load_ushort v26, v[28:29], off offset:2048
	v_add_co_u32_e32 v28, vcc, s38, v18
	s_movk_i32 s8, 0x4000
	s_nop 0
	v_addc_co_u32_e32 v29, vcc, 0, v19, vcc
	global_load_ushort v96, v[28:29], off offset:1024
	v_add_co_u32_e32 v28, vcc, s8, v18
	s_movk_i32 s1, 0x5000
	s_nop 0
	v_addc_co_u32_e32 v29, vcc, 0, v19, vcc
	s_mov_b64 s[6:7], 0x4800
	v_add_co_u32_e32 v32, vcc, s1, v18
	v_lshl_add_u64 v[30:31], v[18:19], 0, s[6:7]
	s_nop 0
	v_addc_co_u32_e32 v33, vcc, 0, v19, vcc
	s_movk_i32 s9, 0x6000
	global_load_ushort v29, v[28:29], off offset:2048
	s_nop 0
	global_load_ushort v30, v[30:31], off offset:2048
	s_mov_b64 s[10:11], 0x6c00
	global_load_ushort v121, v[32:33], off offset:2048
	v_add_co_u32_e32 v32, vcc, s9, v18
	v_lshl_add_u64 v[34:35], v[18:19], 0, s[10:11]
	s_nop 0
	v_addc_co_u32_e32 v33, vcc, 0, v19, vcc
	s_movk_i32 s42, 0x7000
	global_load_ushort v32, v[32:33], off offset:3072
	s_nop 0
	global_load_ushort v31, v[34:35], off offset:2048
	v_add_co_u32_e32 v34, vcc, s42, v18
	s_mov_b32 s44, 0xa000
	s_nop 0
	v_addc_co_u32_e32 v35, vcc, 0, v19, vcc
	s_mov_b64 s[10:11], 0x9000
	v_add_co_u32_e32 v36, vcc, s44, v18
	global_load_ushort v122, v[34:35], off offset:3072
	v_lshl_add_u64 v[34:35], v[18:19], 0, s[10:11]
	v_addc_co_u32_e32 v37, vcc, 0, v19, vcc
	s_mov_b32 s1, 0xb000
	global_load_ushort v33, v[36:37], off offset:-4096
	s_nop 0
	global_load_ushort v34, v[34:35], off offset:2048
	s_nop 0
	global_load_ushort v123, v[36:37], off
	s_mov_b64 s[14:15], 0xb400
	v_add_co_u32_e32 v36, vcc, s1, v18
	v_lshl_add_u64 v[38:39], v[18:19], 0, s[14:15]
	s_nop 0
	v_addc_co_u32_e32 v37, vcc, 0, v19, vcc
	s_mov_b32 s39, 0xc000
	global_load_ushort v36, v[36:37], off offset:1024
	s_nop 0
	global_load_ushort v35, v[38:39], off offset:2048
	v_add_co_u32_e32 v38, vcc, s39, v18
	s_mov_b32 s41, 0xd000
	s_nop 0
	v_addc_co_u32_e32 v39, vcc, 0, v19, vcc
	global_load_ushort v124, v[38:39], off offset:1024
	s_mov_b64 s[14:15], 0xd800
	v_add_co_u32_e32 v38, vcc, s41, v18
	v_lshl_add_u64 v[40:41], v[18:19], 0, s[14:15]
	s_nop 0
	v_addc_co_u32_e32 v39, vcc, 0, v19, vcc
	s_mov_b32 s1, 0xe000
	global_load_ushort v38, v[38:39], off offset:2048
	s_nop 0
	global_load_ushort v37, v[40:41], off offset:2048
	v_add_co_u32_e32 v40, vcc, s1, v18
	s_mov_b32 s49, 0xf000
	s_nop 0
	v_addc_co_u32_e32 v41, vcc, 0, v19, vcc
	s_mov_b64 s[16:17], 0xfc00
	v_add_co_u32_e32 v42, vcc, s49, v18
	global_load_ushort v127, v[40:41], off offset:2048
	v_lshl_add_u64 v[40:41], v[18:19], 0, s[16:17]
	v_addc_co_u32_e32 v43, vcc, 0, v19, vcc
	s_mov_b32 s50, 0x10000
	global_load_ushort v43, v[42:43], off offset:3072
	s_nop 0
	global_load_ushort v39, v[40:41], off offset:2048
	v_add_co_u32_e32 v40, vcc, s50, v18
	s_mov_b32 s73, 0x13000
	s_nop 0
	v_addc_co_u32_e32 v41, vcc, 0, v19, vcc
	s_mov_b64 s[46:47], 0x12000
	v_add_co_u32_e32 v46, vcc, s73, v18
	global_load_ushort v128, v[40:41], off offset:3072
	v_lshl_add_u64 v[40:41], v[18:19], 0, s[46:47]
	v_addc_co_u32_e32 v47, vcc, 0, v19, vcc
	s_mov_b32 s1, 0x14000
	global_load_ushort v45, v[46:47], off offset:-4096
	global_load_ushort v44, v[40:41], off offset:2048
	s_nop 0
	global_load_ushort v41, v[46:47], off
	s_mov_b64 s[16:17], 0x14400
	v_add_co_u32_e32 v46, vcc, s1, v18
	v_lshl_add_u64 v[48:49], v[18:19], 0, s[16:17]
	s_nop 0
	v_addc_co_u32_e32 v47, vcc, 0, v19, vcc
	s_mov_b32 s78, 0x15000
	global_load_ushort v47, v[46:47], off offset:1024
	s_nop 0
	global_load_ushort v46, v[48:49], off offset:2048
	v_add_co_u32_e32 v48, vcc, s78, v18
	s_mov_b32 s72, 0x16000
	s_nop 0
	v_addc_co_u32_e32 v49, vcc, 0, v19, vcc
	global_load_ushort v129, v[48:49], off offset:1024
	s_mov_b64 s[16:17], 0x16800
	v_add_co_u32_e32 v48, vcc, s72, v18
	v_lshl_add_u64 v[50:51], v[18:19], 0, s[16:17]
	s_nop 0
	v_addc_co_u32_e32 v49, vcc, 0, v19, vcc
	s_mov_b32 s1, 0x17000
	global_load_ushort v49, v[48:49], off offset:2048
	s_nop 0
	global_load_ushort v48, v[50:51], off offset:2048
	v_add_co_u32_e32 v50, vcc, s1, v18
	s_mov_b32 s1, 0x18000
	s_nop 0
	v_addc_co_u32_e32 v51, vcc, 0, v19, vcc
	global_load_ushort v130, v[50:51], off offset:2048
	s_mov_b64 s[34:35], 0x18c00
	v_add_co_u32_e32 v50, vcc, s1, v18
	v_lshl_add_u64 v[52:53], v[18:19], 0, s[34:35]
	s_nop 0
	v_addc_co_u32_e32 v51, vcc, 0, v19, vcc
	s_mov_b32 s1, 0x19000
	global_load_ushort v51, v[50:51], off offset:3072
	s_nop 0
	global_load_ushort v50, v[52:53], off offset:2048
	v_add_co_u32_e32 v52, vcc, s1, v18
	s_mov_b32 s1, 0x1c000
	s_nop 0
	v_addc_co_u32_e32 v53, vcc, 0, v19, vcc
	s_mov_b64 s[34:35], 0x1b000
	v_add_co_u32_e32 v56, vcc, s1, v18
	v_lshl_add_u64 v[54:55], v[18:19], 0, s[34:35]
	s_nop 0
	v_addc_co_u32_e32 v57, vcc, 0, v19, vcc
	s_mov_b32 s1, 0x1d000
	global_load_ushort v133, v[52:53], off offset:3072
	s_nop 0
	global_load_ushort v53, v[56:57], off offset:-4096
	global_load_ushort v52, v[54:55], off offset:2048
	global_load_ushort v134, v[56:57], off
	s_mov_b64 s[34:35], 0x1d400
	v_add_co_u32_e32 v54, vcc, s1, v18
	v_lshl_add_u64 v[56:57], v[18:19], 0, s[34:35]
	s_nop 0
	v_addc_co_u32_e32 v55, vcc, 0, v19, vcc
	s_mov_b32 s1, 0x1e000
	global_load_ushort v55, v[54:55], off offset:1024
	s_nop 0
	global_load_ushort v54, v[56:57], off offset:2048
	v_add_co_u32_e32 v56, vcc, s1, v18
	s_mov_b32 s1, 0x1f000
	s_nop 0
	v_addc_co_u32_e32 v57, vcc, 0, v19, vcc
	v_add_co_u32_e32 v58, vcc, s1, v18
	s_mov_b32 s1, 0x20000
	s_nop 0
	v_addc_co_u32_e32 v59, vcc, 0, v19, vcc
	v_add_co_u32_e32 v60, vcc, s1, v18
	s_mov_b32 s1, 0x21000
	s_nop 0
	v_addc_co_u32_e32 v61, vcc, 0, v19, vcc
	s_mov_b64 s[34:35], 0x1f800
	v_add_co_u32_e32 v62, vcc, s1, v18
	global_load_ushort v135, v[56:57], off offset:1024
	v_lshl_add_u64 v[56:57], v[18:19], 0, s[34:35]
	s_mov_b64 s[34:35], 0x21c00
	v_addc_co_u32_e32 v63, vcc, 0, v19, vcc
	s_mov_b32 s1, 0x22000
	global_load_ushort v59, v[58:59], off offset:2048
	s_nop 0
	global_load_ushort v56, v[56:57], off offset:2048
	v_mov_b32_e32 v100, 0x1800
	global_load_ushort v136, v[60:61], off offset:2048
	v_lshl_add_u64 v[60:61], v[18:19], 0, s[34:35]
	v_add_co_u32_e32 v18, vcc, s1, v18
	v_mad_i64_i32 v[4:5], s[0:1], s0, v100, v[4:5]
	s_nop 0
	v_addc_co_u32_e32 v19, vcc, 0, v19, vcc
	global_load_ushort v64, v[62:63], off offset:3072
	s_nop 0
	global_load_ushort v61, v[60:61], off offset:2048
	v_add_co_u32_e32 v62, vcc, s36, v4
	s_mov_b64 s[0:1], 0x1800
	s_nop 0
	v_addc_co_u32_e32 v63, vcc, 0, v5, vcc
	v_add_co_u32_e32 v66, vcc, s38, v4
	global_load_ushort v137, v[18:19], off offset:3072
	v_lshl_add_u64 v[18:19], v[4:5], 0, s[0:1]
	s_mov_b64 s[0:1], 0x3000
	v_addc_co_u32_e32 v67, vcc, 0, v5, vcc
	global_load_ushort v58, v[4:5], off
	global_load_ushort v57, v[4:5], off offset:2048
	s_nop 0
	global_load_ushort v62, v[62:63], off offset:2048
	s_nop 0
	global_load_ushort v60, v[18:19], off offset:2048
	v_lshl_add_u64 v[18:19], v[4:5], 0, s[0:1]
	global_load_ushort v65, v[66:67], off
	global_load_ushort v63, v[18:19], off offset:2048
	v_add_co_u32_e32 v66, vcc, s8, v4
	s_mov_b32 s12, 0x9000
	s_nop 0
	v_addc_co_u32_e32 v67, vcc, 0, v5, vcc
	v_add_co_u32_e32 v68, vcc, s9, v4
	v_lshl_add_u64 v[18:19], v[4:5], 0, s[6:7]
	s_nop 0
	v_addc_co_u32_e32 v69, vcc, 0, v5, vcc
	v_add_co_u32_e32 v70, vcc, s42, v4
	s_mov_b64 s[0:1], 0x6000
	s_nop 0
	v_addc_co_u32_e32 v71, vcc, 0, v5, vcc
	v_add_co_u32_e32 v72, vcc, s12, v4
	global_load_ushort v67, v[66:67], off offset:2048
	s_nop 0
	global_load_ushort v66, v[18:19], off offset:2048
	v_addc_co_u32_e32 v73, vcc, 0, v5, vcc
	v_add_co_u32_e32 v74, vcc, s44, v4
	v_lshl_add_u64 v[18:19], v[4:5], 0, s[0:1]
	s_nop 0
	v_addc_co_u32_e32 v75, vcc, 0, v5, vcc
	v_add_co_u32_e32 v76, vcc, s39, v4
	s_mov_b64 s[0:1], 0x7800
	s_nop 0
	v_addc_co_u32_e32 v77, vcc, 0, v5, vcc
	v_add_co_u32_e32 v78, vcc, s41, v4
	global_load_ushort v69, v[68:69], off
	s_nop 0
	global_load_ushort v68, v[18:19], off offset:2048
	v_addc_co_u32_e32 v79, vcc, 0, v5, vcc
	v_lshl_add_u64 v[18:19], v[4:5], 0, s[0:1]
	v_add_co_u32_e32 v80, vcc, s49, v4
	global_load_ushort v71, v[70:71], off offset:2048
	s_nop 0
	global_load_ushort v70, v[18:19], off offset:2048
	v_lshl_add_u64 v[18:19], v[4:5], 0, s[10:11]
	s_mov_b64 s[0:1], 0xa800
	v_addc_co_u32_e32 v81, vcc, 0, v5, vcc
	global_load_ushort v73, v[72:73], off
	s_nop 0
	global_load_ushort v72, v[18:19], off offset:2048
	v_lshl_add_u64 v[18:19], v[4:5], 0, s[0:1]
	s_mov_b64 s[0:1], 0xc000
	v_add_co_u32_e32 v82, vcc, s50, v4
	s_mov_b32 s13, 0x12000
	global_load_ushort v75, v[74:75], off offset:2048
	s_nop 0
	global_load_ushort v74, v[18:19], off offset:2048
	v_lshl_add_u64 v[18:19], v[4:5], 0, s[0:1]
; __device__ __forceinline__ unsigned f2bf(float f) { return cvt_pk_bf16_nat(f, 0.f) & 0xffffu; }
; __global__ void __launch_bounds__(NTHR, 2) mk_fwd(Args args) {
;     ...
;                 if (gw < 64 * NCHUNK) P4_FETCH(gw);
;     ...
;                     const int s_ = tr, rec = (s_ >> 2) * 8 + (s_ & 3);
; #pragma unroll
;                     for (int e = 0; e < 4; ++e) { const int t = 4 * q + e;
;                         const float qv = s_ < t ? QT[e] : 0.f, gb = s_ <= t ? GB[e] : 0.f, gk = s_ <= t ? GK[e] : 0.f;
;                         QGT[t * 32 + rec] = (bf16)f2bf(qv);
;                         QGT[512 + t * 32 + rec] = (bf16)f2bf(gb); QGT[512 + t * 32 + rec + 4] = (bf16)f2bf(gk); }
;                     float Tr[16]; const pg8::v4i_t PTi = __builtin_bit_cast(pg8::v4i_t, PT);
; #pragma unroll
;                     for (int t = 0; t < 16; ++t) { float acc = (t == s_) ? 1.f : 0.f;
	v_addc_co_u32_e32 v83, vcc, 0, v5, vcc
	global_load_ushort v77, v[76:77], off
	s_nop 0
	global_load_ushort v76, v[18:19], off offset:2048
	v_lshl_add_u64 v[18:19], v[4:5], 0, s[14:15]
	s_mov_b64 s[0:1], 0xf000
	v_add_co_u32_e32 v84, vcc, s13, v4
	global_load_ushort v79, v[78:79], off offset:2048
	s_nop 0
	global_load_ushort v78, v[18:19], off offset:2048
	v_lshl_add_u64 v[18:19], v[4:5], 0, s[0:1]
	s_mov_b64 s[0:1], 0x10800
	v_addc_co_u32_e32 v85, vcc, 0, v5, vcc
	global_load_ushort v81, v[80:81], off
	s_nop 0
	global_load_ushort v80, v[18:19], off offset:2048
	v_lshl_add_u64 v[18:19], v[4:5], 0, s[0:1]
	v_add_co_u32_e32 v86, vcc, s73, v4
	global_load_ushort v83, v[82:83], off offset:2048
	s_nop 0
	global_load_ushort v82, v[18:19], off offset:2048
	v_lshl_add_u64 v[18:19], v[4:5], 0, s[46:47]
	s_mov_b64 s[0:1], 0x13800
	v_addc_co_u32_e32 v87, vcc, 0, v5, vcc
	global_load_ushort v85, v[84:85], off
	s_nop 0
	global_load_ushort v84, v[18:19], off offset:2048
	v_lshl_add_u64 v[18:19], v[4:5], 0, s[0:1]
	s_mov_b64 s[0:1], 0x15000
	v_add_co_u32_e32 v88, vcc, s78, v4
	v_or_b32_e32 v2, s5, v194
	v_readlane_b32 s80, v252, 0
	global_load_ushort v87, v[86:87], off offset:2048
	s_nop 0
	global_load_ushort v86, v[18:19], off offset:2048
	v_lshl_add_u64 v[18:19], v[4:5], 0, s[0:1]
	v_addc_co_u32_e32 v89, vcc, 0, v5, vcc
	v_lshlrev_b32_e32 v6, 2, v2
	v_readlane_b32 s84, v252, 4
	v_readlane_b32 s85, v252, 5
	global_load_ushort v89, v[88:89], off
	s_nop 0
	global_load_ushort v88, v[18:19], off offset:2048
	v_lshl_add_u64 v[18:19], v[4:5], 0, s[16:17]
	v_add_co_u32_e32 v4, vcc, s72, v4
	v_lshl_add_u64 v[2:3], s[84:85], 0, v[6:7]
	s_nop 0
	v_addc_co_u32_e32 v5, vcc, 0, v5, vcc
	v_add_co_u32_e32 v2, vcc, s37, v2
	v_readlane_b32 s86, v252, 6
	s_nop 0
	v_addc_co_u32_e32 v3, vcc, 0, v3, vcc
	v_readlane_b32 s87, v252, 7
	v_readlane_b32 s90, v252, 10
	v_readlane_b32 s91, v252, 11
	global_load_ushort v91, v[4:5], off offset:2048
	global_load_ushort v90, v[18:19], off offset:2048
	global_load_dword v40, v6, s[84:85]
	global_load_dword v42, v[2:3], off offset:-4096
	s_nop 0
	global_load_dword v2, v[2:3], off
	s_nop 0
	global_load_dword v95, v6, s[86:87]
	global_load_dword v94, v6, s[90:91]
	global_load_dword v28, v6, s[52:53]
	global_load_dword v3, v6, s[54:55]
	s_movk_i32 s5, 0x48
	v_lshrrev_b32_e32 v4, 3, v194
	v_mad_u32_u24 v4, v4, s5, v97
	v_lshrrev_b32_e32 v93, 4, v194
	v_lshl_add_u32 v102, v4, 1, s4
	v_or_b32_e32 v4, 64, v194
	v_lshlrev_b32_e32 v104, 2, v93
	v_lshrrev_b32_e32 v5, 3, v4
	v_mad_u32_u24 v5, v5, s5, v97
	v_or_b32_e32 v6, 2, v104
	v_cmp_eq_u32_e32 vcc, 0, v92
	v_lshl_add_u32 v101, v101, 1, s4
	v_lshl_add_u32 v103, v5, 1, s4
	v_cmp_lt_u32_e64 s[4:5], v92, v104
	v_cmp_gt_u32_e64 s[6:7], v92, v104
	v_or_b32_e32 v5, 1, v104
	v_cmp_lt_u32_e64 s[10:11], v92, v6
	v_cmp_gt_u32_e64 s[12:13], v92, v6
	v_lshlrev_b32_e32 v131, 6, v6
	v_or_b32_e32 v6, 3, v104
	v_cndmask_b32_e64 v104, 0, 1.0, vcc
	v_cmp_eq_u32_e32 vcc, 1, v92
	v_cvt_pk_bf16_f32 v120, v104, s0
	v_readlane_b32 s0, v252, 40
	v_cndmask_b32_e64 v105, 0, 1.0, vcc
	v_cmp_eq_u32_e32 vcc, 2, v92
	s_lshl_b32 s0, s0, 3
	v_readlane_b32 s1, v252, 43
	v_cndmask_b32_e64 v106, 0, 1.0, vcc
	v_cmp_eq_u32_e32 vcc, 3, v92
	s_add_i32 s0, s1, s0
	s_mov_b32 s45, 0x5040100
	v_cndmask_b32_e64 v107, 0, 1.0, vcc
	v_cmp_eq_u32_e32 vcc, 4, v92
	s_add_i32 s34, s0, s28
	v_readlane_b32 s0, v252, 37
	v_cndmask_b32_e64 v108, 0, 1.0, vcc
	v_cmp_eq_u32_e32 vcc, 5, v92
	v_mul_u32_u24_e32 v126, 12, v194
	v_lshlrev_b32_e32 v18, 4, v4
	v_cndmask_b32_e64 v109, 0, 1.0, vcc
	v_cmp_eq_u32_e32 vcc, 6, v92
	v_lshlrev_b32_e32 v4, 8, v93
	v_cmp_gt_u32_e64 s[8:9], v92, v5
	v_cndmask_b32_e64 v110, 0, 1.0, vcc
	v_cmp_eq_u32_e32 vcc, 7, v92
	v_lshlrev_b32_e32 v5, 6, v5
	v_cmp_lt_u32_e64 s[14:15], v92, v6
	v_cndmask_b32_e64 v111, 0, 1.0, vcc
	v_cmp_eq_u32_e32 vcc, 8, v92
	v_cmp_gt_u32_e64 s[16:17], v92, v6
	v_lshlrev_b32_e32 v132, 6, v6
	v_cndmask_b32_e64 v112, 0, 1.0, vcc
	v_cmp_eq_u32_e32 vcc, 9, v92
	s_waitcnt vmcnt(0)
	v_perm_b32 v212, v127, v124, s45
	v_perm_b32 v213, v128, v127, s45
	v_cndmask_b32_e64 v113, 0, 1.0, vcc
	v_cmp_eq_u32_e32 vcc, 10, v92
	v_perm_b32 v214, v123, v122, s45
	v_perm_b32 v215, v121, v96, s45
	v_cndmask_b32_e64 v114, 0, 1.0, vcc
	v_cmp_eq_u32_e32 vcc, 11, v92
	v_perm_b32 v93, v137, v136, s45
	v_perm_b32 v96, v134, v133, s45
	v_cndmask_b32_e64 v115, 0, 1.0, vcc
	v_cmp_eq_u32_e32 vcc, 12, v92
	v_perm_b32 v97, v130, v129, s45
	s_add_i32 s34, s30, s28
	v_cndmask_b32_e64 v116, 0, 1.0, vcc
	v_cmp_eq_u32_e32 vcc, 13, v92
	v_lshlrev_b32_e32 v8, 6, v194
	v_lshlrev_b32_e32 v10, 5, v194
	v_cndmask_b32_e64 v117, 0, 1.0, vcc
	v_cmp_eq_u32_e32 vcc, 14, v92
	v_mov_b32_e32 v11, v7
	v_cmp_gt_u32_e64 s[2:3], 16, v194
	v_cndmask_b32_e64 v118, 0, 1.0, vcc
	v_cmp_eq_u32_e32 vcc, 15, v92
	v_perm_b32 v92, v136, v135, s45
	v_lshlrev_b32_e32 v12, 4, v194
	v_mov_b32_e32 v9, v7
	v_mov_b32_e32 v13, v7
	v_mov_b32_e32 v19, v7
	v_cndmask_b32_e64 v119, 0, 1.0, vcc
	s_lshl_b32 s48, s34, 6
	s_lshl_b32 s51, s28, 6
	s_mov_b32 s79, 0xbfb8aa3b
	v_lshlrev_b32_e32 v6, 2, v194
	v_add_u32_e32 v121, v1, v4
	v_add_u32_e32 v122, v1, v5
	v_add_u32_e32 v123, v1, v131
	v_add_u32_e32 v124, v1, v132
	v_add_u32_e32 v125, v125, v126
	s_mov_b32 s34, s30
	v_mov_b32_e32 v160, v57
	v_mov_b32_e32 v163, v60
	v_mov_b32_e32 v166, v63
	v_mov_b32_e32 v169, v66
	v_mov_b32_e32 v171, v68
	v_mov_b32_e32 v173, v70
	v_mov_b32_e32 v175, v72
	v_mov_b32_e32 v177, v74
	v_mov_b32_e32 v179, v76
	v_mov_b32_e32 v181, v78
	v_mov_b32_e32 v183, v80
	v_mov_b32_e32 v185, v82
	v_mov_b32_e32 v187, v84
	v_mov_b32_e32 v189, v86
; #define GAS __attribute__((address_space(1)))
; #define LAS __attribute__((address_space(3)))
; __global__ void __launch_bounds__(NTHR, 2) mk_fwd(Args args) {
;     ...
;                 for (int u = gw; u < 64 * NCHUNK; u += NGW) {
;                     const int h = u & 15, c = (u >> 4) & 255, b = u >> 12, hd = b * 16 + h;
;                     const float mu_r = ncst_[0], mu_k = ncst_[1], mu_v = ncst_[2], c_w0 = ncst_[3], c_a0 = ncst_[4], c_kk = ncst_[5], c_ka = ncst_[6];
;                     unsigned char* pk = ws + WS_R + ((size_t)hd * NCHUNK + c) * PK_BYTES;
;                     float At[16], Rt[16], Bt[16], Kt[16], Vt[16];
;                     float xr_[17], xk_[17], xv_[17], xwl_[16], xal_[16];
; #pragma unroll
;                     for (int t = 0; t < 17; ++t) { xr_[t] = __builtin_bit_cast(float, (unsigned)nr_[t] << 16); xk_[t] = __builtin_bit_cast(float, (unsigned)nk_[t] << 16); xv_[t] = __builtin_bit_cast(float, (unsigned)nv_[t] << 16); }
; #pragma unroll
;                     for (int t = 0; t < 16; ++t) { xwl_[t] = __builtin_bit_cast(float, (unsigned)nwl_[t] << 16); xal_[t] = __builtin_bit_cast(float, (unsigned)nal_[t] << 16); }
;                     if (c == 0) { xr_[0] = 0.f; xk_[0] = 0.f; xv_[0] = 0.f; }
;                     asm volatile("" ::: "memory");
;                     if (u + NGW < 64 * NCHUNK) P4_FETCH(u + NGW);
;     ...
;                     { const v4u q_ = *(const LAS v4u*)(QGT + lane * 8), g_ = *(const LAS v4u*)(QGT + 512 + lane * 8), t_ = *(const LAS v4u*)(QGT + 1024 + lane * 8);
;                       *(GAS v4u*)(pk + PK_QQ + lane * 16) = q_; *(GAS v4u*)(pk + PK_GG + lane * 16) = g_; *(GAS v4u*)(pk + PK_TT + lane * 16) = t_; }
;                     asm volatile("s_waitcnt lgkmcnt(0)" ::: "memory");
	v_mov_b32_e32 v191, v88
	v_mov_b32_e32 v193, v90
	v_mov_b32_e32 v162, v58
	v_mov_b32_e32 v165, v62
	v_mov_b32_e32 v168, v65
	v_mov_b32_e32 v170, v67
	v_mov_b32_e32 v172, v69
	v_mov_b32_e32 v174, v71
	v_mov_b32_e32 v176, v73
	v_mov_b32_e32 v178, v75
	v_mov_b32_e32 v180, v77
	v_mov_b32_e32 v182, v79
	v_mov_b32_e32 v184, v81
	v_mov_b32_e32 v186, v83
	v_mov_b32_e32 v188, v85
	v_mov_b32_e32 v190, v87
	v_mov_b32_e32 v192, v89
	v_mov_b32_e32 v196, v91
	v_mov_b32_e32 v127, v20
	v_mov_b32_e32 v130, v23
	v_mov_b32_e32 v146, v41
	v_mov_b32_e32 v126, v21
	v_mov_b32_e32 v129, v22
	v_mov_b32_e32 v132, v26
	v_mov_b32_e32 v134, v30
	v_mov_b32_e32 v136, v31
	v_mov_b32_e32 v138, v34
	v_mov_b32_e32 v140, v35
	v_mov_b32_e32 v142, v37
	v_mov_b32_e32 v144, v39
	v_mov_b32_e32 v147, v44
	v_mov_b32_e32 v149, v46
	v_mov_b32_e32 v151, v48
	v_mov_b32_e32 v153, v50
	v_mov_b32_e32 v155, v52
	v_mov_b32_e32 v157, v54
	v_mov_b32_e32 v159, v56
	v_mov_b32_e32 v164, v61
	v_mov_b32_e32 v128, v24
	v_mov_b32_e32 v131, v25
	v_mov_b32_e32 v133, v27
	v_mov_b32_e32 v135, v29
	v_mov_b32_e32 v137, v32
	v_mov_b32_e32 v139, v33
	v_mov_b32_e32 v141, v36
	v_mov_b32_e32 v143, v38
	v_mov_b32_e32 v145, v43
	v_mov_b32_e32 v148, v45
	v_mov_b32_e32 v150, v47
	v_mov_b32_e32 v152, v49
	v_mov_b32_e32 v154, v51
	v_mov_b32_e32 v156, v53
	v_mov_b32_e32 v158, v55
	v_mov_b32_e32 v161, v59
	v_mov_b32_e32 v167, v64
	v_mov_b32_e32 v197, v40
	v_mov_b32_e32 v198, v42
	v_mov_b32_e32 v200, v95
	v_mov_b32_e32 v201, v94
	v_mov_b32_e32 v202, v28
	v_mov_b32_e32 v203, v3
	v_mov_b32_e32 v204, v212
	v_mov_b32_e32 v205, v213
	v_mov_b32_e32 v206, v214
	v_mov_b32_e32 v207, v215
	v_mov_b32_e32 v208, v92
	v_mov_b32_e32 v209, v93
	v_mov_b32_e32 v210, v96
	v_mov_b32_e32 v211, v97
	v_readlane_b32 s81, v252, 1
	v_readlane_b32 s82, v252, 2
	v_readlane_b32 s83, v252, 3
	v_readlane_b32 s88, v252, 8
	v_readlane_b32 s89, v252, 9
	v_readlane_b32 s92, v252, 12
	v_readlane_b32 s93, v252, 13
	v_readlane_b32 s94, v252, 14
	v_readlane_b32 s95, v252, 15
	s_branch .Lpr_476
.Lpr_475:
	s_or_b64 exec, exec, s[34:35]
	s_waitcnt lgkmcnt(0)
	ds_read_b128 v[2:5], v125 offset:10240
	ds_read_b128 v[22:25], v125 offset:11264
	ds_read_b128 v[26:29], v125 offset:12288
	v_add_co_u32_e32 v20, vcc, 0x1000, v20
	s_add_i32 s48, s48, s51
	s_nop 0
	v_addc_co_u32_e32 v21, vcc, 0, v21, vcc
	s_waitcnt lgkmcnt(2)
	ds_write_b128 v20, v[2:5]
	s_waitcnt lgkmcnt(1)
	ds_write_b128 v20, v[22:25] offset:2048
	s_waitcnt lgkmcnt(0)
	ds_write_b128 v20, v[26:29] offset:1024
	s_waitcnt lgkmcnt(0)
	v_mov_b32_e32 v2, s98
	v_and_b32_e32 v3, 15, v2
	v_lshrrev_b32_e32 v3, 2, v3
	v_sub_u32_e32 v3, 4, v3
	v_cndmask_b32_e64 v3, 4, v3, s[68:69]
	v_cmp_eq_u32_e32 vcc, 0, v194
	s_nop 1
	v_cndmask_b32_e32 v3, 0, v3, vcc
	ds_add_u32 v2, v3
	s_waitcnt vmcnt(0)
	s_andn2_b64 vcc, exec, s[68:69]
	s_waitcnt vmcnt(51)
	v_mov_b32_e32 v57, v160
	s_waitcnt vmcnt(49)
	v_mov_b32_e32 v60, v163
	s_waitcnt vmcnt(47)
	v_mov_b32_e32 v63, v166
	s_waitcnt vmcnt(45)
	v_mov_b32_e32 v66, v169
	s_waitcnt vmcnt(43)
	v_mov_b32_e32 v68, v171
	s_waitcnt vmcnt(41)
	v_mov_b32_e32 v70, v173
	s_waitcnt vmcnt(39)
	v_mov_b32_e32 v72, v175
	s_waitcnt vmcnt(37)
	v_mov_b32_e32 v74, v177
	s_waitcnt vmcnt(35)
	v_mov_b32_e32 v76, v179
	s_waitcnt vmcnt(33)
	v_mov_b32_e32 v78, v181
	s_waitcnt vmcnt(31)
	v_mov_b32_e32 v80, v183
	s_waitcnt vmcnt(29)
	v_mov_b32_e32 v82, v185
	s_waitcnt vmcnt(27)
	v_mov_b32_e32 v84, v187
	s_waitcnt vmcnt(25)
	v_mov_b32_e32 v86, v189
	s_waitcnt vmcnt(23)
	v_mov_b32_e32 v88, v191
	s_waitcnt vmcnt(21)
	v_mov_b32_e32 v90, v193
	v_mov_b32_e32 v58, v162
	v_mov_b32_e32 v62, v165
	v_mov_b32_e32 v65, v168
	v_mov_b32_e32 v67, v170
	v_mov_b32_e32 v69, v172
	v_mov_b32_e32 v71, v174
	v_mov_b32_e32 v73, v176
	v_mov_b32_e32 v75, v178
	v_mov_b32_e32 v77, v180
	v_mov_b32_e32 v79, v182
	v_mov_b32_e32 v81, v184
	v_mov_b32_e32 v83, v186
	v_mov_b32_e32 v85, v188
	v_mov_b32_e32 v87, v190
	v_mov_b32_e32 v89, v192
	v_mov_b32_e32 v91, v196
	v_mov_b32_e32 v20, v127
	v_mov_b32_e32 v23, v130
	v_mov_b32_e32 v41, v146
	v_mov_b32_e32 v21, v126
	v_mov_b32_e32 v22, v129
	v_mov_b32_e32 v26, v132
	v_mov_b32_e32 v30, v134
	v_mov_b32_e32 v31, v136
	v_mov_b32_e32 v34, v138
	v_mov_b32_e32 v35, v140
	v_mov_b32_e32 v37, v142
	v_mov_b32_e32 v39, v144
	v_mov_b32_e32 v44, v147
	v_mov_b32_e32 v46, v149
	v_mov_b32_e32 v48, v151
	v_mov_b32_e32 v50, v153
	v_mov_b32_e32 v52, v155
	v_mov_b32_e32 v54, v157
	v_mov_b32_e32 v56, v159
	v_mov_b32_e32 v61, v164
	v_mov_b32_e32 v24, v128
	v_mov_b32_e32 v25, v131
	v_mov_b32_e32 v27, v133
	v_mov_b32_e32 v29, v135
	v_mov_b32_e32 v32, v137
	v_mov_b32_e32 v33, v139
	v_mov_b32_e32 v36, v141
	v_mov_b32_e32 v38, v143
	v_mov_b32_e32 v43, v145
	v_mov_b32_e32 v45, v148
	v_mov_b32_e32 v47, v150
	v_mov_b32_e32 v49, v152
	v_mov_b32_e32 v51, v154
	v_mov_b32_e32 v53, v156
	v_mov_b32_e32 v55, v158
	v_mov_b32_e32 v59, v161
	v_mov_b32_e32 v64, v167
	s_waitcnt vmcnt(14)
	v_perm_b32 v204, v205, v204, s45
	v_perm_b32 v205, v210, v205, s45
	v_perm_b32 v206, v209, v206, s45
	v_perm_b32 v207, v208, v207, s45
	v_perm_b32 v208, v255, v254, s45
	v_perm_b32 v209, v195, v255, s45
	v_perm_b32 v210, v253, v251, s45
	v_perm_b32 v211, v250, v211, s45
	v_mov_b32_e32 v3, v203
	v_mov_b32_e32 v28, v202
	v_mov_b32_e32 v94, v201
	v_mov_b32_e32 v95, v200
	v_mov_b32_e32 v2, v199
	v_mov_b32_e32 v42, v198
	v_mov_b32_e32 v40, v197
	s_mov_b32 s34, s75
	v_mov_b32_e32 v212, v204
	v_mov_b32_e32 v213, v205
	v_mov_b32_e32 v214, v206
	v_mov_b32_e32 v215, v207
	v_mov_b32_e32 v92, v208
	v_mov_b32_e32 v93, v209
	v_mov_b32_e32 v96, v210
	v_mov_b32_e32 v97, v211
	s_cbranch_vccz .Lpr_480

; __device__ __forceinline__ float fast_sigmoid(float x) { return __builtin_amdgcn_rcpf(1.0f + __builtin_amdgcn_exp2f(-1.4426950408889634f * x)); }
; __global__ void __launch_bounds__(NTHR, 2) mk_fwd(Args args) {
;     ...
;                     float Wc = 1.f;
; #pragma unroll
;                     for (int t = 0; t < 16; ++t) {
;                         const float cr = xr_[t + 1], ck = xk_[t + 1], cv = xv_[t + 1], wl = xwl_[t] + c_w0, al = xal_[t] + c_a0;
;                         const float pr_r = xr_[t], pr_k = xk_[t], pr_v = xv_[t];
;                         const float r = cr + (pr_r - cr) * mu_r, k = ck + (pr_k - ck) * mu_k, v = cv + (pr_v - cv) * mu_v;
;                         const float dec = fast_decay(wl), a = fast_sigmoid(al);
;                         float kk = k * c_kk; const float ss = wave_sum_dpp(kk * kk); kk = kk * __builtin_amdgcn_rsqf(fmaxf(ss, 1e-24f));
;                         const float k2 = k * (1.0f + (a - 1.0f) * c_ka), bb = kk * a;
;                         const float Wprev = Wc; Wc = Wc * dec; const float iw = __builtin_amdgcn_rcpf(Wc);
;                         At[t] = -kk * Wprev; Rt[t] = r * Wc; Bt[t] = bb * iw; Kt[t] = k2 * iw; Vt[t] = v;
;                     }
.Lpr_478:
	s_ashr_i32 s1, s34, 8
	s_and_b32 s0, s34, 15
	s_and_b32 s1, s1, -16
	s_or_b32 s0, s1, s0
	s_bfe_u32 s35, s34, 0x80004
	s_sub_i32 s99, s35, 3
	s_ashr_i32 s1, s0, 31
	s_lshl_b64 s[0:1], s[0:1], 22
	s_lshl_b32 s34, s35, 14
	s_add_u32 s0, s29, s0
	s_addc_u32 s1, s31, s1
	v_lshlrev_b32_e32 v231, 16, v38
	v_lshlrev_b32_e32 v38, 16, v58
	s_mov_b32 s88, s100
	v_add_f32_e32 v38, v95, v38
	v_lshlrev_b32_e32 v225, 16, v47
	s_mov_b32 s89, 0
	v_mul_f32_e64 v47, |v38|, s79
	s_cmp_eq_u32 s35, 0
	v_exp_f32_e32 v47, v47
	v_lshlrev_b32_e32 v234, 16, v24
	s_cselect_b64 s[0:1], -1, 0
	v_lshlrev_b32_e32 v236, 16, v25
	v_lshlrev_b32_e32 v228, 16, v39
	v_lshlrev_b32_e32 v224, 16, v46
	v_lshlrev_b32_e32 v39, 16, v57
	v_cndmask_b32_e64 v46, v234, 0, s[0:1]
	v_lshlrev_b32_e32 v222, 16, v48
	v_add_f32_e32 v48, v94, v39
	v_sub_f32_e32 v39, v46, v236
	v_lshlrev_b32_e32 v218, 16, v52
	v_fma_f32 v52, v40, v39, v236
	v_add_f32_e32 v39, 1.0, v47
	v_lshlrev_b32_e32 v235, 16, v21
	v_log_f32_e32 v46, v39
	v_lshlrev_b32_e32 v237, 16, v22
	v_lshlrev_b32_e32 v226, 16, v44
	v_cndmask_b32_e64 v44, v235, 0, s[0:1]
	v_sub_f32_e32 v39, v44, v237
	v_mul_f32_e32 v44, 0xbfb8aa3b, v48
	v_max_f32_e64 v38, -v38, 0
	v_exp_f32_e32 v44, v44
	v_fmac_f32_e32 v38, 0x3f317218, v46
	v_fma_f32 v39, v42, v39, v237
	v_add_f32_e32 v38, 0.5, v38
	v_mul_f32_e32 v38, 0xbfb8aa3b, v38
	v_mul_f32_e32 v47, v28, v39
	v_exp_f32_e32 v46, v38
	v_add_f32_e32 v38, 1.0, v44
	v_mul_f32_e32 v44, v47, v47
	v_mov_b32_e32 v48, 0
	v_lshlrev_b32_e32 v4, 16, v20
	v_mov_b32_dpp v44, v44 quad_perm:[1,0,3,2] row_mask:0xf bank_mask:0xf bound_ctrl:1
	v_fmac_f32_e32 v44, v47, v47
	v_cndmask_b32_e64 v4, v4, 0, s[0:1]
	v_rcp_f32_e32 v38, v38
	v_add_f32_dpp v44, v44, v44 quad_perm:[2,3,0,1] row_mask:0xf bank_mask:0xf bound_ctrl:1
	v_lshlrev_b32_e32 v227, 16, v45
	v_lshlrev_b32_e32 v45, 16, v62
	v_add_f32_dpp v44, v44, v44 row_half_mirror row_mask:0xf bank_mask:0xf bound_ctrl:1
	v_lshlrev_b32_e32 v5, 16, v23
	v_and_b32_e32 v23, 0xffff0000, v214
	v_add_f32_dpp v44, v44, v44 row_mirror row_mask:0xf bank_mask:0xf bound_ctrl:1
	v_lshlrev_b32_e32 v22, 16, v214
	v_lshlrev_b32_e32 v223, 16, v49
	v_mov_b32_dpp v48, v44 row_bcast:15 row_mask:0xa bank_mask:0xf
	v_add_f32_e32 v44, v44, v48
	v_mov_b32_e32 v48, 0
	v_lshlrev_b32_e32 v49, 16, v60
	v_lshlrev_b32_e32 v239, 16, v26
	v_mov_b32_dpp v48, v44 row_bcast:31 row_mask:0xc bank_mask:0xf
	v_add_f32_e32 v44, v44, v48
	v_and_b32_e32 v21, 0xffff0000, v215
	v_readlane_b32 s0, v44, 63
	v_lshlrev_b32_e32 v20, 16, v215
	v_lshlrev_b32_e32 v219, 16, v53
	v_max_f32_e64 v44, s0, s0
	v_max_f32_e32 v44, 0x179abe15, v44
	v_rsq_f32_e32 v48, v44
	v_mul_f32_e32 v44, 0xbfb8aa3b, v46
	v_exp_f32_e32 v44, v44
	v_mov_b32_e32 v53, 0
	v_mul_f32_e32 v46, v47, v48
	v_add_f32_e32 v47, -1.0, v38
	v_fma_f32 v47, v3, v47, 1.0
	v_xor_b32_e32 v214, 0x80000000, v46
	v_pk_mul_f32 v[38:39], v[38:39], v[46:47]
	v_add_f32_e32 v46, v95, v45
	v_mul_f32_e64 v45, |v46|, s79
	v_exp_f32_e32 v47, v45
	v_rcp_f32_e32 v48, v44
	v_max_f32_e64 v46, -v46, 0
	v_mul_f32_e32 v215, v52, v44
	v_add_f32_e32 v47, 1.0, v47
	v_pk_mul_f32 v[38:39], v[38:39], v[48:49] op_sel_hi:[1,0]
	v_add_f32_e32 v48, v94, v49
	v_log_f32_e32 v49, v47
	v_mul_f32_e32 v48, 0xbfb8aa3b, v48
	v_exp_f32_e32 v48, v48
	v_sub_f32_e32 v47, v237, v239
	v_fmac_f32_e32 v46, 0x3f317218, v49
	v_add_f32_e32 v46, 0.5, v46
	v_fma_f32 v47, v42, v47, v239
	v_mul_f32_e32 v46, 0xbfb8aa3b, v46
	v_exp_f32_e32 v49, v46
	v_add_f32_e32 v46, 1.0, v48
	v_mul_f32_e32 v48, v28, v47
	v_mul_f32_e32 v52, v48, v48
	v_rcp_f32_e32 v46, v46
	v_mul_f32_e32 v49, 0xbfb8aa3b, v49
	v_mov_b32_dpp v52, v52 quad_perm:[1,0,3,2] row_mask:0xf bank_mask:0xf bound_ctrl:1
	v_fmac_f32_e32 v52, v48, v48
	v_lshlrev_b32_e32 v220, 16, v50
	v_lshlrev_b32_e32 v50, 16, v65
	v_add_f32_dpp v52, v52, v52 quad_perm:[2,3,0,1] row_mask:0xf bank_mask:0xf bound_ctrl:1
	v_lshlrev_b32_e32 v241, 16, v30
	v_lshlrev_b32_e32 v242, 16, v32
	v_add_f32_dpp v52, v52, v52 row_half_mirror row_mask:0xf bank_mask:0xf bound_ctrl:1
	v_lshlrev_b32_e32 v244, 16, v33
	v_lshlrev_b32_e32 v221, 16, v51
	v_add_f32_dpp v52, v52, v52 row_mirror row_mask:0xf bank_mask:0xf bound_ctrl:1
	v_and_b32_e32 v33, 0xffff0000, v96
	v_lshlrev_b32_e32 v32, 16, v96
	v_mov_b32_dpp v53, v52 row_bcast:15 row_mask:0xa bank_mask:0xf
	v_add_f32_e32 v52, v52, v53
	v_mov_b32_e32 v53, 0
	v_lshlrev_b32_e32 v96, 16, v54
	v_lshlrev_b32_e32 v51, 16, v63
	v_mov_b32_dpp v53, v52 row_bcast:31 row_mask:0xc bank_mask:0xf
	v_add_f32_e32 v52, v52, v53
	v_exp_f32_e32 v53, v49
	v_readlane_b32 s0, v52, 63
	v_add_f32_e32 v49, -1.0, v46
	v_fma_f32 v49, v3, v49, 1.0
	v_max_f32_e64 v52, s0, s0
	v_max_f32_e32 v52, 0x179abe15, v52
	v_rsq_f32_e32 v52, v52
	v_sub_f32_e32 v54, v239, v241
	v_lshlrev_b32_e32 v243, 16, v31
	v_and_b32_e32 v31, 0xffff0000, v97
	v_mul_f32_e32 v48, v48, v52
	v_xor_b32_e32 v52, 0x80000000, v48
	v_pk_mul_f32 v[46:47], v[46:47], v[48:49]
	v_add_f32_e32 v48, v95, v50
	v_mul_f32_e64 v49, |v48|, s79
	v_exp_f32_e32 v50, v49
	v_lshlrev_b32_e32 v30, 16, v97
	v_lshlrev_b32_e32 v97, 16, v55
	v_add_f32_e32 v51, v94, v51
	v_add_f32_e32 v50, 1.0, v50
	v_log_f32_e32 v50, v50
	v_fma_f32 v55, v42, v54, v241
	v_max_f32_e64 v48, -v48, 0
	v_lshlrev_b32_e32 v238, 16, v27
	v_fmac_f32_e32 v48, 0x3f317218, v50
	v_mul_f32_e32 v50, 0xbfb8aa3b, v51
	v_mul_f32_e32 v51, v28, v55
	v_mul_f32_e32 v54, v51, v51
	v_lshlrev_b32_e32 v26, 16, v212
	v_and_b32_e32 v27, 0xffff0000, v212
	v_mov_b32_dpp v54, v54 quad_perm:[1,0,3,2] row_mask:0xf bank_mask:0xf bound_ctrl:1
	v_fmac_f32_e32 v54, v51, v51
	v_lshlrev_b32_e32 v212, 16, v56
	v_mov_b32_e32 v56, 0
	v_add_f32_dpp v54, v54, v54 quad_perm:[2,3,0,1] row_mask:0xf bank_mask:0xf bound_ctrl:1
; __device__ __forceinline__ float fast_sigmoid(float x) { return __builtin_amdgcn_rcpf(1.0f + __builtin_amdgcn_exp2f(-1.4426950408889634f * x)); }
; __global__ void __launch_bounds__(NTHR, 2) mk_fwd(Args args) {
;     ...
; #pragma unroll
;                     for (int t = 0; t < 16; ++t) {
;                         const float cr = xr_[t + 1], ck = xk_[t + 1], cv = xv_[t + 1], wl = xwl_[t] + c_w0, al = xal_[t] + c_a0;
;                         const float pr_r = xr_[t], pr_k = xk_[t], pr_v = xv_[t];
;                         const float r = cr + (pr_r - cr) * mu_r, k = ck + (pr_k - ck) * mu_k, v = cv + (pr_v - cv) * mu_v;
;                         const float dec = fast_decay(wl), a = fast_sigmoid(al);
;                         float kk = k * c_kk; const float ss = wave_sum_dpp(kk * kk); kk = kk * __builtin_amdgcn_rsqf(fmaxf(ss, 1e-24f));
;                         const float k2 = k * (1.0f + (a - 1.0f) * c_ka), bb = kk * a;
;                         const float Wprev = Wc; Wc = Wc * dec; const float iw = __builtin_amdgcn_rcpf(Wc);
;                         At[t] = -kk * Wprev; Rt[t] = r * Wc; Bt[t] = bb * iw; Kt[t] = k2 * iw; Vt[t] = v;
;                     }
	v_exp_f32_e32 v50, v50
	v_add_f32_e32 v48, 0.5, v48
	v_add_f32_dpp v54, v54, v54 row_half_mirror row_mask:0xf bank_mask:0xf bound_ctrl:1
	v_mul_f32_e32 v48, 0xbfb8aa3b, v48
	v_exp_f32_e32 v48, v48
	v_add_f32_dpp v54, v54, v54 row_mirror row_mask:0xf bank_mask:0xf bound_ctrl:1
	v_add_f32_e32 v50, 1.0, v50
	v_mul_f32_e32 v53, v44, v53
	v_mov_b32_dpp v56, v54 row_bcast:15 row_mask:0xa bank_mask:0xf
	v_add_f32_e32 v54, v54, v56
	v_mov_b32_e32 v56, 0
	v_rcp_f32_e32 v58, v53
	v_sub_f32_e32 v45, v236, v238
	v_mov_b32_dpp v56, v54 row_bcast:31 row_mask:0xc bank_mask:0xf
	v_add_f32_e32 v54, v54, v56
	v_mul_f32_e32 v48, 0xbfb8aa3b, v48
	v_readlane_b32 s0, v54, 63
	v_lshlrev_b32_e32 v229, 16, v43
	v_and_b32_e32 v25, 0xffff0000, v213
	v_max_f32_e64 v54, s0, s0
	v_max_f32_e32 v54, 0x179abe15, v54
	v_rsq_f32_e32 v56, v54
	v_rcp_f32_e32 v54, v50
	v_lshlrev_b32_e32 v24, 16, v213
	v_lshlrev_b32_e32 v213, 16, v59
	v_lshlrev_b32_e32 v43, 16, v64
	v_lshlrev_b32_e32 v59, 16, v67
	v_fma_f32 v45, v40, v45, v238
	v_exp_f32_e32 v64, v48
	v_add_f32_e32 v48, -1.0, v54
	v_mul_f32_e32 v56, v51, v56
	v_fma_f32 v57, v3, v48, 1.0
	v_pk_mul_f32 v[50:51], v[44:45], v[52:53]
	v_add_f32_e32 v52, v95, v59
	v_pk_mul_f32 v[44:45], v[46:47], v[58:59] op_sel_hi:[1,0]
	v_pk_mul_f32 v[46:47], v[54:55], v[56:57]
	v_mul_f32_e64 v54, |v52|, s79
	v_exp_f32_e32 v54, v54
	v_lshlrev_b32_e32 v240, 16, v29
	v_xor_b32_e32 v48, 0x80000000, v56
	v_sub_f32_e32 v56, v240, v242
	v_add_f32_e32 v54, 1.0, v54
	v_log_f32_e32 v54, v54
	v_lshlrev_b32_e32 v60, 16, v66
	v_fma_f32 v57, v40, v56, v242
	v_sub_f32_e32 v56, v241, v243
	v_add_f32_e32 v55, v94, v60
	v_fma_f32 v59, v42, v56, v243
	v_max_f32_e64 v52, -v52, 0
	v_fmac_f32_e32 v52, 0x3f317218, v54
	v_mul_f32_e32 v54, 0xbfb8aa3b, v55
	v_mul_f32_e32 v55, v28, v59
	v_mul_f32_e32 v56, v55, v55
	v_exp_f32_e32 v54, v54
	v_mov_b32_e32 v58, 0
	v_mov_b32_dpp v56, v56 quad_perm:[1,0,3,2] row_mask:0xf bank_mask:0xf bound_ctrl:1
	v_fmac_f32_e32 v56, v55, v55
	v_add_f32_e32 v52, 0.5, v52
	v_mul_f32_e32 v52, 0xbfb8aa3b, v52
	v_add_f32_dpp v56, v56, v56 quad_perm:[2,3,0,1] row_mask:0xf bank_mask:0xf bound_ctrl:1
	v_exp_f32_e32 v52, v52
	v_add_f32_e32 v54, 1.0, v54
	v_add_f32_dpp v56, v56, v56 row_half_mirror row_mask:0xf bank_mask:0xf bound_ctrl:1
	v_lshlrev_b32_e32 v249, 16, v72
	v_mul_f32_e32 v52, 0xbfb8aa3b, v52
	v_add_f32_dpp v56, v56, v56 row_mirror row_mask:0xf bank_mask:0xf bound_ctrl:1
	v_exp_f32_e32 v72, v52
	v_mul_f32_e32 v65, v53, v64
	v_mov_b32_dpp v58, v56 row_bcast:15 row_mask:0xa bank_mask:0xf
	v_add_f32_e32 v56, v56, v58
	v_mov_b32_e32 v58, 0
	v_lshlrev_b32_e32 v29, 16, v41
	v_lshlrev_b32_e32 v41, 16, v61
	v_mov_b32_dpp v58, v56 row_bcast:31 row_mask:0xc bank_mask:0xf
	v_add_f32_e32 v56, v56, v58
	v_rcp_f32_e32 v58, v54
	v_readlane_b32 s0, v56, 63
	v_lshlrev_b32_e32 v69, 16, v69
	v_sub_f32_e32 v49, v238, v240
	v_max_f32_e64 v56, s0, s0
	v_add_f32_e32 v52, -1.0, v58
	v_max_f32_e32 v56, 0x179abe15, v56
	v_fma_f32 v61, v3, v52, 1.0
	v_rcp_f32_e32 v52, v65
	v_rsq_f32_e32 v56, v56
	v_fma_f32 v49, v40, v49, v240
	v_mov_b32_e32 v64, v53
	v_pk_mul_f32 v[46:47], v[46:47], v[52:53] op_sel_hi:[1,0]
	v_add_f32_e32 v52, v95, v69
	v_mul_f32_e32 v60, v55, v56
	v_mul_f32_e64 v53, |v52|, s79
	v_pk_mul_f32 v[54:55], v[64:65], v[48:49]
	v_pk_mul_f32 v[48:49], v[58:59], v[60:61]
	v_exp_f32_e32 v58, v53
	v_lshlrev_b32_e32 v245, 16, v34
	v_lshlrev_b32_e32 v68, 16, v68
	v_sub_f32_e32 v59, v243, v245
	v_add_f32_e32 v58, 1.0, v58
	v_log_f32_e32 v58, v58
	v_xor_b32_e32 v56, 0x80000000, v60
	v_add_f32_e32 v60, v94, v68
	v_fma_f32 v59, v42, v59, v245
	v_max_f32_e64 v52, -v52, 0
	v_fmac_f32_e32 v52, 0x3f317218, v58
	v_mul_f32_e32 v58, 0xbfb8aa3b, v60
	v_mul_f32_e32 v60, v28, v59
	v_mul_f32_e32 v61, v60, v60
	v_mov_b32_e32 v64, 0
	v_exp_f32_e32 v58, v58
	v_mov_b32_dpp v61, v61 quad_perm:[1,0,3,2] row_mask:0xf bank_mask:0xf bound_ctrl:1
	v_fmac_f32_e32 v61, v60, v60
	v_add_f32_e32 v52, 0.5, v52
	v_mul_f32_e32 v52, 0xbfb8aa3b, v52
	v_add_f32_dpp v61, v61, v61 quad_perm:[2,3,0,1] row_mask:0xf bank_mask:0xf bound_ctrl:1
	v_exp_f32_e32 v52, v52
	v_add_f32_e32 v58, 1.0, v58
	v_add_f32_dpp v61, v61, v61 row_half_mirror row_mask:0xf bank_mask:0xf bound_ctrl:1
	v_rcp_f32_e32 v58, v58
	v_mul_f32_e32 v52, 0xbfb8aa3b, v52
	v_add_f32_dpp v61, v61, v61 row_mirror row_mask:0xf bank_mask:0xf bound_ctrl:1
	v_lshlrev_b32_e32 v62, 16, v74
	v_lshlrev_b32_e32 v74, 16, v80
	v_mov_b32_dpp v64, v61 row_bcast:15 row_mask:0xa bank_mask:0xf
	v_add_f32_e32 v61, v61, v64
	v_mov_b32_e32 v64, 0
	v_exp_f32_e32 v80, v52
	v_add_f32_e32 v52, -1.0, v58
	v_mov_b32_dpp v64, v61 row_bcast:31 row_mask:0xc bank_mask:0xf
	v_add_f32_e32 v61, v61, v64
	v_lshlrev_b32_e32 v246, 16, v71
	v_readlane_b32 s0, v61, 63
	v_lshlrev_b32_e32 v248, 16, v73
	v_fma_f32 v69, v3, v52, 1.0
	v_max_f32_e64 v61, s0, s0
	v_max_f32_e32 v61, 0x179abe15, v61
	v_rsq_f32_e32 v61, v61
	v_mul_f32_e32 v73, v65, v72
	v_mov_b32_e32 v72, v65
	v_rcp_f32_e32 v64, v73
	v_mul_f32_e32 v68, v60, v61
	v_pk_mul_f32 v[60:61], v[72:73], v[56:57]
	v_pk_mul_f32 v[56:57], v[58:59], v[68:69]
	v_add_f32_e32 v58, v95, v246
	v_mul_f32_e64 v59, |v58|, s79
	v_exp_f32_e32 v59, v59
	v_lshlrev_b32_e32 v233, 16, v36
	v_pk_mul_f32 v[48:49], v[48:49], v[64:65] op_sel_hi:[1,0]
	v_sub_f32_e32 v65, v244, v233
	v_add_f32_e32 v59, 1.0, v59
	v_lshlrev_b32_e32 v247, 16, v70
	v_fma_f32 v69, v40, v65, v233
	v_log_f32_e32 v65, v59
	v_add_f32_e32 v64, v94, v247
	v_mul_f32_e32 v64, 0xbfb8aa3b, v64
	v_max_f32_e64 v58, -v58, 0
	v_exp_f32_e32 v64, v64
	v_lshlrev_b32_e32 v232, 16, v35
	v_fmac_f32_e32 v58, 0x3f317218, v65
	v_sub_f32_e32 v59, v245, v232
	v_add_f32_e32 v58, 0.5, v58
; __device__ __forceinline__ float fast_sigmoid(float x) { return __builtin_amdgcn_rcpf(1.0f + __builtin_amdgcn_exp2f(-1.4426950408889634f * x)); }
; __global__ void __launch_bounds__(NTHR, 2) mk_fwd(Args args) {
;     ...
; #pragma unroll
;                     for (int t = 0; t < 16; ++t) {
;                         const float cr = xr_[t + 1], ck = xk_[t + 1], cv = xv_[t + 1], wl = xwl_[t] + c_w0, al = xal_[t] + c_a0;
;                         const float pr_r = xr_[t], pr_k = xk_[t], pr_v = xv_[t];
;                         const float r = cr + (pr_r - cr) * mu_r, k = ck + (pr_k - ck) * mu_k, v = cv + (pr_v - cv) * mu_v;
;                         const float dec = fast_decay(wl), a = fast_sigmoid(al);
;                         float kk = k * c_kk; const float ss = wave_sum_dpp(kk * kk); kk = kk * __builtin_amdgcn_rsqf(fmaxf(ss, 1e-24f));
;                         const float k2 = k * (1.0f + (a - 1.0f) * c_ka), bb = kk * a;
;                         const float Wprev = Wc; Wc = Wc * dec; const float iw = __builtin_amdgcn_rcpf(Wc);
;                         At[t] = -kk * Wprev; Rt[t] = r * Wc; Bt[t] = bb * iw; Kt[t] = k2 * iw; Vt[t] = v;
;                     }
	v_fma_f32 v59, v42, v59, v232
	v_mul_f32_e32 v58, 0xbfb8aa3b, v58
	v_exp_f32_e32 v65, v58
	v_add_f32_e32 v58, 1.0, v64
	v_mul_f32_e32 v64, v28, v59
	v_xor_b32_e32 v52, 0x80000000, v68
	v_mul_f32_e32 v68, v64, v64
	v_mov_b32_e32 v72, 0
	v_lshlrev_b32_e32 v63, 16, v75
	v_mov_b32_dpp v68, v68 quad_perm:[1,0,3,2] row_mask:0xf bank_mask:0xf bound_ctrl:1
	v_fmac_f32_e32 v68, v64, v64
	v_lshlrev_b32_e32 v75, 16, v81
	v_rcp_f32_e32 v58, v58
	v_add_f32_dpp v68, v68, v68 quad_perm:[2,3,0,1] row_mask:0xf bank_mask:0xf bound_ctrl:1
	v_mul_f32_e32 v81, v73, v80
	v_sub_f32_e32 v53, v242, v244
	v_add_f32_dpp v68, v68, v68 row_half_mirror row_mask:0xf bank_mask:0xf bound_ctrl:1
	v_lshlrev_b32_e32 v66, 16, v76
	v_fma_f32 v53, v40, v53, v244
	v_add_f32_dpp v68, v68, v68 row_mirror row_mask:0xf bank_mask:0xf bound_ctrl:1
	v_mul_f32_e32 v65, 0xbfb8aa3b, v65
	v_mov_b32_e32 v80, v73
	v_mov_b32_dpp v72, v68 row_bcast:15 row_mask:0xa bank_mask:0xf
	v_add_f32_e32 v68, v68, v72
	v_mov_b32_e32 v72, 0
	v_and_b32_e32 v35, 0xffff0000, v93
	v_lshlrev_b32_e32 v34, 16, v93
	v_mov_b32_dpp v72, v68 row_bcast:31 row_mask:0xc bank_mask:0xf
	v_add_f32_e32 v68, v68, v72
	v_rcp_f32_e32 v72, v81
	v_readlane_b32 s0, v68, 63
	v_lshlrev_b32_e32 v67, 16, v77
	v_lshlrev_b32_e32 v93, 16, v88
	v_max_f32_e64 v68, s0, s0
	v_max_f32_e32 v68, 0x179abe15, v68
	v_rsq_f32_e32 v68, v68
	v_exp_f32_e32 v88, v65
	v_lshlrev_b32_e32 v230, 16, v37
	v_lshlrev_b32_e32 v70, 16, v78
	v_mul_f32_e32 v76, v64, v68
	v_add_f32_e32 v64, -1.0, v58
	v_fma_f32 v77, v3, v64, 1.0
	v_pk_mul_f32 v[64:65], v[80:81], v[52:53]
	v_pk_mul_f32 v[52:53], v[56:57], v[72:73] op_sel_hi:[1,0]
	v_add_f32_e32 v72, v95, v248
	v_pk_mul_f32 v[56:57], v[58:59], v[76:77]
	v_mul_f32_e64 v58, |v72|, s79
	v_exp_f32_e32 v58, v58
	v_sub_f32_e32 v59, v233, v231
	v_fma_f32 v73, v40, v59, v231
	v_sub_f32_e32 v59, v232, v230
	v_add_f32_e32 v58, 1.0, v58
	v_log_f32_e32 v80, v58
	v_fma_f32 v77, v42, v59, v230
	v_pk_add_f32 v[58:59], v[26:27], v[24:25] neg_lo:[0,1] neg_hi:[0,1]
	v_max_f32_e64 v27, -v72, 0
	v_xor_b32_e32 v68, 0x80000000, v76
	v_add_f32_e32 v76, v94, v249
	v_fmac_f32_e32 v27, 0x3f317218, v80
	v_mul_f32_e32 v80, v28, v77
	v_mul_f32_e32 v72, 0xbfb8aa3b, v76
	v_mul_f32_e32 v76, v80, v80
	v_lshlrev_b32_e32 v78, 16, v82
	v_mov_b32_e32 v82, 0
	v_mov_b32_dpp v76, v76 quad_perm:[1,0,3,2] row_mask:0xf bank_mask:0xf bound_ctrl:1
	v_fmac_f32_e32 v76, v80, v80
	v_lshlrev_b32_e32 v36, 16, v92
	v_and_b32_e32 v37, 0xffff0000, v92
	v_add_f32_dpp v76, v76, v76 quad_perm:[2,3,0,1] row_mask:0xf bank_mask:0xf bound_ctrl:1
	v_lshlrev_b32_e32 v92, 16, v89
	v_mul_f32_e32 v89, v81, v88
	v_add_f32_dpp v76, v76, v76 row_half_mirror row_mask:0xf bank_mask:0xf bound_ctrl:1
	v_exp_f32_e32 v72, v72
	v_add_f32_e32 v63, v95, v63
	v_add_f32_dpp v76, v76, v76 row_mirror row_mask:0xf bank_mask:0xf bound_ctrl:1
	v_lshlrev_b32_e32 v71, 16, v79
	v_add_f32_e32 v72, 1.0, v72
	v_mov_b32_dpp v82, v76 row_bcast:15 row_mask:0xa bank_mask:0xf
	v_add_f32_e32 v76, v76, v82
	v_mov_b32_e32 v82, 0
	v_lshlrev_b32_e32 v79, 16, v83
	v_add_f32_e32 v27, 0.5, v27
	v_mov_b32_dpp v82, v76 row_bcast:31 row_mask:0xc bank_mask:0xf
	v_add_f32_e32 v76, v76, v82
	v_mul_f32_e32 v27, 0xbfb8aa3b, v27
	v_readlane_b32 s0, v76, 63
	v_mov_b32_e32 v88, v81
	v_exp_f32_e32 v27, v27
	v_max_f32_e64 v76, s0, s0
	v_max_f32_e32 v76, 0x179abe15, v76
	v_rsq_f32_e32 v82, v76
	v_rcp_f32_e32 v76, v72
	v_pk_mul_f32 v[68:69], v[88:89], v[68:69]
	v_mov_b32_e32 v88, 0
	v_mul_f32_e32 v82, v80, v82
	v_rcp_f32_e32 v80, v89
	v_add_f32_e32 v72, -1.0, v76
	v_fma_f32 v83, v3, v72, 1.0
	v_xor_b32_e32 v72, 0x80000000, v82
	v_pk_mul_f32 v[56:57], v[56:57], v[80:81] op_sel_hi:[1,0]
	v_mul_f32_e64 v80, |v63|, s79
	v_exp_f32_e32 v80, v80
	v_pk_mul_f32 v[76:77], v[76:77], v[82:83]
	v_sub_f32_e32 v82, v230, v228
	v_fma_f32 v83, v42, v82, v228
	v_add_f32_e32 v80, 1.0, v80
	v_log_f32_e32 v80, v80
	v_max_f32_e64 v63, -v63, 0
	v_add_f32_e32 v62, v94, v62
	v_mul_f32_e32 v62, 0xbfb8aa3b, v62
	v_fmac_f32_e32 v63, 0x3f317218, v80
	v_mul_f32_e32 v80, v28, v83
	v_mul_f32_e32 v82, v80, v80
	v_exp_f32_e32 v62, v62
	v_mul_f32_e32 v27, 0xbfb8aa3b, v27
	v_mov_b32_dpp v82, v82 quad_perm:[1,0,3,2] row_mask:0xf bank_mask:0xf bound_ctrl:1
	v_fmac_f32_e32 v82, v80, v80
	v_exp_f32_e32 v27, v27
	v_add_f32_e32 v63, 0.5, v63
	v_add_f32_dpp v82, v82, v82 quad_perm:[2,3,0,1] row_mask:0xf bank_mask:0xf bound_ctrl:1
	v_mul_f32_e32 v63, 0xbfb8aa3b, v63
	v_exp_f32_e32 v63, v63
	v_add_f32_dpp v82, v82, v82 row_half_mirror row_mask:0xf bank_mask:0xf bound_ctrl:1
	v_add_f32_e32 v62, 1.0, v62
	v_sub_f32_e32 v81, v231, v229
	v_add_f32_dpp v82, v82, v82 row_mirror row_mask:0xf bank_mask:0xf bound_ctrl:1
	v_mul_f32_e32 v231, v89, v27
	v_add_f32_e32 v27, v95, v67
	v_mov_b32_dpp v88, v82 row_bcast:15 row_mask:0xa bank_mask:0xf
	v_add_f32_e32 v82, v82, v88
	v_mov_b32_e32 v88, 0
	v_mul_f32_e64 v67, |v27|, s79
	v_exp_f32_e32 v67, v67
	v_mov_b32_dpp v88, v82 row_bcast:31 row_mask:0xc bank_mask:0xf
	v_add_f32_e32 v82, v82, v88
	v_lshlrev_b32_e32 v217, 16, v91
	v_readlane_b32 s0, v82, 63
	v_add_f32_e32 v67, 1.0, v67
	v_log_f32_e32 v67, v67
	v_max_f32_e64 v82, s0, s0
	v_max_f32_e32 v82, 0x179abe15, v82
	v_rsq_f32_e32 v88, v82
	v_rcp_f32_e32 v82, v62
	v_mul_f32_e32 v62, 0xbfb8aa3b, v63
	v_exp_f32_e32 v232, v62
	v_lshlrev_b32_e32 v216, 16, v90
	v_add_f32_e32 v62, -1.0, v82
	v_fma_f32 v91, v3, v62, 1.0
	v_rcp_f32_e32 v62, v231
	v_mul_f32_e32 v90, v80, v88
	v_mov_b32_e32 v230, v89
	v_pk_mul_f32 v[82:83], v[82:83], v[90:91]
	v_pk_mul_f32 v[62:63], v[76:77], v[62:63] op_sel_hi:[1,0]
	v_sub_f32_e32 v76, v229, v227
	v_fma_f32 v89, v40, v76, v227
	v_sub_f32_e32 v76, v228, v226
; __device__ __forceinline__ float fast_sigmoid(float x) { return __builtin_amdgcn_rcpf(1.0f + __builtin_amdgcn_exp2f(-1.4426950408889634f * x)); }
; __global__ void __launch_bounds__(NTHR, 2) mk_fwd(Args args) {
;     ...
; #pragma unroll
;                     for (int t = 0; t < 16; ++t) {
;                         const float cr = xr_[t + 1], ck = xk_[t + 1], cv = xv_[t + 1], wl = xwl_[t] + c_w0, al = xal_[t] + c_a0;
;                         const float pr_r = xr_[t], pr_k = xk_[t], pr_v = xv_[t];
;                         const float r = cr + (pr_r - cr) * mu_r, k = ck + (pr_k - ck) * mu_k, v = cv + (pr_v - cv) * mu_v;
;                         const float dec = fast_decay(wl), a = fast_sigmoid(al);
;                         float kk = k * c_kk; const float ss = wave_sum_dpp(kk * kk); kk = kk * __builtin_amdgcn_rsqf(fmaxf(ss, 1e-24f));
;                         const float k2 = k * (1.0f + (a - 1.0f) * c_ka), bb = kk * a;
;                         const float Wprev = Wc; Wc = Wc * dec; const float iw = __builtin_amdgcn_rcpf(Wc);
;                         At[t] = -kk * Wprev; Rt[t] = r * Wc; Bt[t] = bb * iw; Kt[t] = k2 * iw; Vt[t] = v;
;                     }
	v_fma_f32 v91, v42, v76, v226
	v_max_f32_e64 v27, -v27, 0
	v_fmac_f32_e32 v27, 0x3f317218, v67
	v_mul_f32_e32 v67, v28, v91
	v_mul_f32_e32 v76, v67, v67
	v_mov_b32_e32 v77, 0
	v_add_f32_e32 v66, v94, v66
	v_mov_b32_dpp v76, v76 quad_perm:[1,0,3,2] row_mask:0xf bank_mask:0xf bound_ctrl:1
	v_fmac_f32_e32 v76, v67, v67
	v_mul_f32_e32 v66, 0xbfb8aa3b, v66
	v_exp_f32_e32 v66, v66
	v_add_f32_dpp v76, v76, v76 quad_perm:[2,3,0,1] row_mask:0xf bank_mask:0xf bound_ctrl:1
	v_fma_f32 v81, v40, v81, v229
	v_xor_b32_e32 v80, 0x80000000, v90
	v_add_f32_dpp v76, v76, v76 row_half_mirror row_mask:0xf bank_mask:0xf bound_ctrl:1
	v_add_f32_e32 v66, 1.0, v66
	v_rcp_f32_e32 v90, v66
	v_add_f32_dpp v76, v76, v76 row_mirror row_mask:0xf bank_mask:0xf bound_ctrl:1
	v_mul_f32_e32 v233, v231, v232
	v_mov_b32_e32 v232, v231
	v_mov_b32_dpp v77, v76 row_bcast:15 row_mask:0xa bank_mask:0xf
	v_add_f32_e32 v76, v76, v77
	v_mov_b32_e32 v77, 0
	v_add_f32_e32 v71, v95, v71
	v_add_f32_e32 v66, -1.0, v90
	v_mov_b32_dpp v77, v76 row_bcast:31 row_mask:0xc bank_mask:0xf
	v_add_f32_e32 v76, v76, v77
	v_fma_f32 v229, v3, v66, 1.0
	v_readlane_b32 s0, v76, 63
	v_rcp_f32_e32 v66, v233
	v_add_f32_e32 v27, 0.5, v27
	v_max_f32_e64 v76, s0, s0
	v_max_f32_e32 v76, 0x179abe15, v76
	v_rsq_f32_e32 v76, v76
	v_mul_f32_e32 v27, 0xbfb8aa3b, v27
	v_exp_f32_e32 v27, v27
	v_add_f32_e32 v70, v94, v70
	v_mul_f32_e32 v228, v67, v76
	v_pk_mul_f32 v[76:77], v[232:233], v[80:81]
	v_mul_f32_e64 v80, |v71|, s79
	v_exp_f32_e32 v80, v80
	v_sub_f32_e32 v81, v227, v225
	v_pk_mul_f32 v[66:67], v[82:83], v[66:67] op_sel_hi:[1,0]
	v_pk_mul_f32 v[82:83], v[90:91], v[228:229]
	v_add_f32_e32 v80, 1.0, v80
	v_log_f32_e32 v80, v80
	v_fma_f32 v91, v40, v81, v225
	v_sub_f32_e32 v81, v226, v224
	v_fma_f32 v227, v42, v81, v224
	v_max_f32_e64 v71, -v71, 0
	v_fmac_f32_e32 v71, 0x3f317218, v80
	v_mul_f32_e32 v80, v28, v227
	v_mul_f32_e32 v81, v80, v80
	v_mul_f32_e32 v70, 0xbfb8aa3b, v70
	v_exp_f32_e32 v70, v70
	v_mov_b32_dpp v81, v81 quad_perm:[1,0,3,2] row_mask:0xf bank_mask:0xf bound_ctrl:1
	v_fmac_f32_e32 v81, v80, v80
	v_mul_f32_e32 v27, 0xbfb8aa3b, v27
	v_exp_f32_e32 v27, v27
	v_add_f32_dpp v81, v81, v81 quad_perm:[2,3,0,1] row_mask:0xf bank_mask:0xf bound_ctrl:1
	v_add_f32_e32 v71, 0.5, v71
	v_mul_f32_e32 v71, 0xbfb8aa3b, v71
	v_add_f32_dpp v81, v81, v81 row_half_mirror row_mask:0xf bank_mask:0xf bound_ctrl:1
	v_mov_b32_e32 v90, 0
	v_exp_f32_e32 v71, v71
	v_add_f32_dpp v81, v81, v81 row_mirror row_mask:0xf bank_mask:0xf bound_ctrl:1
	v_add_f32_e32 v70, 1.0, v70
	v_rcp_f32_e32 v226, v70
	v_mov_b32_dpp v90, v81 row_bcast:15 row_mask:0xa bank_mask:0xf
	v_add_f32_e32 v81, v81, v90
	v_mov_b32_e32 v90, 0
	v_pk_mul_f32 v[72:73], v[230:231], v[72:73]
	v_mul_f32_e32 v231, v233, v27
	v_mov_b32_dpp v90, v81 row_bcast:31 row_mask:0xc bank_mask:0xf
	v_add_f32_e32 v27, v95, v75
	v_add_f32_e32 v81, v81, v90
	v_mul_f32_e64 v75, |v27|, s79
	v_readlane_b32 s0, v81, 63
	v_mul_f32_e32 v70, 0xbfb8aa3b, v71
	v_exp_f32_e32 v75, v75
	v_max_f32_e64 v81, s0, s0
	v_exp_f32_e32 v232, v70
	v_add_f32_e32 v70, -1.0, v226
	v_max_f32_e32 v81, 0x179abe15, v81
	v_fma_f32 v229, v3, v70, 1.0
	v_rcp_f32_e32 v70, v231
	v_rsq_f32_e32 v81, v81
	v_add_f32_e32 v75, 1.0, v75
	v_log_f32_e32 v75, v75
	v_pk_mul_f32 v[70:71], v[82:83], v[70:71] op_sel_hi:[1,0]
	v_sub_f32_e32 v82, v225, v223
	v_xor_b32_e32 v88, 0x80000000, v228
	v_mul_f32_e32 v228, v80, v81
	v_mov_b32_e32 v230, v233
	v_fma_f32 v225, v40, v82, v223
	v_sub_f32_e32 v82, v224, v222
	v_pk_mul_f32 v[80:81], v[230:231], v[88:89]
	v_pk_mul_f32 v[88:89], v[226:227], v[228:229]
	v_fma_f32 v227, v42, v82, v222
	v_max_f32_e64 v27, -v27, 0
	v_fmac_f32_e32 v27, 0x3f317218, v75
	v_mul_f32_e32 v75, v28, v227
	v_mul_f32_e32 v82, v75, v75
	v_add_f32_e32 v74, v94, v74
	v_mul_f32_e32 v74, 0xbfb8aa3b, v74
	v_mov_b32_dpp v82, v82 quad_perm:[1,0,3,2] row_mask:0xf bank_mask:0xf bound_ctrl:1
	v_fmac_f32_e32 v82, v75, v75
	v_exp_f32_e32 v74, v74
	v_mov_b32_e32 v83, 0
	v_add_f32_dpp v82, v82, v82 quad_perm:[2,3,0,1] row_mask:0xf bank_mask:0xf bound_ctrl:1
	v_mul_f32_e32 v233, v231, v232
	v_add_f32_e32 v74, 1.0, v74
	v_add_f32_dpp v82, v82, v82 row_half_mirror row_mask:0xf bank_mask:0xf bound_ctrl:1
	v_rcp_f32_e32 v226, v74
	v_add_f32_e32 v79, v95, v79
	v_add_f32_dpp v82, v82, v82 row_mirror row_mask:0xf bank_mask:0xf bound_ctrl:1
	v_xor_b32_e32 v90, 0x80000000, v228
	v_add_f32_e32 v74, -1.0, v226
	v_mov_b32_dpp v83, v82 row_bcast:15 row_mask:0xa bank_mask:0xf
	v_add_f32_e32 v82, v82, v83
	v_mov_b32_e32 v83, 0
	v_fma_f32 v229, v3, v74, 1.0
	v_rcp_f32_e32 v74, v233
	v_mov_b32_dpp v83, v82 row_bcast:31 row_mask:0xc bank_mask:0xf
	v_add_f32_e32 v82, v82, v83
	v_add_f32_e32 v27, 0.5, v27
	v_readlane_b32 s0, v82, 63
	v_mov_b32_e32 v232, v231
	v_mul_f32_e32 v27, 0xbfb8aa3b, v27
	v_max_f32_e64 v82, s0, s0
	v_max_f32_e32 v82, 0x179abe15, v82
	v_rsq_f32_e32 v82, v82
	v_exp_f32_e32 v27, v27
	v_add_f32_e32 v78, v94, v78
	v_mul_f32_e32 v78, 0xbfb8aa3b, v78
	v_mul_f32_e32 v228, v75, v82
	v_pk_mul_f32 v[74:75], v[88:89], v[74:75] op_sel_hi:[1,0]
	v_mul_f32_e64 v88, |v79|, s79
	v_exp_f32_e32 v88, v88
	v_sub_f32_e32 v89, v223, v221
	v_fma_f32 v223, v40, v89, v221
	v_sub_f32_e32 v89, v222, v220
	v_add_f32_e32 v88, 1.0, v88
	v_log_f32_e32 v88, v88
	v_pk_mul_f32 v[82:83], v[232:233], v[90:91]
	v_pk_mul_f32 v[90:91], v[226:227], v[228:229]
	v_fma_f32 v227, v42, v89, v220
	v_max_f32_e64 v79, -v79, 0
	v_fmac_f32_e32 v79, 0x3f317218, v88
	v_mul_f32_e32 v88, v28, v227
	v_mul_f32_e32 v89, v88, v88
	v_exp_f32_e32 v78, v78
	v_mul_f32_e32 v27, 0xbfb8aa3b, v27
	v_mov_b32_dpp v89, v89 quad_perm:[1,0,3,2] row_mask:0xf bank_mask:0xf bound_ctrl:1
; __device__ __forceinline__ float fast_sigmoid(float x) { return __builtin_amdgcn_rcpf(1.0f + __builtin_amdgcn_exp2f(-1.4426950408889634f * x)); }
; __global__ void __launch_bounds__(NTHR, 2) mk_fwd(Args args) {
;     ...
; #pragma unroll
;                     for (int t = 0; t < 16; ++t) {
;                         const float cr = xr_[t + 1], ck = xk_[t + 1], cv = xv_[t + 1], wl = xwl_[t] + c_w0, al = xal_[t] + c_a0;
;                         const float pr_r = xr_[t], pr_k = xk_[t], pr_v = xv_[t];
;                         const float r = cr + (pr_r - cr) * mu_r, k = ck + (pr_k - ck) * mu_k, v = cv + (pr_v - cv) * mu_v;
;                         const float dec = fast_decay(wl), a = fast_sigmoid(al);
;                         float kk = k * c_kk; const float ss = wave_sum_dpp(kk * kk); kk = kk * __builtin_amdgcn_rsqf(fmaxf(ss, 1e-24f));
;                         const float k2 = k * (1.0f + (a - 1.0f) * c_ka), bb = kk * a;
;                         const float Wprev = Wc; Wc = Wc * dec; const float iw = __builtin_amdgcn_rcpf(Wc);
;                         At[t] = -kk * Wprev; Rt[t] = r * Wc; Bt[t] = bb * iw; Kt[t] = k2 * iw; Vt[t] = v;
;                     }
	v_fmac_f32_e32 v89, v88, v88
	v_exp_f32_e32 v27, v27
	v_add_f32_e32 v79, 0.5, v79
	v_add_f32_dpp v89, v89, v89 quad_perm:[2,3,0,1] row_mask:0xf bank_mask:0xf bound_ctrl:1
	v_mul_f32_e32 v79, 0xbfb8aa3b, v79
	v_mov_b32_e32 v222, 0
	v_add_f32_dpp v89, v89, v89 row_half_mirror row_mask:0xf bank_mask:0xf bound_ctrl:1
	v_exp_f32_e32 v79, v79
	v_add_f32_e32 v78, 1.0, v78
	v_add_f32_dpp v89, v89, v89 row_mirror row_mask:0xf bank_mask:0xf bound_ctrl:1
	v_lshlrev_b32_e32 v85, 16, v85
	v_rcp_f32_e32 v226, v78
	v_mov_b32_dpp v222, v89 row_bcast:15 row_mask:0xa bank_mask:0xf
	v_add_f32_e32 v89, v89, v222
	v_mov_b32_e32 v222, 0
	v_mul_f32_e32 v231, v233, v27
	v_add_f32_e32 v27, v95, v85
	v_mov_b32_dpp v222, v89 row_bcast:31 row_mask:0xc bank_mask:0xf
	v_add_f32_e32 v89, v89, v222
	v_mul_f32_e64 v85, |v27|, s79
	v_readlane_b32 s0, v89, 63
	v_mul_f32_e32 v78, 0xbfb8aa3b, v79
	v_exp_f32_e32 v85, v85
	v_max_f32_e64 v89, s0, s0
	v_exp_f32_e32 v232, v78
	v_add_f32_e32 v78, -1.0, v226
	v_max_f32_e32 v89, 0x179abe15, v89
	v_fma_f32 v229, v3, v78, 1.0
	v_rcp_f32_e32 v78, v231
	v_rsq_f32_e32 v89, v89
	v_add_f32_e32 v85, 1.0, v85
	v_log_f32_e32 v85, v85
	v_pk_mul_f32 v[78:79], v[90:91], v[78:79] op_sel_hi:[1,0]
	v_sub_f32_e32 v90, v221, v219
	v_xor_b32_e32 v224, 0x80000000, v228
	v_mul_f32_e32 v228, v88, v89
	v_mov_b32_e32 v230, v233
	v_fma_f32 v221, v40, v90, v219
	v_sub_f32_e32 v90, v220, v218
	v_pk_mul_f32 v[88:89], v[230:231], v[224:225]
	v_pk_mul_f32 v[224:225], v[226:227], v[228:229]
	v_fma_f32 v227, v42, v90, v218
	v_max_f32_e64 v27, -v27, 0
	v_fmac_f32_e32 v27, 0x3f317218, v85
	v_mul_f32_e32 v85, v28, v227
	v_lshlrev_b32_e32 v84, 16, v84
	v_mul_f32_e32 v90, v85, v85
	v_add_f32_e32 v84, v94, v84
	v_mul_f32_e32 v84, 0xbfb8aa3b, v84
	v_mov_b32_dpp v90, v90 quad_perm:[1,0,3,2] row_mask:0xf bank_mask:0xf bound_ctrl:1
	v_fmac_f32_e32 v90, v85, v85
	v_exp_f32_e32 v84, v84
	v_mov_b32_e32 v91, 0
	v_add_f32_dpp v90, v90, v90 quad_perm:[2,3,0,1] row_mask:0xf bank_mask:0xf bound_ctrl:1
	v_mul_f32_e32 v233, v231, v232
	v_add_f32_e32 v84, 1.0, v84
	v_add_f32_dpp v90, v90, v90 row_half_mirror row_mask:0xf bank_mask:0xf bound_ctrl:1
	v_rcp_f32_e32 v226, v84
	v_lshlrev_b32_e32 v87, 16, v87
	v_add_f32_dpp v90, v90, v90 row_mirror row_mask:0xf bank_mask:0xf bound_ctrl:1
	v_add_f32_e32 v87, v95, v87
	v_add_f32_e32 v84, -1.0, v226
	v_mov_b32_dpp v91, v90 row_bcast:15 row_mask:0xa bank_mask:0xf
	v_add_f32_e32 v90, v90, v91
	v_mov_b32_e32 v91, 0
	v_fma_f32 v229, v3, v84, 1.0
	v_rcp_f32_e32 v84, v233
	v_mov_b32_dpp v91, v90 row_bcast:31 row_mask:0xc bank_mask:0xf
	v_add_f32_e32 v90, v90, v91
	v_xor_b32_e32 v222, 0x80000000, v228
	v_readlane_b32 s0, v90, 63
	v_sub_f32_e32 v218, v218, v96
	v_mov_b32_e32 v232, v231
	v_max_f32_e64 v90, s0, s0
	v_max_f32_e32 v90, 0x179abe15, v90
	v_rsq_f32_e32 v90, v90
	v_lshlrev_b32_e32 v86, 16, v86
	v_add_f32_e32 v27, 0.5, v27
	v_add_f32_e32 v86, v94, v86
	v_mul_f32_e32 v228, v85, v90
	v_pk_mul_f32 v[84:85], v[224:225], v[84:85] op_sel_hi:[1,0]
	v_mul_f32_e64 v224, |v87|, s79
	v_exp_f32_e32 v224, v224
	v_fma_f32 v225, v42, v218, v96
	v_max_f32_e64 v87, -v87, 0
	v_mul_f32_e32 v218, v28, v225
	v_add_f32_e32 v224, 1.0, v224
	v_log_f32_e32 v224, v224
	v_pk_mul_f32 v[90:91], v[232:233], v[222:223]
	v_pk_mul_f32 v[222:223], v[226:227], v[228:229]
	v_mov_b32_e32 v226, 0
	v_fmac_f32_e32 v87, 0x3f317218, v224
	v_mul_f32_e32 v224, v218, v218
	v_mul_f32_e32 v27, 0xbfb8aa3b, v27
	v_mul_f32_e32 v86, 0xbfb8aa3b, v86
	v_mov_b32_dpp v224, v224 quad_perm:[1,0,3,2] row_mask:0xf bank_mask:0xf bound_ctrl:1
	v_fmac_f32_e32 v224, v218, v218
	v_exp_f32_e32 v27, v27
	v_exp_f32_e32 v86, v86
	v_add_f32_dpp v224, v224, v224 quad_perm:[2,3,0,1] row_mask:0xf bank_mask:0xf bound_ctrl:1
	v_add_f32_e32 v87, 0.5, v87
	v_mul_f32_e32 v87, 0xbfb8aa3b, v87
	v_add_f32_dpp v224, v224, v224 row_half_mirror row_mask:0xf bank_mask:0xf bound_ctrl:1
	v_mul_f32_e32 v27, 0xbfb8aa3b, v27
	v_exp_f32_e32 v87, v87
	v_add_f32_dpp v224, v224, v224 row_mirror row_mask:0xf bank_mask:0xf bound_ctrl:1
	v_add_f32_e32 v86, 1.0, v86
	v_exp_f32_e32 v27, v27
	v_mov_b32_dpp v226, v224 row_bcast:15 row_mask:0xa bank_mask:0xf
	v_add_f32_e32 v224, v224, v226
	v_mov_b32_e32 v226, 0
	v_mul_f32_e32 v229, v233, v27
	v_sub_f32_e32 v219, v219, v97
	v_mov_b32_dpp v226, v224 row_bcast:31 row_mask:0xc bank_mask:0xf
	v_add_f32_e32 v224, v224, v226
	v_fma_f32 v219, v40, v219, v97
	v_readlane_b32 s0, v224, 63
	v_add_f32_e32 v27, v95, v92
	v_add_f32_e32 v92, v94, v93
	v_max_f32_e64 v224, s0, s0
	v_max_f32_e32 v224, 0x179abe15, v224
	v_rsq_f32_e32 v226, v224
	v_rcp_f32_e32 v224, v86
	v_mul_f32_e32 v86, 0xbfb8aa3b, v87
	v_exp_f32_e32 v232, v86
	v_mul_f32_e32 v226, v218, v226
	v_add_f32_e32 v86, -1.0, v224
	v_fma_f32 v227, v3, v86, 1.0
	v_rcp_f32_e32 v86, v229
	v_sub_f32_e32 v97, v97, v213
	v_sub_f32_e32 v96, v96, v212
	v_xor_b32_e32 v218, 0x80000000, v226
	v_pk_mul_f32 v[86:87], v[222:223], v[86:87] op_sel_hi:[1,0]
	v_pk_mul_f32 v[222:223], v[224:225], v[226:227]
	v_fma_f32 v225, v40, v97, v213
	v_fma_f32 v227, v42, v96, v212
	v_pk_add_f32 v[96:97], v[36:37], v[34:35] neg_lo:[0,1] neg_hi:[0,1]
	v_mul_f32_e32 v37, 0xbfb8aa3b, v92
	v_exp_f32_e32 v37, v37
	v_mul_f32_e64 v93, |v27|, s79
	v_exp_f32_e32 v93, v93
	v_sub_f32_e32 v213, v213, v43
	v_add_f32_e32 v37, 1.0, v37
	v_rcp_f32_e32 v226, v37
	v_add_f32_e32 v93, 1.0, v93
	v_log_f32_e32 v93, v93
	v_fmac_f32_e32 v43, v40, v213
	v_add_f32_e32 v37, -1.0, v226
	v_fma_f32 v231, v3, v37, 1.0
	v_add_f32_e32 v37, v95, v217
	v_mul_f32_e64 v95, |v37|, s79
	v_exp_f32_e32 v95, v95
	v_max_f32_e64 v27, -v27, 0
	v_mul_f32_e32 v92, v28, v227
	v_fmac_f32_e32 v27, 0x3f317218, v93
; __device__ __forceinline__ unsigned cvt_pk_bf16_nat(float lo, float hi) { const f32x2n v = {lo, hi}; return __builtin_bit_cast(unsigned, __builtin_convertvector(v, bf16x2n)); }
; __device__ __forceinline__ float fast_sigmoid(float x) { return __builtin_amdgcn_rcpf(1.0f + __builtin_amdgcn_exp2f(-1.4426950408889634f * x)); }
; __global__ void __launch_bounds__(NTHR, 2) mk_fwd(Args args) {
;     ...
; #pragma unroll
;                     for (int t = 0; t < 16; ++t) {
;                         const float cr = xr_[t + 1], ck = xk_[t + 1], cv = xv_[t + 1], wl = xwl_[t] + c_w0, al = xal_[t] + c_a0;
;                         const float pr_r = xr_[t], pr_k = xk_[t], pr_v = xv_[t];
;                         const float r = cr + (pr_r - cr) * mu_r, k = ck + (pr_k - ck) * mu_k, v = cv + (pr_v - cv) * mu_v;
;                         const float dec = fast_decay(wl), a = fast_sigmoid(al);
;                         float kk = k * c_kk; const float ss = wave_sum_dpp(kk * kk); kk = kk * __builtin_amdgcn_rsqf(fmaxf(ss, 1e-24f));
;                         const float k2 = k * (1.0f + (a - 1.0f) * c_ka), bb = kk * a;
;                         const float Wprev = Wc; Wc = Wc * dec; const float iw = __builtin_amdgcn_rcpf(Wc);
;                         At[t] = -kk * Wprev; Rt[t] = r * Wc; Bt[t] = bb * iw; Kt[t] = k2 * iw; Vt[t] = v;
;                     }
; #pragma unroll
;                     for (int t = 0; t < 16; ++t) {
;                         const unsigned ar_ = cvt_pk_bf16_nat(At[t], Rt[t]), bk_ = cvt_pk_bf16_nat(Bt[t], Kt[t]); const bf16 ab = (bf16)ar_, rb = (bf16)(ar_ >> 16);
;                         IMG[0 * 1152 + t * 72 + pos] = ab; IMG[1 * 1152 + t * 72 + pos] = rb; IMG[2 * 1152 + t * 72 + pos] = (bf16)bk_; IMG[3 * 1152 + t * 72 + pos] = (bf16)(bk_ >> 16);
;                     }
	v_add_f32_e32 v40, 1.0, v95
	v_sub_f32_e32 v95, v212, v41
	v_fmac_f32_e32 v41, v42, v95
	v_mul_f32_e32 v93, v92, v92
	v_mul_f32_e32 v28, v28, v41
	v_mul_f32_e32 v42, v28, v28
	v_mov_b32_dpp v93, v93 quad_perm:[1,0,3,2] row_mask:0xf bank_mask:0xf bound_ctrl:1
	v_fmac_f32_e32 v93, v92, v92
	v_log_f32_e32 v40, v40
	v_mov_b32_dpp v42, v42 quad_perm:[1,0,3,2] row_mask:0xf bank_mask:0xf bound_ctrl:1
	v_add_f32_dpp v93, v93, v93 quad_perm:[2,3,0,1] row_mask:0xf bank_mask:0xf bound_ctrl:1
	v_fmac_f32_e32 v42, v28, v28
	v_mov_b32_e32 v224, 0
	v_add_f32_dpp v93, v93, v93 row_half_mirror row_mask:0xf bank_mask:0xf bound_ctrl:1
	v_add_f32_dpp v42, v42, v42 quad_perm:[2,3,0,1] row_mask:0xf bank_mask:0xf bound_ctrl:1
	v_add_f32_e32 v94, v94, v216
	v_add_f32_dpp v93, v93, v93 row_mirror row_mask:0xf bank_mask:0xf bound_ctrl:1
	v_max_f32_e64 v37, -v37, 0
	v_add_f32_dpp v42, v42, v42 row_half_mirror row_mask:0xf bank_mask:0xf bound_ctrl:1
	v_mov_b32_dpp v224, v93 row_bcast:15 row_mask:0xa bank_mask:0xf
	v_fmac_f32_e32 v37, 0x3f317218, v40
	v_mul_f32_e32 v40, 0xbfb8aa3b, v94
	v_add_f32_dpp v42, v42, v42 row_mirror row_mask:0xf bank_mask:0xf bound_ctrl:1
	v_mov_b32_e32 v94, 0
	v_add_f32_e32 v93, v93, v224
	v_mov_b32_e32 v224, 0
	v_mov_b32_dpp v94, v42 row_bcast:15 row_mask:0xa bank_mask:0xf
	v_add_f32_e32 v42, v42, v94
	v_mov_b32_dpp v224, v93 row_bcast:31 row_mask:0xc bank_mask:0xf
	v_mov_b32_e32 v94, 0
	v_add_f32_e32 v27, 0.5, v27
	v_add_f32_e32 v93, v93, v224
	v_exp_f32_e32 v40, v40
	v_mov_b32_dpp v94, v42 row_bcast:31 row_mask:0xc bank_mask:0xf
	v_mul_f32_e32 v27, 0xbfb8aa3b, v27
	v_readlane_b32 s0, v93, 63
	v_add_f32_e32 v42, v42, v94
	v_exp_f32_e32 v27, v27
	v_max_f32_e64 v93, s0, s0
	v_readlane_b32 s0, v42, 63
	v_add_f32_e32 v40, 1.0, v40
	v_rcp_f32_e32 v40, v40
	v_max_f32_e64 v42, s0, s0
	v_max_f32_e32 v42, 0x179abe15, v42
	v_rsq_f32_e32 v42, v42
	v_mul_f32_e32 v27, 0xbfb8aa3b, v27
	v_exp_f32_e32 v27, v27
	v_xor_b32_e32 v220, 0x80000000, v228
	v_mul_f32_e32 v212, v28, v42
	v_add_f32_e32 v28, -1.0, v40
	v_mov_b32_e32 v228, v233
	v_mul_f32_e32 v233, v229, v232
	v_fma_f32 v213, v3, v28, 1.0
	v_cvt_pk_bf16_f32 v3, v214, v215
	v_add_f32_e32 v37, 0.5, v37
	v_mul_f32_e32 v217, v233, v27
	v_cvt_pk_bf16_f32 v27, v38, v39
	ds_write_b16 v101, v3
	ds_write_b16_d16_hi v101, v3 offset:2304
	ds_write_b16 v101, v27 offset:4608
	ds_write_b16_d16_hi v101, v27 offset:6912
	v_cvt_pk_bf16_f32 v3, v50, v51
	v_mul_f32_e32 v37, 0xbfb8aa3b, v37
	v_cvt_pk_bf16_f32 v27, v44, v45
	ds_write_b16 v101, v3 offset:144
	ds_write_b16_d16_hi v101, v3 offset:2448
	ds_write_b16 v101, v27 offset:4752
	ds_write_b16_d16_hi v101, v27 offset:7056
	v_cvt_pk_bf16_f32 v3, v54, v55
	v_max_f32_e32 v93, 0x179abe15, v93
	v_exp_f32_e32 v37, v37
	v_cvt_pk_bf16_f32 v27, v46, v47
	ds_write_b16 v101, v3 offset:288
	ds_write_b16_d16_hi v101, v3 offset:2592
	ds_write_b16 v101, v27 offset:4896
	ds_write_b16_d16_hi v101, v27 offset:7200
	v_cvt_pk_bf16_f32 v3, v60, v61
	v_rsq_f32_e32 v93, v93
	v_cvt_pk_bf16_f32 v27, v48, v49
	ds_write_b16 v101, v3 offset:432
	ds_write_b16_d16_hi v101, v3 offset:2736
	ds_write_b16 v101, v27 offset:5040
	ds_write_b16_d16_hi v101, v27 offset:7344
	v_cvt_pk_bf16_f32 v3, v64, v65
	v_cvt_pk_bf16_f32 v27, v52, v53
	ds_write_b16 v101, v3 offset:576
	ds_write_b16_d16_hi v101, v3 offset:2880
	ds_write_b16 v101, v27 offset:5184
	ds_write_b16_d16_hi v101, v27 offset:7488
	v_cvt_pk_bf16_f32 v3, v68, v69
	v_cvt_pk_bf16_f32 v27, v56, v57
	ds_write_b16 v101, v3 offset:720
	ds_write_b16_d16_hi v101, v3 offset:3024
	ds_write_b16 v101, v27 offset:5328
	ds_write_b16_d16_hi v101, v27 offset:7632
	v_cvt_pk_bf16_f32 v3, v72, v73
	v_mul_f32_e32 v37, 0xbfb8aa3b, v37
	v_cvt_pk_bf16_f32 v27, v62, v63
	ds_write_b16 v101, v3 offset:864
	ds_write_b16_d16_hi v101, v3 offset:3168
	ds_write_b16 v101, v27 offset:5472
	ds_write_b16_d16_hi v101, v27 offset:7776
	v_cvt_pk_bf16_f32 v3, v76, v77
	v_mul_f32_e32 v230, v92, v93
	v_rcp_f32_e32 v92, v233
	v_exp_f32_e32 v37, v37
	v_cvt_pk_bf16_f32 v27, v66, v67
	ds_write_b16 v101, v3 offset:1008
	ds_write_b16_d16_hi v101, v3 offset:3312
	ds_write_b16 v101, v27 offset:5616
	ds_write_b16_d16_hi v101, v27 offset:7920
	v_cvt_pk_bf16_f32 v3, v80, v81
	v_rcp_f32_e32 v28, v217
	v_cvt_pk_bf16_f32 v27, v70, v71
	ds_write_b16 v101, v3 offset:1152
	ds_write_b16_d16_hi v101, v3 offset:3456
	ds_write_b16 v101, v27 offset:5760
	ds_write_b16_d16_hi v101, v27 offset:8064
	v_cvt_pk_bf16_f32 v3, v82, v83
	v_cvt_pk_bf16_f32 v27, v74, v75
	ds_write_b16 v101, v3 offset:1296
	ds_write_b16_d16_hi v101, v3 offset:3600
	ds_write_b16 v101, v27 offset:5904
	ds_write_b16_d16_hi v101, v27 offset:8208
	v_cvt_pk_bf16_f32 v3, v88, v89
	v_pk_mul_f32 v[220:221], v[228:229], v[220:221]
	v_mov_b32_e32 v232, v229
	v_cvt_pk_bf16_f32 v27, v78, v79
	ds_write_b16 v101, v3 offset:1440
	ds_write_b16_d16_hi v101, v3 offset:3744
	ds_write_b16 v101, v27 offset:6048
	ds_write_b16_d16_hi v101, v27 offset:8352
	v_cvt_pk_bf16_f32 v3, v90, v91
	v_xor_b32_e32 v224, 0x80000000, v230
	v_pk_mul_f32 v[218:219], v[232:233], v[218:219]
	v_pk_mul_f32 v[92:93], v[222:223], v[92:93] op_sel_hi:[1,0]
	v_pk_mul_f32 v[222:223], v[226:227], v[230:231]
	v_mov_b32_e32 v216, v233
	v_mul_f32_e32 v95, v217, v37
	v_cvt_pk_bf16_f32 v27, v84, v85
	ds_write_b16 v101, v3 offset:1584
	ds_write_b16_d16_hi v101, v3 offset:3888
	ds_write_b16 v101, v27 offset:6192
	ds_write_b16_d16_hi v101, v27 offset:8496
	v_cvt_pk_bf16_f32 v3, v220, v221
	v_xor_b32_e32 v42, 0x80000000, v212
	v_pk_mul_f32 v[224:225], v[216:217], v[224:225]
	v_pk_mul_f32 v[222:223], v[222:223], v[28:29] op_sel_hi:[1,0]
	v_rcp_f32_e32 v28, v95
	v_mov_b32_e32 v94, v217
; #define GAS __attribute__((address_space(1)))
; __device__ __forceinline__ unsigned cvt_pk_bf16_nat(float lo, float hi) { const f32x2n v = {lo, hi}; return __builtin_bit_cast(unsigned, __builtin_convertvector(v, bf16x2n)); }
; __device__ __forceinline__ unsigned pk2(float lo, float hi) { return cvt_pk_bf16_nat(lo, hi); }
; __global__ void __launch_bounds__(NTHR, 2) mk_fwd(Args args) {
;     ...
;                     for (int t = 0; t < 16; ++t) {
;                         const unsigned ar_ = cvt_pk_bf16_nat(At[t], Rt[t]), bk_ = cvt_pk_bf16_nat(Bt[t], Kt[t]); const bf16 ab = (bf16)ar_, rb = (bf16)(ar_ >> 16);
;                         IMG[0 * 1152 + t * 72 + pos] = ab; IMG[1 * 1152 + t * 72 + pos] = rb; IMG[2 * 1152 + t * 72 + pos] = (bf16)bk_; IMG[3 * 1152 + t * 72 + pos] = (bf16)(bk_ >> 16);
;                     }
; #pragma unroll
;                     for (int qq = 0; qq < 4; ++qq) { v4u o; o.x = pk2(Bt[4 * qq] * Wc, Bt[4 * qq + 1] * Wc); o.y = pk2(Bt[4 * qq + 2] * Wc, Bt[4 * qq + 3] * Wc); o.z = pk2(Kt[4 * qq] * Wc, Kt[4 * qq + 1] * Wc); o.w = pk2(Kt[4 * qq + 2] * Wc, Kt[4 * qq + 3] * Wc);
;                         *(GAS v4u*)(pk + PK_BK + j * 64 + qq * 16) = o; }
; #pragma unroll
;                     for (int g = 0; g < 2; ++g) { v4u o; o.x = pk2(Vt[8 * g], Vt[8 * g + 1]); o.y = pk2(Vt[8 * g + 2], Vt[8 * g + 3]); o.z = pk2(Vt[8 * g + 4], Vt[8 * g + 5]); o.w = pk2(Vt[8 * g + 6], Vt[8 * g + 7]);
;                         *(GAS v4u*)(pk + PK_VT + j * 32 + g * 16) = o; }
;                     ((GAS float*)(pk + PK_WC))[j] = Wc;
	v_cvt_pk_bf16_f32 v27, v86, v87
	ds_write_b16 v101, v3 offset:1728
	ds_write_b16_d16_hi v101, v3 offset:4032
	ds_write_b16 v101, v27 offset:6336
	ds_write_b16_d16_hi v101, v27 offset:8640
	v_cvt_pk_bf16_f32 v3, v218, v219
	v_pk_mul_f32 v[42:43], v[94:95], v[42:43]
	v_cvt_pk_bf16_f32 v27, v92, v93
	ds_write_b16 v101, v3 offset:1872
	ds_write_b16_d16_hi v101, v3 offset:4176
	ds_write_b16 v101, v27 offset:6480
	ds_write_b16_d16_hi v101, v27 offset:8784
	v_cvt_pk_bf16_f32 v3, v224, v225
	v_cvt_pk_bf16_f32 v27, v222, v223
	ds_write_b16 v101, v3 offset:2016
	ds_write_b16_d16_hi v101, v3 offset:4320
	ds_write_b16 v101, v27 offset:6624
	ds_write_b16_d16_hi v101, v27 offset:8928
	v_cvt_pk_bf16_f32 v3, v42, v43
	v_mov_b32_e32 v42, v5
	v_mov_b32_e32 v43, v20
	v_pk_mul_f32 v[40:41], v[40:41], v[212:213]
	v_pk_add_f32 v[4:5], v[4:5], v[42:43] neg_lo:[0,1] neg_hi:[0,1]
	v_pk_mul_f32 v[40:41], v[40:41], v[28:29] op_sel_hi:[1,0]
	v_pk_fma_f32 v[42:43], v[2:3], v[4:5], v[42:43] op_sel_hi:[0,1,1]
	v_pk_mov_b32 v[4:5], v[20:21], v[22:23] op_sel:[1,0]
	v_cvt_pk_bf16_f32 v27, v40, v41
	v_pk_add_f32 v[20:21], v[20:21], v[4:5] neg_lo:[0,1] neg_hi:[0,1]
	v_mov_b32_e32 v28, v25
	v_pk_fma_f32 v[20:21], v[2:3], v[20:21], v[4:5] op_sel_hi:[0,1,1]
	v_pk_mov_b32 v[4:5], v[22:23], v[26:27] op_sel:[1,0]
	ds_write_b16 v101, v3 offset:2160
	ds_write_b16_d16_hi v101, v3 offset:4464
	ds_write_b16 v101, v27 offset:6768
	ds_write_b16_d16_hi v101, v27 offset:9072
	v_pk_add_f32 v[22:23], v[22:23], v[4:5] neg_lo:[0,1] neg_hi:[0,1]
	v_pk_fma_f32 v[26:27], v[2:3], v[58:59], v[24:25] op_sel_hi:[0,1,1]
	v_pk_fma_f32 v[22:23], v[2:3], v[22:23], v[4:5] op_sel_hi:[0,1,1]
	v_mov_b32_e32 v4, v29
	v_mov_b32_e32 v5, v30
	v_pk_add_f32 v[24:25], v[28:29], v[4:5] neg_lo:[0,1] neg_hi:[0,1]
	v_mov_b32_e32 v50, v95
	v_pk_fma_f32 v[24:25], v[2:3], v[24:25], v[4:5] op_sel_hi:[0,1,1]
	v_pk_mov_b32 v[4:5], v[30:31], v[32:33] op_sel:[1,0]
	s_mov_b64 s[0:1], 0x1c00
	v_pk_add_f32 v[28:29], v[30:31], v[4:5] neg_lo:[0,1] neg_hi:[0,1]
	s_mov_b32 s34, 0
	v_pk_fma_f32 v[28:29], v[2:3], v[28:29], v[4:5] op_sel_hi:[0,1,1]
	v_pk_mov_b32 v[4:5], v[32:33], v[36:37] op_sel:[1,0]
	s_nop 0
	v_pk_add_f32 v[30:31], v[32:33], v[4:5] neg_lo:[0,1] neg_hi:[0,1]
	v_pk_fma_f32 v[32:33], v[2:3], v[96:97], v[34:35] op_sel_hi:[0,1,1]
	v_pk_fma_f32 v[30:31], v[2:3], v[30:31], v[4:5] op_sel_hi:[0,1,1]
	v_mov_b32_e32 v2, v38
	v_mov_b32_e32 v3, v44
	v_mov_b32_e32 v4, v46
	v_mov_b32_e32 v5, v48
.Lpr_slot_poll:
	v_mov_b32_e32 v34, 0x27390
	ds_read_b32 v35, v34
	ds_read_b32 v34, v34 offset:4
	s_waitcnt lgkmcnt(0)
	v_min_u32_e32 v35, v35, v34
	v_mov_b32_e32 v34, 0x27398
	ds_read_b32 v34, v34
	s_waitcnt lgkmcnt(0)
	v_min_u32_e32 v35, v35, v34
	v_mov_b32_e32 v34, 0x2739c
	ds_read_b32 v34, v34
	s_waitcnt lgkmcnt(0)
	v_min_u32_e32 v35, v35, v34
	v_cmp_le_i32_e32 vcc, s99, v35
	s_cbranch_vccnz .Lpr_slot_ok
	s_sleep 0
	s_branch .Lpr_slot_poll
.Lpr_slot_ok:
	v_lshl_add_u64 v[34:35], s[88:89], 0, v[8:9]
	v_pk_mul_f32 v[2:3], v[50:51], v[2:3] op_sel_hi:[0,1]
	v_pk_mul_f32 v[4:5], v[50:51], v[4:5] op_sel_hi:[0,1]
	v_mov_b32_e32 v44, v39
	v_mov_b32_e32 v48, v47
	v_lshl_add_u64 v[36:37], v[34:35], 0, s[0:1]
	v_cvt_pk_bf16_f32 v2, v2, v3
	v_cvt_pk_bf16_f32 v3, v4, v5
	v_pk_mul_f32 v[4:5], v[50:51], v[44:45] op_sel_hi:[0,1]
	v_pk_mul_f32 v[38:39], v[50:51], v[48:49] op_sel_hi:[0,1]
	v_add_co_u32_e32 v34, vcc, s36, v34
	v_cvt_pk_bf16_f32 v4, v4, v5
	v_cvt_pk_bf16_f32 v5, v38, v39
	v_addc_co_u32_e32 v35, vcc, 0, v35, vcc
	ds_write_b128 v34, v[2:5] offset:3072
	s_mov_b64 s[0:1], 0x2c00
	s_nop 0
	v_mov_b32_e32 v2, v52
	v_mov_b32_e32 v3, v56
	v_mov_b32_e32 v4, v62
	v_mov_b32_e32 v5, v66
	v_pk_mul_f32 v[2:3], v[50:51], v[2:3] op_sel_hi:[0,1]
	v_pk_mul_f32 v[4:5], v[50:51], v[4:5] op_sel_hi:[0,1]
	v_mov_b32_e32 v56, v53
	v_mov_b32_e32 v66, v63
	v_cvt_pk_bf16_f32 v2, v2, v3
	v_cvt_pk_bf16_f32 v3, v4, v5
	v_pk_mul_f32 v[4:5], v[50:51], v[56:57] op_sel_hi:[0,1]
	v_pk_mul_f32 v[34:35], v[50:51], v[66:67] op_sel_hi:[0,1]
	v_cvt_pk_bf16_f32 v4, v4, v5
	v_cvt_pk_bf16_f32 v5, v34, v35
	ds_write_b128 v36, v[2:5] offset:16
	s_nop 1
	v_mov_b32_e32 v2, v70
	v_mov_b32_e32 v3, v74
	v_mov_b32_e32 v4, v78
	v_mov_b32_e32 v5, v84
	v_pk_mul_f32 v[2:3], v[50:51], v[2:3] op_sel_hi:[0,1]
	v_pk_mul_f32 v[4:5], v[50:51], v[4:5] op_sel_hi:[0,1]
	v_mov_b32_e32 v74, v71
	v_mov_b32_e32 v84, v79
	v_cvt_pk_bf16_f32 v2, v2, v3
	v_cvt_pk_bf16_f32 v3, v4, v5
	v_pk_mul_f32 v[4:5], v[50:51], v[74:75] op_sel_hi:[0,1]
	v_pk_mul_f32 v[34:35], v[50:51], v[84:85] op_sel_hi:[0,1]
	v_cvt_pk_bf16_f32 v4, v4, v5
	v_cvt_pk_bf16_f32 v5, v34, v35
	ds_write_b128 v36, v[2:5] offset:32
	s_nop 1
	v_mov_b32_e32 v2, v86
	v_mov_b32_e32 v3, v92
	v_mov_b32_e32 v4, v222
	v_mov_b32_e32 v5, v40
	v_pk_mul_f32 v[2:3], v[50:51], v[2:3] op_sel_hi:[0,1]
	v_pk_mul_f32 v[4:5], v[50:51], v[4:5] op_sel_hi:[0,1]
	v_mov_b32_e32 v92, v87
	v_mov_b32_e32 v40, v223
	v_cvt_pk_bf16_f32 v2, v2, v3
	v_cvt_pk_bf16_f32 v3, v4, v5
	v_pk_mul_f32 v[4:5], v[50:51], v[92:93] op_sel_hi:[0,1]
	v_pk_mul_f32 v[34:35], v[50:51], v[40:41] op_sel_hi:[0,1]
	v_cvt_pk_bf16_f32 v4, v4, v5
	v_cvt_pk_bf16_f32 v5, v34, v35
	v_lshl_add_u64 v[34:35], s[88:89], 0, v[10:11]
	ds_write_b128 v36, v[2:5] offset:48
	v_lshl_add_u64 v[36:37], v[34:35], 0, s[0:1]
	s_nop 0
	v_cvt_pk_bf16_f32 v3, v20, v21
	v_add_co_u32_e32 v20, vcc, s37, v34
	v_cvt_pk_bf16_f32 v2, v42, v43
	v_cvt_pk_bf16_f32 v4, v22, v23
	v_cvt_pk_bf16_f32 v5, v26, v27
	v_addc_co_u32_e32 v21, vcc, 0, v35, vcc
	ds_write_b128 v20, v[2:5] offset:3072
	s_nop 1
	v_cvt_pk_bf16_f32 v2, v24, v25
	v_cvt_pk_bf16_f32 v3, v28, v29
	v_cvt_pk_bf16_f32 v4, v30, v31
	v_cvt_pk_bf16_f32 v5, v32, v33
	ds_write_b128 v36, v[2:5] offset:16
	s_nop 1
	v_lshl_add_u64 v[2:3], s[88:89], 0, v[6:7]
	v_add_co_u32_e32 v2, vcc, s38, v2
	s_nop 1
	v_addc_co_u32_e32 v3, vcc, 0, v3, vcc
	ds_write_b32 v2, v95 offset:1024
	s_waitcnt lgkmcnt(0)
; #define GAS __attribute__((address_space(1)))
; __global__ void __launch_bounds__(NTHR, 2) mk_fwd(Args args) {
;     ...
;                     asm volatile("s_waitcnt lgkmcnt(0)" ::: "memory");
; #pragma unroll
;                     for (int i = 0; i < 2; ++i) { const int p_ = lane + 64 * i, off_ = (p_ >> 3) * 72 + (p_ & 7) * 8;
;                         *(GAS v4u*)(pk + PK_PA + p_ * 16) = *(const LAS v4u*)(IMG + 0 * 1152 + off_); *(GAS v4u*)(pk + PK_PR + p_ * 16) = *(const LAS v4u*)(IMG + 1 * 1152 + off_); }
;                     const bf16x8 fa0 = *(const LAS bf16x8*)(IMG + 0 * 1152 + tr * 72 + 8 * q), fa1 = *(const LAS bf16x8*)(IMG + 0 * 1152 + tr * 72 + 32 + 8 * q);
;                     const bf16x8 fr0 = *(const LAS bf16x8*)(IMG + 1 * 1152 + tr * 72 + 8 * q), fr1 = *(const LAS bf16x8*)(IMG + 1 * 1152 + tr * 72 + 32 + 8 * q);
;                     const bf16x8 fb0 = *(const LAS bf16x8*)(IMG + 2 * 1152 + tr * 72 + 8 * q), fb1 = *(const LAS bf16x8*)(IMG + 2 * 1152 + tr * 72 + 32 + 8 * q);
;                     const bf16x8 fk0 = *(const LAS bf16x8*)(IMG + 3 * 1152 + tr * 72 + 8 * q), fk1 = *(const LAS bf16x8*)(IMG + 3 * 1152 + tr * 72 + 32 + 8 * q);
;                     const f32x4 z4 = (f32x4){0.f, 0.f, 0.f, 0.f};
;                     f32x4 PT = __builtin_amdgcn_mfma_f32_16x16x32_bf16(fa0, fb0, z4, 0, 0, 0); PT = __builtin_amdgcn_mfma_f32_16x16x32_bf16(fa1, fb1, PT, 0, 0, 0);
;                     f32x4 QT = __builtin_amdgcn_mfma_f32_16x16x32_bf16(fa0, fk0, z4, 0, 0, 0); QT = __builtin_amdgcn_mfma_f32_16x16x32_bf16(fa1, fk1, QT, 0, 0, 0);
;                     f32x4 GB = __builtin_amdgcn_mfma_f32_16x16x32_bf16(fr0, fb0, z4, 0, 0, 0); GB = __builtin_amdgcn_mfma_f32_16x16x32_bf16(fr1, fb1, GB, 0, 0, 0);
;                     f32x4 GK = __builtin_amdgcn_mfma_f32_16x16x32_bf16(fr0, fk0, z4, 0, 0, 0); GK = __builtin_amdgcn_mfma_f32_16x16x32_bf16(fr1, fk1, GK, 0, 0, 0);
;                     const int s_ = tr, rec = (s_ >> 2) * 8 + (s_ & 3);
; #pragma unroll
;                     for (int e = 0; e < 4; ++e) { const int t = 4 * q + e;
;                         const float qv = s_ < t ? QT[e] : 0.f, gb = s_ <= t ? GB[e] : 0.f, gk = s_ <= t ? GK[e] : 0.f;
;                         QGT[t * 32 + rec] = (bf16)f2bf(qv);
;                         QGT[512 + t * 32 + rec] = (bf16)f2bf(gb); QGT[512 + t * 32 + rec + 4] = (bf16)f2bf(gk); }
	ds_read_b128 v[20:23], v98
	ds_read_b128 v[24:27], v98 offset:64
	ds_read_b128 v[28:31], v98 offset:4608
	ds_read_b128 v[32:35], v98 offset:4672
	ds_read_b128 v[36:39], v98 offset:6912
	ds_read_b128 v[40:43], v98 offset:6976
	ds_read_b128 v[44:47], v98 offset:2304
	s_waitcnt lgkmcnt(4)
	v_mfma_f32_16x16x32_bf16 v[2:5], v[20:23], v[28:31], 0
	ds_read_b128 v[48:51], v98 offset:2368
	ds_read_b128 v[52:55], v102
	ds_read_b128 v[56:59], v102 offset:2304
	s_waitcnt lgkmcnt(5)
	v_mfma_f32_16x16x32_bf16 v[20:23], v[20:23], v[36:39], 0
	v_mfma_f32_16x16x32_bf16 v[2:5], v[24:27], v[32:35], v[2:5]
	s_waitcnt lgkmcnt(4)
	v_mfma_f32_16x16x32_bf16 v[22:25], v[24:27], v[40:43], v[20:23]
	s_waitcnt lgkmcnt(3)
	v_mfma_f32_16x16x32_bf16 v[26:29], v[44:47], v[28:31], 0
	s_nop 2
	v_lshl_add_u64 v[20:21], s[88:89], 0, v[12:13]
	s_waitcnt lgkmcnt(1)
	ds_write_b128 v20, v[52:55]
	v_cvt_pk_bf16_f32 v22, v22, s0
	v_mfma_f32_16x16x32_bf16 v[26:29], v[48:51], v[32:35], v[26:29]
	ds_read_b128 v[30:33], v103
	ds_read_b128 v[52:55], v103 offset:2304
	s_waitcnt lgkmcnt(2)
	ds_write_b128 v20, v[56:59] offset:2048
	v_cndmask_b32_e64 v22, 0, v22, s[4:5]
	v_mfma_f32_16x16x32_bf16 v[34:37], v[44:47], v[36:39], 0
	v_lshl_add_u64 v[38:39], s[88:89], 0, v[18:19]
	s_waitcnt lgkmcnt(1)
	ds_write_b128 v38, v[30:33]
	s_waitcnt lgkmcnt(0)
	ds_write_b128 v38, v[52:55] offset:2048
	ds_write_b16 v121, v22 offset:10240
	v_mfma_f32_16x16x32_bf16 v[30:33], v[48:51], v[40:43], v[34:37]
	v_cvt_pk_bf16_f32 v22, v26, s0
	v_cndmask_b32_e64 v22, v22, 0, s[6:7]
	ds_write_b16 v121, v22 offset:11264
	s_nop 4
	v_cvt_pk_bf16_f32 v22, v30, s0
	v_cndmask_b32_e64 v22, v22, 0, s[6:7]
	ds_write_b16 v121, v22 offset:11272
	v_cvt_pk_bf16_f32 v22, v23, s0
	v_cndmask_b32_e64 v22, v22, 0, s[6:7]
	ds_write_b16 v122, v22 offset:10240
	v_cvt_pk_bf16_f32 v22, v27, s0
	v_cndmask_b32_e64 v22, v22, 0, s[8:9]
	ds_write_b16 v122, v22 offset:11264
	v_cvt_pk_bf16_f32 v22, v31, s0
	v_cndmask_b32_e64 v22, v22, 0, s[8:9]
	ds_write_b16 v122, v22 offset:11272
	v_cvt_pk_bf16_f32 v22, v24, s0
	v_cndmask_b32_e64 v22, 0, v22, s[10:11]
	ds_write_b16 v123, v22 offset:10240
	v_cvt_pk_bf16_f32 v22, v28, s0
	v_cndmask_b32_e64 v22, v22, 0, s[12:13]
	ds_write_b16 v123, v22 offset:11264
	v_cvt_pk_bf16_f32 v22, v32, s0
	v_cndmask_b32_e64 v22, v22, 0, s[12:13]
	ds_write_b16 v123, v22 offset:11272
	v_cvt_pk_bf16_f32 v22, v25, s0
	v_cndmask_b32_e64 v22, 0, v22, s[14:15]
	ds_write_b16 v124, v22 offset:10240
	v_cvt_pk_bf16_f32 v22, v29, s0
	v_cndmask_b32_e64 v22, v22, 0, s[16:17]
	ds_write_b16 v124, v22 offset:11264
	v_cvt_pk_bf16_f32 v22, v33, s0
	v_cndmask_b32_e64 v22, v22, 0, s[16:17]
	s_mov_b32 s0, 0
	ds_write_b16 v124, v22 offset:11272
	s_mov_b32 s0, 0
	s_nop 0
	v_readlane_b32 s0, v3, s0
	s_nop 1
	v_fma_f32 v22, s0, v104, v105
	s_mov_b32 s0, 0
	s_nop 0
	v_readlane_b32 s1, v4, s0
	s_add_i32 s0, s0, 1
	v_readlane_b32 s0, v4, s0
	v_fma_f32 v23, s1, v104, v106
	s_nop 0
	v_fmac_f32_e32 v23, s0, v22
	s_mov_b32 s0, 0
	s_nop 0
	v_readlane_b32 s1, v5, s0
	s_nop 1
	v_fma_f32 v24, s1, v104, v107
	s_add_i32 s1, s0, 1
	v_readlane_b32 s1, v5, s1
	s_add_i32 s0, s0, 2
	v_readlane_b32 s0, v5, s0
	v_fmac_f32_e32 v24, s1, v22
	s_nop 0
	v_fmac_f32_e32 v24, s0, v23
	s_mov_b32 s0, 0
	s_add_i32 s1, s0, 16
	v_readlane_b32 s1, v2, s1
	s_nop 1
	v_fma_f32 v25, s1, v104, v108
	s_add_i32 s1, s0, 17
	v_readlane_b32 s1, v2, s1
	s_nop 1
	v_fmac_f32_e32 v25, s1, v22
	s_add_i32 s1, s0, 18
	v_readlane_b32 s1, v2, s1
	s_add_i32 s0, s0, 19
	v_readlane_b32 s0, v2, s0
	v_fmac_f32_e32 v25, s1, v23
	s_nop 0
	v_fmac_f32_e32 v25, s0, v24
	s_mov_b32 s0, 0
	s_add_i32 s1, s0, 16
	v_readlane_b32 s1, v3, s1
	s_nop 1
	v_fma_f32 v26, s1, v104, v109
	s_add_i32 s1, s0, 17
	v_readlane_b32 s1, v3, s1
	s_nop 1
	v_fmac_f32_e32 v26, s1, v22
	s_add_i32 s1, s0, 18
	v_readlane_b32 s1, v3, s1
	s_nop 1
	v_fmac_f32_e32 v26, s1, v23
	s_add_i32 s1, s0, 19
	v_readlane_b32 s1, v3, s1
	s_add_i32 s0, s0, 20
	v_readlane_b32 s0, v3, s0
	v_fmac_f32_e32 v26, s1, v24
	s_nop 0
	v_fmac_f32_e32 v26, s0, v25
	s_mov_b32 s0, 0
	s_add_i32 s1, s0, 16
	v_readlane_b32 s1, v4, s1
	s_nop 1
	v_fma_f32 v27, s1, v104, v110
	s_add_i32 s1, s0, 17
	v_readlane_b32 s1, v4, s1
	s_nop 1
	v_fmac_f32_e32 v27, s1, v22
	s_add_i32 s1, s0, 18
	v_readlane_b32 s1, v4, s1
	s_nop 1
	v_fmac_f32_e32 v27, s1, v23
	s_add_i32 s1, s0, 19
	v_readlane_b32 s1, v4, s1
	s_nop 1
	v_fmac_f32_e32 v27, s1, v24
	s_add_i32 s1, s0, 20
	v_readlane_b32 s1, v4, s1
	s_add_i32 s0, s0, 21
	v_readlane_b32 s0, v4, s0
	v_fmac_f32_e32 v27, s1, v25
	s_nop 0
	v_fmac_f32_e32 v27, s0, v26
	s_mov_b32 s0, 0
	s_add_i32 s1, s0, 16
	v_readlane_b32 s1, v5, s1
	s_nop 1
	v_fma_f32 v28, s1, v104, v111
	s_add_i32 s1, s0, 17
	v_readlane_b32 s1, v5, s1
	s_nop 1
	v_fmac_f32_e32 v28, s1, v22
	s_add_i32 s1, s0, 18
	v_readlane_b32 s1, v5, s1
	s_nop 1
	v_fmac_f32_e32 v28, s1, v23
	s_add_i32 s1, s0, 19
	v_readlane_b32 s1, v5, s1
	s_nop 1
	v_fmac_f32_e32 v28, s1, v24
	s_add_i32 s1, s0, 20
	v_readlane_b32 s1, v5, s1
	s_nop 1
	v_fmac_f32_e32 v28, s1, v25
	s_add_i32 s1, s0, 21
	v_readlane_b32 s1, v5, s1
	s_add_i32 s0, s0, 22
	v_readlane_b32 s0, v5, s0
	v_fmac_f32_e32 v28, s1, v26
	s_nop 0
	v_fmac_f32_e32 v28, s0, v27
	s_mov_b32 s0, 0
	s_xor_b32 s1, s0, 32
	v_readlane_b32 s1, v2, s1
	s_nop 1
	v_fma_f32 v29, s1, v104, v112
	s_add_i32 s1, s0, 33
	v_readlane_b32 s1, v2, s1
	s_nop 1
	v_fmac_f32_e32 v29, s1, v22
	s_add_i32 s1, s0, 34
	v_readlane_b32 s1, v2, s1
	s_nop 1
	v_fmac_f32_e32 v29, s1, v23
	s_add_i32 s1, s0, 35
	v_readlane_b32 s1, v2, s1
	s_nop 1
	v_fmac_f32_e32 v29, s1, v24
	s_add_i32 s1, s0, 36
	v_readlane_b32 s1, v2, s1
	s_nop 1
	v_fmac_f32_e32 v29, s1, v25
	s_add_i32 s1, s0, 37
; __global__ void __launch_bounds__(NTHR, 2) mk_fwd(Args args) {
;     ...
;                     float Tr[16]; const pg8::v4i_t PTi = __builtin_bit_cast(pg8::v4i_t, PT);
; #pragma unroll
;                     for (int t = 0; t < 16; ++t) { float acc = (t == s_) ? 1.f : 0.f;
;                         int zt_ = 0; { const float dep_ = t > 0 ? Tr[t > 0 ? t - 1 : 0] : 0.f; asm volatile("" : "+s"(zt_) : "v"(dep_)); }
; #pragma unroll
;                         for (int r = 0; r < t; ++r) acc = __builtin_fmaf(__int_as_float(__builtin_amdgcn_readlane(PTi[t & 3], 16 * (t >> 2) + r + zt_)), Tr[r], acc);
;                         Tr[t] = acc; }
	v_readlane_b32 s1, v2, s1
	s_nop 1
	v_fmac_f32_e32 v29, s1, v26
	s_add_i32 s1, s0, 38
	v_readlane_b32 s1, v2, s1
	s_add_i32 s0, s0, 39
	v_readlane_b32 s0, v2, s0
	v_fmac_f32_e32 v29, s1, v27
	s_nop 0
	v_fmac_f32_e32 v29, s0, v28
	s_mov_b32 s0, 0
	s_xor_b32 s1, s0, 32
	v_readlane_b32 s1, v3, s1
	s_nop 1
	v_fma_f32 v30, s1, v104, v113
	s_add_i32 s1, s0, 33
	v_readlane_b32 s1, v3, s1
	s_nop 1
	v_fmac_f32_e32 v30, s1, v22
	s_add_i32 s1, s0, 34
	v_readlane_b32 s1, v3, s1
	s_nop 1
	v_fmac_f32_e32 v30, s1, v23
	s_add_i32 s1, s0, 35
	v_readlane_b32 s1, v3, s1
	s_nop 1
	v_fmac_f32_e32 v30, s1, v24
	s_add_i32 s1, s0, 36
	v_readlane_b32 s1, v3, s1
	s_nop 1
	v_fmac_f32_e32 v30, s1, v25
	s_add_i32 s1, s0, 37
	v_readlane_b32 s1, v3, s1
	s_nop 1
	v_fmac_f32_e32 v30, s1, v26
	s_add_i32 s1, s0, 38
	v_readlane_b32 s1, v3, s1
	s_nop 1
	v_fmac_f32_e32 v30, s1, v27
	s_add_i32 s1, s0, 39
	v_readlane_b32 s1, v3, s1
	s_add_i32 s0, s0, 40
	v_readlane_b32 s0, v3, s0
	v_fmac_f32_e32 v30, s1, v28
	s_nop 0
	v_fmac_f32_e32 v30, s0, v29
	s_mov_b32 s0, 0
	s_xor_b32 s1, s0, 32
	v_readlane_b32 s1, v4, s1
	s_nop 1
	v_fma_f32 v31, s1, v104, v114
	s_add_i32 s1, s0, 33
	v_readlane_b32 s1, v4, s1
	s_nop 1
	v_fmac_f32_e32 v31, s1, v22
	s_add_i32 s1, s0, 34
	v_readlane_b32 s1, v4, s1
	s_nop 1
	v_fmac_f32_e32 v31, s1, v23
	s_add_i32 s1, s0, 35
	v_readlane_b32 s1, v4, s1
	s_nop 1
	v_fmac_f32_e32 v31, s1, v24
	s_add_i32 s1, s0, 36
	v_readlane_b32 s1, v4, s1
	s_nop 1
	v_fmac_f32_e32 v31, s1, v25
	s_add_i32 s1, s0, 37
	v_readlane_b32 s1, v4, s1
	s_nop 1
	v_fmac_f32_e32 v31, s1, v26
	s_add_i32 s1, s0, 38
	v_readlane_b32 s1, v4, s1
	s_nop 1
	v_fmac_f32_e32 v31, s1, v27
	s_add_i32 s1, s0, 39
	v_readlane_b32 s1, v4, s1
	s_nop 1
	v_fmac_f32_e32 v31, s1, v28
	s_add_i32 s1, s0, 40
	v_readlane_b32 s1, v4, s1
	s_add_i32 s0, s0, 41
	v_readlane_b32 s0, v4, s0
	v_fmac_f32_e32 v31, s1, v29
	s_nop 0
	v_fmac_f32_e32 v31, s0, v30
	s_mov_b32 s0, 0
	s_xor_b32 s1, s0, 32
	v_readlane_b32 s1, v5, s1
	s_nop 1
	v_fma_f32 v32, s1, v104, v115
	s_add_i32 s1, s0, 33
	v_readlane_b32 s1, v5, s1
	s_nop 1
	v_fmac_f32_e32 v32, s1, v22
	s_add_i32 s1, s0, 34
	v_readlane_b32 s1, v5, s1
	s_nop 1
	v_fmac_f32_e32 v32, s1, v23
	s_add_i32 s1, s0, 35
	v_readlane_b32 s1, v5, s1
	s_nop 1
	v_fmac_f32_e32 v32, s1, v24
	s_add_i32 s1, s0, 36
	v_readlane_b32 s1, v5, s1
	s_nop 1
	v_fmac_f32_e32 v32, s1, v25
	s_add_i32 s1, s0, 37
	v_readlane_b32 s1, v5, s1
	s_nop 1
	v_fmac_f32_e32 v32, s1, v26
	s_add_i32 s1, s0, 38
	v_readlane_b32 s1, v5, s1
	s_nop 1
	v_fmac_f32_e32 v32, s1, v27
	s_add_i32 s1, s0, 39
	v_readlane_b32 s1, v5, s1
	s_nop 1
	v_fmac_f32_e32 v32, s1, v28
	s_add_i32 s1, s0, 40
	v_readlane_b32 s1, v5, s1
	s_nop 1
	v_fmac_f32_e32 v32, s1, v29
	s_add_i32 s1, s0, 41
	v_readlane_b32 s1, v5, s1
	s_add_i32 s0, s0, 42
	v_readlane_b32 s0, v5, s0
	v_fmac_f32_e32 v32, s1, v30
	s_nop 0
	v_fmac_f32_e32 v32, s0, v31
	s_mov_b32 s0, 0
	s_add_i32 s1, s0, 48
	v_readlane_b32 s1, v2, s1
	s_nop 1
	v_fma_f32 v33, s1, v104, v116
	s_add_i32 s1, s0, 49
	v_readlane_b32 s1, v2, s1
	s_nop 1
	v_fmac_f32_e32 v33, s1, v22
	s_add_i32 s1, s0, 50
	v_readlane_b32 s1, v2, s1
	s_nop 1
	v_fmac_f32_e32 v33, s1, v23
	s_add_i32 s1, s0, 51
	v_readlane_b32 s1, v2, s1
	s_nop 1
	v_fmac_f32_e32 v33, s1, v24
	s_add_i32 s1, s0, 52
	v_readlane_b32 s1, v2, s1
	s_nop 1
	v_fmac_f32_e32 v33, s1, v25
	s_add_i32 s1, s0, 53
	v_readlane_b32 s1, v2, s1
	s_nop 1
	v_fmac_f32_e32 v33, s1, v26
	s_add_i32 s1, s0, 54
	v_readlane_b32 s1, v2, s1
	s_nop 1
	v_fmac_f32_e32 v33, s1, v27
	s_add_i32 s1, s0, 55
	v_readlane_b32 s1, v2, s1
	s_nop 1
	v_fmac_f32_e32 v33, s1, v28
	s_add_i32 s1, s0, 56
	v_readlane_b32 s1, v2, s1
	s_nop 1
	v_fmac_f32_e32 v33, s1, v29
	s_add_i32 s1, s0, 57
	v_readlane_b32 s1, v2, s1
	s_nop 1
	v_fmac_f32_e32 v33, s1, v30
	s_add_i32 s1, s0, 58
	v_readlane_b32 s1, v2, s1
	s_add_i32 s0, s0, 59
	v_readlane_b32 s0, v2, s0
	v_fmac_f32_e32 v33, s1, v31
	s_nop 0
	v_fmac_f32_e32 v33, s0, v32
	s_mov_b32 s0, 0
	s_add_i32 s1, s0, 48
	v_readlane_b32 s1, v3, s1
	s_nop 1
	v_fma_f32 v2, s1, v104, v117
	s_add_i32 s1, s0, 49
	v_readlane_b32 s1, v3, s1
	s_nop 1
	v_fmac_f32_e32 v2, s1, v22
	s_add_i32 s1, s0, 50
	v_readlane_b32 s1, v3, s1
	s_nop 1
	v_fmac_f32_e32 v2, s1, v23
	s_add_i32 s1, s0, 51
	v_readlane_b32 s1, v3, s1
	s_nop 1
	v_fmac_f32_e32 v2, s1, v24
	s_add_i32 s1, s0, 52
	v_readlane_b32 s1, v3, s1
	s_nop 1
	v_fmac_f32_e32 v2, s1, v25
	s_add_i32 s1, s0, 53
; __device__ __forceinline__ unsigned f2bf(float f) { return cvt_pk_bf16_nat(f, 0.f) & 0xffffu; }
; __global__ void __launch_bounds__(NTHR, 2) mk_fwd(Args args) {
;     ...
;                     float Tr[16]; const pg8::v4i_t PTi = __builtin_bit_cast(pg8::v4i_t, PT);
; #pragma unroll
;                     for (int t = 0; t < 16; ++t) { float acc = (t == s_) ? 1.f : 0.f;
;                         int zt_ = 0; { const float dep_ = t > 0 ? Tr[t > 0 ? t - 1 : 0] : 0.f; asm volatile("" : "+s"(zt_) : "v"(dep_)); }
; #pragma unroll
;                         for (int r = 0; r < t; ++r) acc = __builtin_fmaf(__int_as_float(__builtin_amdgcn_readlane(PTi[t & 3], 16 * (t >> 2) + r + zt_)), Tr[r], acc);
;                         Tr[t] = acc; }
;                     if (q == 0) {
; #pragma unroll
;                         for (int t = 0; t < 16; ++t) QGT[1024 + t * 32 + rec] = (bf16)f2bf(Tr[t]); }
	v_readlane_b32 s1, v3, s1
	s_nop 1
	v_fmac_f32_e32 v2, s1, v26
	s_add_i32 s1, s0, 54
	v_readlane_b32 s1, v3, s1
	s_nop 1
	v_fmac_f32_e32 v2, s1, v27
	s_add_i32 s1, s0, 55
	v_readlane_b32 s1, v3, s1
	s_nop 1
	v_fmac_f32_e32 v2, s1, v28
	s_add_i32 s1, s0, 56
	v_readlane_b32 s1, v3, s1
	s_nop 1
	v_fmac_f32_e32 v2, s1, v29
	s_add_i32 s1, s0, 57
	v_readlane_b32 s1, v3, s1
	s_nop 1
	v_fmac_f32_e32 v2, s1, v30
	s_add_i32 s1, s0, 58
	v_readlane_b32 s1, v3, s1
	s_nop 1
	v_fmac_f32_e32 v2, s1, v31
	s_add_i32 s1, s0, 59
	v_readlane_b32 s1, v3, s1
	s_add_i32 s0, s0, 60
	v_readlane_b32 s0, v3, s0
	v_fmac_f32_e32 v2, s1, v32
	s_nop 0
	v_fmac_f32_e32 v2, s0, v33
	s_mov_b32 s0, 0
	s_add_i32 s1, s0, 48
	v_readlane_b32 s1, v4, s1
	s_nop 1
	v_fma_f32 v3, s1, v104, v118
	s_add_i32 s1, s0, 49
	v_readlane_b32 s1, v4, s1
	s_nop 1
	v_fmac_f32_e32 v3, s1, v22
	s_add_i32 s1, s0, 50
	v_readlane_b32 s1, v4, s1
	s_nop 1
	v_fmac_f32_e32 v3, s1, v23
	s_add_i32 s1, s0, 51
	v_readlane_b32 s1, v4, s1
	s_nop 1
	v_fmac_f32_e32 v3, s1, v24
	s_add_i32 s1, s0, 52
	v_readlane_b32 s1, v4, s1
	s_nop 1
	v_fmac_f32_e32 v3, s1, v25
	s_add_i32 s1, s0, 53
	v_readlane_b32 s1, v4, s1
	s_nop 1
	v_fmac_f32_e32 v3, s1, v26
	s_add_i32 s1, s0, 54
	v_readlane_b32 s1, v4, s1
	s_nop 1
	v_fmac_f32_e32 v3, s1, v27
	s_add_i32 s1, s0, 55
	v_readlane_b32 s1, v4, s1
	s_nop 1
	v_fmac_f32_e32 v3, s1, v28
	s_add_i32 s1, s0, 56
	v_readlane_b32 s1, v4, s1
	s_nop 1
	v_fmac_f32_e32 v3, s1, v29
	s_add_i32 s1, s0, 57
	v_readlane_b32 s1, v4, s1
	s_nop 1
	v_fmac_f32_e32 v3, s1, v30
	s_add_i32 s1, s0, 58
	v_readlane_b32 s1, v4, s1
	s_nop 1
	v_fmac_f32_e32 v3, s1, v31
	s_add_i32 s1, s0, 59
	v_readlane_b32 s1, v4, s1
	s_nop 1
	v_fmac_f32_e32 v3, s1, v32
	s_add_i32 s1, s0, 60
	v_readlane_b32 s1, v4, s1
	s_add_i32 s0, s0, 61
	v_readlane_b32 s0, v4, s0
	v_fmac_f32_e32 v3, s1, v33
	s_nop 0
	v_fmac_f32_e32 v3, s0, v2
	s_add_i32 s0, s34, 48
	v_readlane_b32 s76, v5, s0
	s_add_i32 s0, s34, 49
	v_readlane_b32 s88, v5, s0
	s_add_i32 s0, s34, 50
	v_readlane_b32 s89, v5, s0
	s_add_i32 s0, s34, 51
	v_readlane_b32 vcc_lo, v5, s0
	s_add_i32 s0, s34, 52
	v_readlane_b32 vcc_hi, v5, s0
	s_add_i32 s0, s34, 53
	v_readlane_b32 s40, v5, s0
	s_add_i32 s0, s34, 54
	v_readlane_b32 s43, v5, s0
	s_add_i32 s0, s34, 55
	v_readlane_b32 s92, v5, s0
	s_add_i32 s0, s34, 56
	v_readlane_b32 s93, v5, s0
	s_add_i32 s0, s34, 57
	v_readlane_b32 s96, v5, s0
	s_add_i32 s0, s34, 58
	v_readlane_b32 s97, v5, s0
	s_add_i32 s0, s34, 59
	s_add_i32 s1, s34, 60
	s_add_i32 s35, s34, 61
	s_add_i32 s34, s34, 62
	v_readlane_b32 s0, v5, s0
	v_readlane_b32 s1, v5, s1
	v_readlane_b32 s64, v5, s35
	v_readlane_b32 s65, v5, s34
	s_and_saveexec_b64 s[34:35], s[2:3]
	s_cbranch_execz .Lpr_475
	v_fma_f32 v4, s76, v104, v119
	v_fmac_f32_e32 v4, s88, v22
	v_fmac_f32_e32 v4, s89, v23
	v_fmac_f32_e32 v4, vcc_lo, v24
	v_fmac_f32_e32 v4, vcc_hi, v25
	v_cvt_pk_bf16_f32 v5, v22, s0
	v_fmac_f32_e32 v4, s40, v26
	ds_write_b16 v1, v5 offset:12352
	v_cvt_pk_bf16_f32 v5, v23, s0
	v_fmac_f32_e32 v4, s43, v27
	ds_write_b16 v1, v5 offset:12416
	v_cvt_pk_bf16_f32 v5, v24, s0
	v_fmac_f32_e32 v4, s92, v28
	ds_write_b16 v1, v5 offset:12480
	v_cvt_pk_bf16_f32 v5, v25, s0
	v_fmac_f32_e32 v4, s93, v29
	ds_write_b16 v1, v5 offset:12544
	v_cvt_pk_bf16_f32 v5, v26, s0
	v_fmac_f32_e32 v4, s96, v30
	ds_write_b16 v1, v5 offset:12608
	v_cvt_pk_bf16_f32 v5, v27, s0
	v_fmac_f32_e32 v4, s97, v31
	ds_write_b16 v1, v5 offset:12672
	v_cvt_pk_bf16_f32 v5, v28, s0
	v_fmac_f32_e32 v4, s0, v32
	ds_write_b16 v1, v5 offset:12736
	v_cvt_pk_bf16_f32 v5, v29, s0
	v_fmac_f32_e32 v4, s1, v33
	ds_write_b16 v1, v5 offset:12800
	v_cvt_pk_bf16_f32 v5, v30, s0
	v_fmac_f32_e32 v4, s64, v2
	ds_write_b16 v1, v5 offset:12864
	v_cvt_pk_bf16_f32 v5, v31, s0
	v_cvt_pk_bf16_f32 v2, v2, s0
	v_fmac_f32_e32 v4, s65, v3
	ds_write_b16 v1, v5 offset:12928
	v_cvt_pk_bf16_f32 v5, v32, s0
	ds_write_b16 v1, v2 offset:13120
	v_cvt_pk_bf16_f32 v2, v3, s0
	ds_write_b16 v1, v5 offset:12992
	v_cvt_pk_bf16_f32 v5, v33, s0
	ds_write_b16 v1, v2 offset:13184
	v_cvt_pk_bf16_f32 v2, v4, s0
	ds_write_b16 v1, v120 offset:12288
	ds_write_b16 v1, v5 offset:13056
	ds_write_b16 v1, v2 offset:13248
	s_branch .Lpr_475
.Lpr_480:
	v_lshlrev_b32_e32 v195, 2, v0
	v_readlane_b32 s88, v252, 44
	v_readlane_b32 s78, v252, 50
	v_readlane_b32 s2, v252, 52
	v_readlane_b32 s89, v252, 45
	v_readlane_b32 s79, v252, 51
	v_readlane_b32 s3, v252, 53
	s_branch .Lprod_exit

; __global__ void __launch_bounds__(NTHR, 2) mk_fwd(Args args) {
	.amdhsa_kernel _Z6mk_fwd4Args
		.amdhsa_group_segment_fixed_size 0
		.amdhsa_private_segment_fixed_size 0
		.amdhsa_kernarg_size 496
		.amdhsa_user_sgpr_count 2
		.amdhsa_user_sgpr_dispatch_ptr 0
		.amdhsa_user_sgpr_queue_ptr 0
		.amdhsa_user_sgpr_kernarg_segment_ptr 1
		.amdhsa_user_sgpr_dispatch_id 0
		.amdhsa_user_sgpr_kernarg_preload_length 0
		.amdhsa_user_sgpr_kernarg_preload_offset 0
		.amdhsa_user_sgpr_private_segment_size 0
		.amdhsa_uses_dynamic_stack 0
		.amdhsa_enable_private_segment 0
		.amdhsa_system_sgpr_workgroup_id_x 1
		.amdhsa_system_sgpr_workgroup_id_y 0
		.amdhsa_system_sgpr_workgroup_id_z 0
		.amdhsa_system_sgpr_workgroup_info 0
		.amdhsa_system_vgpr_workitem_id 0
		.amdhsa_next_free_vgpr 256
		.amdhsa_next_free_sgpr 102
		.amdhsa_accum_offset 256
		.amdhsa_reserve_vcc 1
		.amdhsa_float_round_mode_32 0
		.amdhsa_float_round_mode_16_64 0
		.amdhsa_float_denorm_mode_32 3
		.amdhsa_float_denorm_mode_16_64 3
		.amdhsa_dx10_clamp 1
		.amdhsa_ieee_mode 1
		.amdhsa_fp16_overflow 0
		.amdhsa_tg_split 0
		.amdhsa_exception_fp_ieee_invalid_op 0
		.amdhsa_exception_fp_denorm_src 0
		.amdhsa_exception_fp_ieee_div_zero 0
		.amdhsa_exception_fp_ieee_overflow 0
		.amdhsa_exception_fp_ieee_underflow 0
		.amdhsa_exception_fp_ieee_inexact 0
		.amdhsa_exception_int_div_zero 0
	.end_amdhsa_kernel

; __global__ void __launch_bounds__(NTHR, 2) mk_fwd(Args args) {
.Lfunc_end0:
	.size	_Z6mk_fwd4Args, .Lfunc_end0-_Z6mk_fwd4Args
	.set _Z6mk_fwd4Args.num_vgpr, 256
	.set _Z6mk_fwd4Args.num_agpr, 0
	.set _Z6mk_fwd4Args.numbered_sgpr, 102
	.set _Z6mk_fwd4Args.num_named_barrier, 0
	.set _Z6mk_fwd4Args.private_seg_size, 0
	.set _Z6mk_fwd4Args.uses_vcc, 1
	.set _Z6mk_fwd4Args.uses_flat_scratch, 0
	.set _Z6mk_fwd4Args.has_dyn_sized_stack, 0
	.set _Z6mk_fwd4Args.has_recursion, 0
	.set _Z6mk_fwd4Args.has_indirect_call, 0

; __global__ void __launch_bounds__(NTHR, 2) mk_fwd(Args args) {
amdhsa.kernels:
  - .agpr_count:     0
    .args:
      - .offset:         0
        .size:           240
        .value_kind:     by_value
      - .offset:         240
        .size:           4
        .value_kind:     hidden_block_count_x
      - .offset:         244
        .size:           4
        .value_kind:     hidden_block_count_y
      - .offset:         248
        .size:           4
        .value_kind:     hidden_block_count_z
      - .offset:         252
        .size:           2
        .value_kind:     hidden_group_size_x
      - .offset:         254
        .size:           2
        .value_kind:     hidden_group_size_y
      - .offset:         256
        .size:           2
        .value_kind:     hidden_group_size_z
      - .offset:         258
        .size:           2
        .value_kind:     hidden_remainder_x
      - .offset:         260
        .size:           2
        .value_kind:     hidden_remainder_y
      - .offset:         262
        .size:           2
        .value_kind:     hidden_remainder_z
      - .offset:         280
        .size:           8
        .value_kind:     hidden_global_offset_x
      - .offset:         288
        .size:           8
        .value_kind:     hidden_global_offset_y
      - .offset:         296
        .size:           8
        .value_kind:     hidden_global_offset_z
      - .offset:         304
        .size:           2
        .value_kind:     hidden_grid_dims
      - .offset:         360
        .size:           4
        .value_kind:     hidden_dynamic_lds_size
    .group_segment_fixed_size: 0
    .kernarg_segment_align: 8
    .kernarg_segment_size: 496
    .language:       OpenCL C
    .language_version:
      - 2
      - 0
    .max_flat_workgroup_size: 512
    .name:           _Z6mk_fwd4Args
    .private_segment_fixed_size: 0
    .sgpr_count:     108
    .sgpr_spill_count: 54
    .symbol:         _Z6mk_fwd4Args.kd
    .uniform_work_group_size: 1
    .uses_dynamic_stack: false
    .vgpr_count:     256
    .vgpr_spill_count: 0
    .wavefront_size: 64
